# residual-epilogue (P2/P12/P14) and P11 output stores write-through (sc1) so the following seams' L2 write-back is short
# baseline (speedup 1.0000x reference)
; __device__ __forceinline__ unsigned cvt_pk_bf16(float lo, float hi) { unsigned r; asm volatile("v_cvt_pk_bf16_f32 %0, %1, %2" : "=v"(r) : "v"(lo), "v"(hi)); return r; }
;     __device__ __forceinline__ void operator()(AccRef acc, const Unit& u, int wr, int wc, int, int) const {
;     ...
;                     const size_t p = (size_t)row * D + col0 + bj * 128;
;                     f32x4 x0, x1;
;                     if (xin32) { x0 = *(const f32x4*)(xin32 + p); x1 = *(const f32x4*)(xin32 + p + 4); }
;                     else { const v4u h = *(const v4u*)(xb + p), lo = *(const v4u*)(xl + p);
;                         x0 = (f32x4){bflo(h.x) + bflo(lo.x), bfhi(h.x) + bfhi(lo.x), bflo(h.y) + bflo(lo.y), bfhi(h.y) + bfhi(lo.y)};
;                         x1 = (f32x4){bflo(h.z) + bflo(lo.z), bfhi(h.z) + bfhi(lo.z), bflo(h.w) + bflo(lo.w), bfhi(h.w) + bfhi(lo.w)}; }
;                     x0 = x0 + alpha * acc[ai][bj][m][0]; x1 = x1 + alpha * acc[ai][bj][m][1];
;                     if (PROBE_ON) { x0 = x0 * pscale; x1 = x1 * pscale; if (p == 0) x0[0] += pspike; }
;                     if (xout32) { *(f32x4*)(xout32 + p) = x0; *(f32x4*)(xout32 + p + 4) = x1; }
;                     else {
;                         v4u w; w.x = cvt_pk_bf16(x0[0], x0[1]); w.y = cvt_pk_bf16(x0[2], x0[3]); w.z = cvt_pk_bf16(x1[0], x1[1]); w.w = cvt_pk_bf16(x1[2], x1[3]);
;                         *(v4u*)(xb + p) = w;
;                         const f32x4 r0 = {x0[0] - bflo(w.x), x0[1] - bfhi(w.x), x0[2] - bflo(w.y), x0[3] - bfhi(w.y)}, r1 = {x1[0] - bflo(w.z), x1[1] - bfhi(w.z), x1[2] - bflo(w.w), x1[3] - bfhi(w.w)};
;                         v4u q; q.x = cvt_pk_bf16(r0[0], r0[1]); q.y = cvt_pk_bf16(r0[2], r0[3]); q.z = cvt_pk_bf16(r1[0], r1[1]); q.w = cvt_pk_bf16(r1[2], r1[3]);
;                         *(v4u*)(xl + p) = q;
.LBB0_209:
	s_waitcnt vmcnt(0)
	v_pk_fma_f32 v[132:133], v[128:129], 0.5, v[132:133] op_sel_hi:[1,0,1]
	v_pk_fma_f32 v[158:159], v[126:127], 0.5, v[130:131] op_sel_hi:[1,0,1]
	v_pk_fma_f32 v[130:131], v[124:125], 0.5, v[136:137] op_sel_hi:[1,0,1]
	v_pk_fma_f32 v[134:135], v[122:123], 0.5, v[134:135] op_sel_hi:[1,0,1]
	v_cvt_pk_bf16_f32 v122, v158, v159
	v_cvt_pk_bf16_f32 v123, v132, v133
	s_and_b64 vcc, exec, s[6:7]
	v_cvt_pk_bf16_f32 v124, v134, v135
	v_cvt_pk_bf16_f32 v125, v130, v131
	global_store_dwordx4 v[154:155], v[122:125], off sc1
	v_lshlrev_b32_e32 v126, 16, v122
	v_lshlrev_b32_e32 v127, 16, v123
	v_and_b32_e32 v122, 0xffff0000, v122
	v_and_b32_e32 v123, 0xffff0000, v123
	v_lshlrev_b32_e32 v128, 16, v124
	v_and_b32_e32 v124, 0xffff0000, v124
	v_lshlrev_b32_e32 v129, 16, v125
	v_and_b32_e32 v125, 0xffff0000, v125
	v_sub_f32_e32 v122, v159, v122
	v_sub_f32_e32 v123, v133, v123
	v_sub_f32_e32 v124, v135, v124
	v_sub_f32_e32 v125, v131, v125
	v_sub_f32_e32 v126, v158, v126
	v_sub_f32_e32 v127, v132, v127
	v_sub_f32_e32 v128, v134, v128
	v_sub_f32_e32 v129, v130, v129
	v_cvt_pk_bf16_f32 v122, v126, v122
	v_cvt_pk_bf16_f32 v123, v127, v123
	v_cvt_pk_bf16_f32 v124, v128, v124
	v_cvt_pk_bf16_f32 v125, v129, v125
	global_store_dwordx4 v[152:153], v[122:125], off sc1
	s_cbranch_vccnz .LBB0_216
	global_load_dwordx4 v[126:129], v[156:157], off offset:528
	global_load_dwordx4 v[122:125], v[156:157], off offset:512
	s_cbranch_execnz .LBB0_212

; __device__ __forceinline__ unsigned cvt_pk_bf16(float lo, float hi) { unsigned r; asm volatile("v_cvt_pk_bf16_f32 %0, %1, %2" : "=v"(r) : "v"(lo), "v"(hi)); return r; }
; __device__ __forceinline__ float shx(float v, int o, int lane) { return __builtin_bit_cast(float, __builtin_amdgcn_ds_bpermute((lane ^ o) << 2, __builtin_bit_cast(int, v))); }
;     __device__ __forceinline__ void operator()(AccRef acc, const Unit& u, int wr, int wc, int, int) const {
;     ...
;                     x0 = x0 + alpha * acc[ai][bj][m][0]; x1 = x1 + alpha * acc[ai][bj][m][1];
;                     if (PROBE_ON) { x0 = x0 * pscale; x1 = x1 * pscale; if (p == 0) x0[0] += pspike; }
;                     if (xout32) { *(f32x4*)(xout32 + p) = x0; *(f32x4*)(xout32 + p + 4) = x1; }
;                     else {
;                         v4u w; w.x = cvt_pk_bf16(x0[0], x0[1]); w.y = cvt_pk_bf16(x0[2], x0[3]); w.z = cvt_pk_bf16(x1[0], x1[1]); w.w = cvt_pk_bf16(x1[2], x1[3]);
;                         *(v4u*)(xb + p) = w;
;                         const f32x4 r0 = {x0[0] - bflo(w.x), x0[1] - bfhi(w.x), x0[2] - bflo(w.y), x0[3] - bfhi(w.y)}, r1 = {x1[0] - bflo(w.z), x1[1] - bfhi(w.z), x1[2] - bflo(w.w), x1[3] - bfhi(w.w)};
;                         v4u q; q.x = cvt_pk_bf16(r0[0], r0[1]); q.y = cvt_pk_bf16(r0[2], r0[3]); q.z = cvt_pk_bf16(r1[0], r1[1]); q.w = cvt_pk_bf16(r1[2], r1[3]);
;                         *(v4u*)(xl + p) = q;
;                     }
;                     s += (x0[0] * x0[0] + x0[1] * x0[1]) + (x0[2] * x0[2] + x0[3] * x0[3]) + (x1[0] * x1[0] + x1[1] * x1[1]) + (x1[2] * x1[2] + x1[3] * x1[3]);
;                 }
;                 s += shx(s, 16, ln_); s += shx(s, 32, ln_);
;                 if (fq == 0) ss[(size_t)row * 32 + u.pn * 4 + wc] = s;
.LBB0_212:
	s_waitcnt vmcnt(0)
	v_pk_fma_f32 v[120:121], v[120:121], 0.5, v[124:125] op_sel_hi:[1,0,1]
	v_pk_fma_f32 v[118:119], v[118:119], 0.5, v[122:123] op_sel_hi:[1,0,1]
	v_pk_fma_f32 v[124:125], v[114:115], 0.5, v[126:127] op_sel_hi:[1,0,1]
	v_cvt_pk_bf16_f32 v114, v118, v119
	v_cvt_pk_bf16_f32 v115, v120, v121
	v_pk_fma_f32 v[122:123], v[116:117], 0.5, v[128:129] op_sel_hi:[1,0,1]
	v_cvt_pk_bf16_f32 v116, v124, v125
	v_lshlrev_b32_e32 v127, 16, v115
	v_cvt_pk_bf16_f32 v117, v122, v123
	global_store_dwordx4 v[154:155], v[114:117], off offset:256 sc1
	v_lshlrev_b32_e32 v126, 16, v114
	v_sub_f32_e32 v126, v118, v126
	v_and_b32_e32 v115, 0xffff0000, v115
	v_sub_f32_e32 v128, v121, v115
	v_lshlrev_b32_e32 v115, 16, v116
	v_sub_f32_e32 v129, v124, v115
	v_and_b32_e32 v115, 0xffff0000, v116
	v_mul_f32_e32 v116, v118, v118
	v_mul_f32_e32 v118, v120, v120
	v_fmac_f32_e32 v116, v119, v119
	v_fmac_f32_e32 v118, v121, v121
	v_mul_f32_e32 v136, v158, v158
	v_mul_f32_e32 v132, v132, v132
	v_add_f32_e32 v116, v118, v116
	v_mul_f32_e32 v118, v124, v124
	v_fmac_f32_e32 v136, v159, v159
	v_fmac_f32_e32 v132, v133, v133
	v_mul_f32_e32 v133, v134, v134
	v_fmac_f32_e32 v118, v125, v125
	v_add_f32_e32 v132, v132, v136
	v_fmac_f32_e32 v133, v135, v135
	v_mul_f32_e32 v131, v131, v131
	v_add_f32_e32 v116, v118, v116
	v_mul_f32_e32 v118, v123, v123
	v_add_f32_e32 v132, v133, v132
	v_fmac_f32_e32 v131, v130, v130
	v_fmac_f32_e32 v118, v122, v122
	v_add_f32_e32 v130, v131, v132
	v_lshlrev_b32_e32 v131, 2, v162
	v_add_f32_e32 v116, v118, v116
	v_xor_b32_e32 v133, 64, v131
	v_and_b32_e32 v114, 0xffff0000, v114
	v_add_f32_e32 v118, v130, v116
	v_sub_f32_e32 v114, v119, v114
	ds_bpermute_b32 v119, v133, v118
	v_xor_b32_e32 v132, 0x80, v131
	v_sub_f32_e32 v131, v125, v115
	v_lshlrev_b32_e32 v115, 16, v117
	v_sub_f32_e32 v127, v120, v127
	v_sub_f32_e32 v120, v122, v115
	v_and_b32_e32 v115, 0xffff0000, v117
	v_cvt_pk_bf16_f32 v116, v126, v114
	s_waitcnt lgkmcnt(0)
	v_add_f32_e32 v114, v118, v119
	v_sub_f32_e32 v121, v123, v115
	ds_bpermute_b32 v115, v132, v114
	s_lshl_b32 s26, s2, 2
	v_cmp_gt_u32_e64 s[8:9], 16, v162
	s_ashr_i32 s27, s26, 31
	v_cvt_pk_bf16_f32 v117, v127, v128
	v_cvt_pk_bf16_f32 v118, v129, v131
	v_cvt_pk_bf16_f32 v119, v120, v121
	global_store_dwordx4 v[152:153], v[116:119], off offset:256 sc1
	s_and_saveexec_b64 s[28:29], s[8:9]
	s_cbranch_execz .LBB0_214
	v_lshlrev_b64 v[116:117], 7, v[150:151]
	v_lshl_add_u64 v[116:117], s[16:17], 0, v[116:117]
	v_lshl_add_u64 v[116:117], s[26:27], 2, v[116:117]
	s_lshl_b32 s96, s43, 2
	v_lshl_add_u64 v[116:117], v[116:117], 0, s[96:97]
	s_waitcnt lgkmcnt(0)
	v_add_f32_e32 v114, v114, v115
	global_store_dword v[116:117], v114, off

; __device__ __forceinline__ unsigned cvt_pk_bf16(float lo, float hi) { unsigned r; asm volatile("v_cvt_pk_bf16_f32 %0, %1, %2" : "=v"(r) : "v"(lo), "v"(hi)); return r; }
;     __device__ __forceinline__ void operator()(AccRef acc, const Unit& u, int wr, int wc, int, int) const {
;     ...
;                     const size_t p = (size_t)row * D + col0 + bj * 128;
;                     f32x4 x0, x1;
;                     if (xin32) { x0 = *(const f32x4*)(xin32 + p); x1 = *(const f32x4*)(xin32 + p + 4); }
;                     else { const v4u h = *(const v4u*)(xb + p), lo = *(const v4u*)(xl + p);
;                         x0 = (f32x4){bflo(h.x) + bflo(lo.x), bfhi(h.x) + bfhi(lo.x), bflo(h.y) + bflo(lo.y), bfhi(h.y) + bfhi(lo.y)};
;                         x1 = (f32x4){bflo(h.z) + bflo(lo.z), bfhi(h.z) + bfhi(lo.z), bflo(h.w) + bflo(lo.w), bfhi(h.w) + bfhi(lo.w)}; }
;                     x0 = x0 + alpha * acc[ai][bj][m][0]; x1 = x1 + alpha * acc[ai][bj][m][1];
;                     if (PROBE_ON) { x0 = x0 * pscale; x1 = x1 * pscale; if (p == 0) x0[0] += pspike; }
;                     if (xout32) { *(f32x4*)(xout32 + p) = x0; *(f32x4*)(xout32 + p + 4) = x1; }
;                     else {
;                         v4u w; w.x = cvt_pk_bf16(x0[0], x0[1]); w.y = cvt_pk_bf16(x0[2], x0[3]); w.z = cvt_pk_bf16(x1[0], x1[1]); w.w = cvt_pk_bf16(x1[2], x1[3]);
;                         *(v4u*)(xb + p) = w;
;                         const f32x4 r0 = {x0[0] - bflo(w.x), x0[1] - bfhi(w.x), x0[2] - bflo(w.y), x0[3] - bfhi(w.y)}, r1 = {x1[0] - bflo(w.z), x1[1] - bfhi(w.z), x1[2] - bflo(w.w), x1[3] - bfhi(w.w)};
;                         v4u q; q.x = cvt_pk_bf16(r0[0], r0[1]); q.y = cvt_pk_bf16(r0[2], r0[3]); q.z = cvt_pk_bf16(r1[0], r1[1]); q.w = cvt_pk_bf16(r1[2], r1[3]);
;                         *(v4u*)(xl + p) = q;
.LBB0_220:
	s_waitcnt vmcnt(0)
	v_pk_fma_f32 v[116:117], v[112:113], 0.5, v[116:117] op_sel_hi:[1,0,1]
	v_pk_fma_f32 v[130:131], v[110:111], 0.5, v[114:115] op_sel_hi:[1,0,1]
	v_pk_fma_f32 v[114:115], v[108:109], 0.5, v[120:121] op_sel_hi:[1,0,1]
	v_pk_fma_f32 v[118:119], v[106:107], 0.5, v[118:119] op_sel_hi:[1,0,1]
	v_cvt_pk_bf16_f32 v106, v130, v131
	v_cvt_pk_bf16_f32 v107, v116, v117
	s_and_b64 vcc, exec, s[6:7]
	v_cvt_pk_bf16_f32 v108, v118, v119
	v_cvt_pk_bf16_f32 v109, v114, v115
	global_store_dwordx4 v[126:127], v[106:109], off sc1
	v_lshlrev_b32_e32 v110, 16, v106
	v_lshlrev_b32_e32 v111, 16, v107
	v_and_b32_e32 v106, 0xffff0000, v106
	v_and_b32_e32 v107, 0xffff0000, v107
	v_lshlrev_b32_e32 v112, 16, v108
	v_and_b32_e32 v108, 0xffff0000, v108
	v_lshlrev_b32_e32 v113, 16, v109
	v_and_b32_e32 v109, 0xffff0000, v109
	v_sub_f32_e32 v106, v131, v106
	v_sub_f32_e32 v107, v117, v107
	v_sub_f32_e32 v108, v119, v108
	v_sub_f32_e32 v109, v115, v109
	v_sub_f32_e32 v110, v130, v110
	v_sub_f32_e32 v111, v116, v111
	v_sub_f32_e32 v112, v118, v112
	v_sub_f32_e32 v113, v114, v113
	v_cvt_pk_bf16_f32 v106, v110, v106
	v_cvt_pk_bf16_f32 v107, v111, v107
	v_cvt_pk_bf16_f32 v108, v112, v108
	v_cvt_pk_bf16_f32 v109, v113, v109
	global_store_dwordx4 v[124:125], v[106:109], off sc1
	s_cbranch_vccnz .LBB0_227
	global_load_dwordx4 v[110:113], v[128:129], off offset:528
	global_load_dwordx4 v[106:109], v[128:129], off offset:512
	s_cbranch_execnz .LBB0_223

; __device__ __forceinline__ unsigned cvt_pk_bf16(float lo, float hi) { unsigned r; asm volatile("v_cvt_pk_bf16_f32 %0, %1, %2" : "=v"(r) : "v"(lo), "v"(hi)); return r; }
; __device__ __forceinline__ float shx(float v, int o, int lane) { return __builtin_bit_cast(float, __builtin_amdgcn_ds_bpermute((lane ^ o) << 2, __builtin_bit_cast(int, v))); }
;     __device__ __forceinline__ void operator()(AccRef acc, const Unit& u, int wr, int wc, int, int) const {
;     ...
;                     x0 = x0 + alpha * acc[ai][bj][m][0]; x1 = x1 + alpha * acc[ai][bj][m][1];
;                     if (PROBE_ON) { x0 = x0 * pscale; x1 = x1 * pscale; if (p == 0) x0[0] += pspike; }
;                     if (xout32) { *(f32x4*)(xout32 + p) = x0; *(f32x4*)(xout32 + p + 4) = x1; }
;                     else {
;                         v4u w; w.x = cvt_pk_bf16(x0[0], x0[1]); w.y = cvt_pk_bf16(x0[2], x0[3]); w.z = cvt_pk_bf16(x1[0], x1[1]); w.w = cvt_pk_bf16(x1[2], x1[3]);
;                         *(v4u*)(xb + p) = w;
;                         const f32x4 r0 = {x0[0] - bflo(w.x), x0[1] - bfhi(w.x), x0[2] - bflo(w.y), x0[3] - bfhi(w.y)}, r1 = {x1[0] - bflo(w.z), x1[1] - bfhi(w.z), x1[2] - bflo(w.w), x1[3] - bfhi(w.w)};
;                         v4u q; q.x = cvt_pk_bf16(r0[0], r0[1]); q.y = cvt_pk_bf16(r0[2], r0[3]); q.z = cvt_pk_bf16(r1[0], r1[1]); q.w = cvt_pk_bf16(r1[2], r1[3]);
;                         *(v4u*)(xl + p) = q;
;                     }
;                     s += (x0[0] * x0[0] + x0[1] * x0[1]) + (x0[2] * x0[2] + x0[3] * x0[3]) + (x1[0] * x1[0] + x1[1] * x1[1]) + (x1[2] * x1[2] + x1[3] * x1[3]);
;                 }
;                 s += shx(s, 16, ln_); s += shx(s, 32, ln_);
;                 if (fq == 0) ss[(size_t)row * 32 + u.pn * 4 + wc] = s;
.LBB0_223:
	s_waitcnt vmcnt(0)
	v_pk_fma_f32 v[104:105], v[104:105], 0.5, v[108:109] op_sel_hi:[1,0,1]
	v_pk_fma_f32 v[102:103], v[102:103], 0.5, v[106:107] op_sel_hi:[1,0,1]
	v_pk_fma_f32 v[108:109], v[98:99], 0.5, v[110:111] op_sel_hi:[1,0,1]
	v_cvt_pk_bf16_f32 v98, v102, v103
	v_cvt_pk_bf16_f32 v99, v104, v105
	v_pk_fma_f32 v[106:107], v[100:101], 0.5, v[112:113] op_sel_hi:[1,0,1]
	v_cvt_pk_bf16_f32 v100, v108, v109
	v_lshlrev_b32_e32 v111, 16, v99
	v_cvt_pk_bf16_f32 v101, v106, v107
	global_store_dwordx4 v[126:127], v[98:101], off offset:256 sc1
	v_lshlrev_b32_e32 v110, 16, v98
	v_sub_f32_e32 v110, v102, v110
	v_and_b32_e32 v99, 0xffff0000, v99
	v_sub_f32_e32 v112, v105, v99
	v_lshlrev_b32_e32 v99, 16, v100
	v_sub_f32_e32 v113, v108, v99
	v_and_b32_e32 v99, 0xffff0000, v100
	v_mul_f32_e32 v100, v102, v102
	v_mul_f32_e32 v102, v104, v104
	v_fmac_f32_e32 v100, v103, v103
	v_fmac_f32_e32 v102, v105, v105
	v_mul_f32_e32 v120, v130, v130
	v_mul_f32_e32 v116, v116, v116
	v_add_f32_e32 v100, v102, v100
	v_mul_f32_e32 v102, v108, v108
	v_fmac_f32_e32 v120, v131, v131
	v_fmac_f32_e32 v116, v117, v117
	v_mul_f32_e32 v117, v118, v118
	v_fmac_f32_e32 v102, v109, v109
	v_add_f32_e32 v116, v116, v120
	v_fmac_f32_e32 v117, v119, v119
	v_mul_f32_e32 v115, v115, v115
	v_add_f32_e32 v100, v102, v100
	v_mul_f32_e32 v102, v107, v107
	v_add_f32_e32 v116, v117, v116
	v_fmac_f32_e32 v115, v114, v114
	v_fmac_f32_e32 v102, v106, v106
	v_add_f32_e32 v114, v115, v116
	v_add_f32_e32 v100, v102, v100
	v_and_b32_e32 v98, 0xffff0000, v98
	v_add_f32_e32 v102, v114, v100
	v_sub_f32_e32 v98, v103, v98
	ds_bpermute_b32 v103, v133, v102
	v_sub_f32_e32 v115, v109, v99
	v_lshlrev_b32_e32 v99, 16, v101
	v_sub_f32_e32 v111, v104, v111
	v_sub_f32_e32 v104, v106, v99
	v_and_b32_e32 v99, 0xffff0000, v101
	v_cvt_pk_bf16_f32 v100, v110, v98
	s_waitcnt lgkmcnt(0)
	v_add_f32_e32 v98, v102, v103
	v_sub_f32_e32 v105, v107, v99
	ds_bpermute_b32 v99, v132, v98
	v_cvt_pk_bf16_f32 v101, v111, v112
	v_cvt_pk_bf16_f32 v102, v113, v115
	v_cvt_pk_bf16_f32 v103, v104, v105
	global_store_dwordx4 v[124:125], v[100:103], off offset:256 sc1
	s_and_saveexec_b64 s[28:29], s[8:9]
	s_cbranch_execz .LBB0_225
	v_lshlrev_b64 v[100:101], 7, v[122:123]
	v_lshl_add_u64 v[100:101], s[16:17], 0, v[100:101]
	v_lshl_add_u64 v[100:101], s[26:27], 2, v[100:101]
	s_lshl_b32 s96, s43, 2
	v_lshl_add_u64 v[100:101], v[100:101], 0, s[96:97]
	s_waitcnt lgkmcnt(0)
	v_add_f32_e32 v98, v98, v99
	global_store_dword v[100:101], v98, off

; __device__ __forceinline__ unsigned cvt_pk_bf16(float lo, float hi) { unsigned r; asm volatile("v_cvt_pk_bf16_f32 %0, %1, %2" : "=v"(r) : "v"(lo), "v"(hi)); return r; }
;     __device__ __forceinline__ void operator()(AccRef acc, const Unit& u, int wr, int wc, int, int) const {
;     ...
;                     if (xin32) { x0 = *(const f32x4*)(xin32 + p); x1 = *(const f32x4*)(xin32 + p + 4); }
;                     else { const v4u h = *(const v4u*)(xb + p), lo = *(const v4u*)(xl + p);
;                         x0 = (f32x4){bflo(h.x) + bflo(lo.x), bfhi(h.x) + bfhi(lo.x), bflo(h.y) + bflo(lo.y), bfhi(h.y) + bfhi(lo.y)};
;                         x1 = (f32x4){bflo(h.z) + bflo(lo.z), bfhi(h.z) + bfhi(lo.z), bflo(h.w) + bflo(lo.w), bfhi(h.w) + bfhi(lo.w)}; }
;                     x0 = x0 + alpha * acc[ai][bj][m][0]; x1 = x1 + alpha * acc[ai][bj][m][1];
;                     if (PROBE_ON) { x0 = x0 * pscale; x1 = x1 * pscale; if (p == 0) x0[0] += pspike; }
;                     if (xout32) { *(f32x4*)(xout32 + p) = x0; *(f32x4*)(xout32 + p + 4) = x1; }
;                     else {
;                         v4u w; w.x = cvt_pk_bf16(x0[0], x0[1]); w.y = cvt_pk_bf16(x0[2], x0[3]); w.z = cvt_pk_bf16(x1[0], x1[1]); w.w = cvt_pk_bf16(x1[2], x1[3]);
;                         *(v4u*)(xb + p) = w;
;                         const f32x4 r0 = {x0[0] - bflo(w.x), x0[1] - bfhi(w.x), x0[2] - bflo(w.y), x0[3] - bfhi(w.y)}, r1 = {x1[0] - bflo(w.z), x1[1] - bfhi(w.z), x1[2] - bflo(w.w), x1[3] - bfhi(w.w)};
;                         v4u q; q.x = cvt_pk_bf16(r0[0], r0[1]); q.y = cvt_pk_bf16(r0[2], r0[3]); q.z = cvt_pk_bf16(r1[0], r1[1]); q.w = cvt_pk_bf16(r1[2], r1[3]);
;                         *(v4u*)(xl + p) = q;
.LBB0_231:
	s_waitcnt vmcnt(0)
	v_pk_fma_f32 v[100:101], v[96:97], 0.5, v[100:101] op_sel_hi:[1,0,1]
	v_pk_fma_f32 v[114:115], v[94:95], 0.5, v[98:99] op_sel_hi:[1,0,1]
	v_pk_fma_f32 v[98:99], v[92:93], 0.5, v[104:105] op_sel_hi:[1,0,1]
	v_pk_fma_f32 v[102:103], v[90:91], 0.5, v[102:103] op_sel_hi:[1,0,1]
	v_cvt_pk_bf16_f32 v90, v114, v115
	v_cvt_pk_bf16_f32 v91, v100, v101
	s_and_b64 vcc, exec, s[6:7]
	v_cvt_pk_bf16_f32 v92, v102, v103
	v_cvt_pk_bf16_f32 v93, v98, v99
	global_store_dwordx4 v[110:111], v[90:93], off sc1
	v_lshlrev_b32_e32 v94, 16, v90
	v_lshlrev_b32_e32 v95, 16, v91
	v_and_b32_e32 v90, 0xffff0000, v90
	v_and_b32_e32 v91, 0xffff0000, v91
	v_lshlrev_b32_e32 v96, 16, v92
	v_and_b32_e32 v92, 0xffff0000, v92
	v_lshlrev_b32_e32 v97, 16, v93
	v_and_b32_e32 v93, 0xffff0000, v93
	v_sub_f32_e32 v90, v115, v90
	v_sub_f32_e32 v91, v101, v91
	v_sub_f32_e32 v92, v103, v92
	v_sub_f32_e32 v93, v99, v93
	v_sub_f32_e32 v94, v114, v94
	v_sub_f32_e32 v95, v100, v95
	v_sub_f32_e32 v96, v102, v96
	v_sub_f32_e32 v97, v98, v97
	v_cvt_pk_bf16_f32 v90, v94, v90
	v_cvt_pk_bf16_f32 v91, v95, v91
	v_cvt_pk_bf16_f32 v92, v96, v92
	v_cvt_pk_bf16_f32 v93, v97, v93
	global_store_dwordx4 v[108:109], v[90:93], off sc1
	s_cbranch_vccnz .LBB0_238
	global_load_dwordx4 v[94:97], v[112:113], off offset:528
	global_load_dwordx4 v[90:93], v[112:113], off offset:512
	s_cbranch_execnz .LBB0_234

; __device__ __forceinline__ unsigned cvt_pk_bf16(float lo, float hi) { unsigned r; asm volatile("v_cvt_pk_bf16_f32 %0, %1, %2" : "=v"(r) : "v"(lo), "v"(hi)); return r; }
; __device__ __forceinline__ float shx(float v, int o, int lane) { return __builtin_bit_cast(float, __builtin_amdgcn_ds_bpermute((lane ^ o) << 2, __builtin_bit_cast(int, v))); }
;     __device__ __forceinline__ void operator()(AccRef acc, const Unit& u, int wr, int wc, int, int) const {
;     ...
;                     if (xin32) { x0 = *(const f32x4*)(xin32 + p); x1 = *(const f32x4*)(xin32 + p + 4); }
;                     else { const v4u h = *(const v4u*)(xb + p), lo = *(const v4u*)(xl + p);
;                         x0 = (f32x4){bflo(h.x) + bflo(lo.x), bfhi(h.x) + bfhi(lo.x), bflo(h.y) + bflo(lo.y), bfhi(h.y) + bfhi(lo.y)};
;                         x1 = (f32x4){bflo(h.z) + bflo(lo.z), bfhi(h.z) + bfhi(lo.z), bflo(h.w) + bflo(lo.w), bfhi(h.w) + bfhi(lo.w)}; }
;                     x0 = x0 + alpha * acc[ai][bj][m][0]; x1 = x1 + alpha * acc[ai][bj][m][1];
;                     if (PROBE_ON) { x0 = x0 * pscale; x1 = x1 * pscale; if (p == 0) x0[0] += pspike; }
;                     if (xout32) { *(f32x4*)(xout32 + p) = x0; *(f32x4*)(xout32 + p + 4) = x1; }
;                     else {
;                         v4u w; w.x = cvt_pk_bf16(x0[0], x0[1]); w.y = cvt_pk_bf16(x0[2], x0[3]); w.z = cvt_pk_bf16(x1[0], x1[1]); w.w = cvt_pk_bf16(x1[2], x1[3]);
;                         *(v4u*)(xb + p) = w;
;                         const f32x4 r0 = {x0[0] - bflo(w.x), x0[1] - bfhi(w.x), x0[2] - bflo(w.y), x0[3] - bfhi(w.y)}, r1 = {x1[0] - bflo(w.z), x1[1] - bfhi(w.z), x1[2] - bflo(w.w), x1[3] - bfhi(w.w)};
;                         v4u q; q.x = cvt_pk_bf16(r0[0], r0[1]); q.y = cvt_pk_bf16(r0[2], r0[3]); q.z = cvt_pk_bf16(r1[0], r1[1]); q.w = cvt_pk_bf16(r1[2], r1[3]);
;                         *(v4u*)(xl + p) = q;
;                     }
;                     s += (x0[0] * x0[0] + x0[1] * x0[1]) + (x0[2] * x0[2] + x0[3] * x0[3]) + (x1[0] * x1[0] + x1[1] * x1[1]) + (x1[2] * x1[2] + x1[3] * x1[3]);
;                 }
;                 s += shx(s, 16, ln_); s += shx(s, 32, ln_);
;                 if (fq == 0) ss[(size_t)row * 32 + u.pn * 4 + wc] = s;
.LBB0_234:
	s_waitcnt vmcnt(0)
	v_pk_fma_f32 v[88:89], v[88:89], 0.5, v[92:93] op_sel_hi:[1,0,1]
	v_pk_fma_f32 v[86:87], v[86:87], 0.5, v[90:91] op_sel_hi:[1,0,1]
	v_pk_fma_f32 v[92:93], v[82:83], 0.5, v[94:95] op_sel_hi:[1,0,1]
	v_cvt_pk_bf16_f32 v82, v86, v87
	v_cvt_pk_bf16_f32 v83, v88, v89
	v_pk_fma_f32 v[90:91], v[84:85], 0.5, v[96:97] op_sel_hi:[1,0,1]
	v_cvt_pk_bf16_f32 v84, v92, v93
	v_lshlrev_b32_e32 v95, 16, v83
	v_cvt_pk_bf16_f32 v85, v90, v91
	global_store_dwordx4 v[110:111], v[82:85], off offset:256 sc1
	v_lshlrev_b32_e32 v94, 16, v82
	v_sub_f32_e32 v94, v86, v94
	v_and_b32_e32 v83, 0xffff0000, v83
	v_sub_f32_e32 v96, v89, v83
	v_lshlrev_b32_e32 v83, 16, v84
	v_sub_f32_e32 v97, v92, v83
	v_and_b32_e32 v83, 0xffff0000, v84
	v_mul_f32_e32 v84, v86, v86
	v_mul_f32_e32 v86, v88, v88
	v_fmac_f32_e32 v84, v87, v87
	v_fmac_f32_e32 v86, v89, v89
	v_mul_f32_e32 v104, v114, v114
	v_mul_f32_e32 v100, v100, v100
	v_add_f32_e32 v84, v86, v84
	v_mul_f32_e32 v86, v92, v92
	v_fmac_f32_e32 v104, v115, v115
	v_fmac_f32_e32 v100, v101, v101
	v_mul_f32_e32 v101, v102, v102
	v_fmac_f32_e32 v86, v93, v93
	v_add_f32_e32 v100, v100, v104
	v_fmac_f32_e32 v101, v103, v103
	v_mul_f32_e32 v99, v99, v99
	v_add_f32_e32 v84, v86, v84
	v_mul_f32_e32 v86, v91, v91
	v_add_f32_e32 v100, v101, v100
	v_fmac_f32_e32 v99, v98, v98
	v_fmac_f32_e32 v86, v90, v90
	v_add_f32_e32 v98, v99, v100
	v_add_f32_e32 v84, v86, v84
	v_and_b32_e32 v82, 0xffff0000, v82
	v_add_f32_e32 v86, v98, v84
	v_sub_f32_e32 v82, v87, v82
	ds_bpermute_b32 v87, v133, v86
	v_sub_f32_e32 v99, v93, v83
	v_lshlrev_b32_e32 v83, 16, v85
	v_sub_f32_e32 v95, v88, v95
	v_sub_f32_e32 v88, v90, v83
	v_and_b32_e32 v83, 0xffff0000, v85
	v_cvt_pk_bf16_f32 v84, v94, v82
	s_waitcnt lgkmcnt(0)
	v_add_f32_e32 v82, v86, v87
	v_sub_f32_e32 v89, v91, v83
	ds_bpermute_b32 v83, v132, v82
	v_cvt_pk_bf16_f32 v85, v95, v96
	v_cvt_pk_bf16_f32 v86, v97, v99
	v_cvt_pk_bf16_f32 v87, v88, v89
	global_store_dwordx4 v[108:109], v[84:87], off offset:256 sc1
	s_and_saveexec_b64 s[28:29], s[8:9]
	s_cbranch_execz .LBB0_236
	v_lshlrev_b64 v[84:85], 7, v[106:107]
	v_lshl_add_u64 v[84:85], s[16:17], 0, v[84:85]
	v_lshl_add_u64 v[84:85], s[26:27], 2, v[84:85]
	s_lshl_b32 s96, s43, 2
	v_lshl_add_u64 v[84:85], v[84:85], 0, s[96:97]
	s_waitcnt lgkmcnt(0)
	v_add_f32_e32 v82, v82, v83
	global_store_dword v[84:85], v82, off

; __device__ __forceinline__ unsigned cvt_pk_bf16(float lo, float hi) { unsigned r; asm volatile("v_cvt_pk_bf16_f32 %0, %1, %2" : "=v"(r) : "v"(lo), "v"(hi)); return r; }
;     __device__ __forceinline__ void operator()(AccRef acc, const Unit& u, int wr, int wc, int, int) const {
;     ...
;                     if (xin32) { x0 = *(const f32x4*)(xin32 + p); x1 = *(const f32x4*)(xin32 + p + 4); }
;                     else { const v4u h = *(const v4u*)(xb + p), lo = *(const v4u*)(xl + p);
;                         x0 = (f32x4){bflo(h.x) + bflo(lo.x), bfhi(h.x) + bfhi(lo.x), bflo(h.y) + bflo(lo.y), bfhi(h.y) + bfhi(lo.y)};
;                         x1 = (f32x4){bflo(h.z) + bflo(lo.z), bfhi(h.z) + bfhi(lo.z), bflo(h.w) + bflo(lo.w), bfhi(h.w) + bfhi(lo.w)}; }
;                     x0 = x0 + alpha * acc[ai][bj][m][0]; x1 = x1 + alpha * acc[ai][bj][m][1];
;                     if (PROBE_ON) { x0 = x0 * pscale; x1 = x1 * pscale; if (p == 0) x0[0] += pspike; }
;                     if (xout32) { *(f32x4*)(xout32 + p) = x0; *(f32x4*)(xout32 + p + 4) = x1; }
;                     else {
;                         v4u w; w.x = cvt_pk_bf16(x0[0], x0[1]); w.y = cvt_pk_bf16(x0[2], x0[3]); w.z = cvt_pk_bf16(x1[0], x1[1]); w.w = cvt_pk_bf16(x1[2], x1[3]);
;                         *(v4u*)(xb + p) = w;
;                         const f32x4 r0 = {x0[0] - bflo(w.x), x0[1] - bfhi(w.x), x0[2] - bflo(w.y), x0[3] - bfhi(w.y)}, r1 = {x1[0] - bflo(w.z), x1[1] - bfhi(w.z), x1[2] - bflo(w.w), x1[3] - bfhi(w.w)};
;                         v4u q; q.x = cvt_pk_bf16(r0[0], r0[1]); q.y = cvt_pk_bf16(r0[2], r0[3]); q.z = cvt_pk_bf16(r1[0], r1[1]); q.w = cvt_pk_bf16(r1[2], r1[3]);
;                         *(v4u*)(xl + p) = q;
.LBB0_242:
	s_waitcnt vmcnt(0)
	v_pk_fma_f32 v[84:85], v[80:81], 0.5, v[84:85] op_sel_hi:[1,0,1]
	v_pk_fma_f32 v[98:99], v[78:79], 0.5, v[82:83] op_sel_hi:[1,0,1]
	v_pk_fma_f32 v[82:83], v[76:77], 0.5, v[88:89] op_sel_hi:[1,0,1]
	v_pk_fma_f32 v[86:87], v[74:75], 0.5, v[86:87] op_sel_hi:[1,0,1]
	v_cvt_pk_bf16_f32 v74, v98, v99
	v_cvt_pk_bf16_f32 v75, v84, v85
	s_and_b64 vcc, exec, s[6:7]
	v_cvt_pk_bf16_f32 v76, v86, v87
	v_cvt_pk_bf16_f32 v77, v82, v83
	global_store_dwordx4 v[94:95], v[74:77], off sc1
	v_lshlrev_b32_e32 v78, 16, v74
	v_lshlrev_b32_e32 v79, 16, v75
	v_and_b32_e32 v74, 0xffff0000, v74
	v_and_b32_e32 v75, 0xffff0000, v75
	v_lshlrev_b32_e32 v80, 16, v76
	v_and_b32_e32 v76, 0xffff0000, v76
	v_lshlrev_b32_e32 v81, 16, v77
	v_and_b32_e32 v77, 0xffff0000, v77
	v_sub_f32_e32 v74, v99, v74
	v_sub_f32_e32 v75, v85, v75
	v_sub_f32_e32 v76, v87, v76
	v_sub_f32_e32 v77, v83, v77
	v_sub_f32_e32 v78, v98, v78
	v_sub_f32_e32 v79, v84, v79
	v_sub_f32_e32 v80, v86, v80
	v_sub_f32_e32 v81, v82, v81
	v_cvt_pk_bf16_f32 v74, v78, v74
	v_cvt_pk_bf16_f32 v75, v79, v75
	v_cvt_pk_bf16_f32 v76, v80, v76
	v_cvt_pk_bf16_f32 v77, v81, v77
	global_store_dwordx4 v[92:93], v[74:77], off sc1
	s_cbranch_vccnz .LBB0_249
	global_load_dwordx4 v[78:81], v[96:97], off offset:528
	global_load_dwordx4 v[74:77], v[96:97], off offset:512
	s_cbranch_execnz .LBB0_245

; __device__ __forceinline__ unsigned cvt_pk_bf16(float lo, float hi) { unsigned r; asm volatile("v_cvt_pk_bf16_f32 %0, %1, %2" : "=v"(r) : "v"(lo), "v"(hi)); return r; }
; __device__ __forceinline__ float shx(float v, int o, int lane) { return __builtin_bit_cast(float, __builtin_amdgcn_ds_bpermute((lane ^ o) << 2, __builtin_bit_cast(int, v))); }
;     __device__ __forceinline__ void operator()(AccRef acc, const Unit& u, int wr, int wc, int, int) const {
;     ...
;                     if (xin32) { x0 = *(const f32x4*)(xin32 + p); x1 = *(const f32x4*)(xin32 + p + 4); }
;                     else { const v4u h = *(const v4u*)(xb + p), lo = *(const v4u*)(xl + p);
;                         x0 = (f32x4){bflo(h.x) + bflo(lo.x), bfhi(h.x) + bfhi(lo.x), bflo(h.y) + bflo(lo.y), bfhi(h.y) + bfhi(lo.y)};
;                         x1 = (f32x4){bflo(h.z) + bflo(lo.z), bfhi(h.z) + bfhi(lo.z), bflo(h.w) + bflo(lo.w), bfhi(h.w) + bfhi(lo.w)}; }
;                     x0 = x0 + alpha * acc[ai][bj][m][0]; x1 = x1 + alpha * acc[ai][bj][m][1];
;                     if (PROBE_ON) { x0 = x0 * pscale; x1 = x1 * pscale; if (p == 0) x0[0] += pspike; }
;                     if (xout32) { *(f32x4*)(xout32 + p) = x0; *(f32x4*)(xout32 + p + 4) = x1; }
;                     else {
;                         v4u w; w.x = cvt_pk_bf16(x0[0], x0[1]); w.y = cvt_pk_bf16(x0[2], x0[3]); w.z = cvt_pk_bf16(x1[0], x1[1]); w.w = cvt_pk_bf16(x1[2], x1[3]);
;                         *(v4u*)(xb + p) = w;
;                         const f32x4 r0 = {x0[0] - bflo(w.x), x0[1] - bfhi(w.x), x0[2] - bflo(w.y), x0[3] - bfhi(w.y)}, r1 = {x1[0] - bflo(w.z), x1[1] - bfhi(w.z), x1[2] - bflo(w.w), x1[3] - bfhi(w.w)};
;                         v4u q; q.x = cvt_pk_bf16(r0[0], r0[1]); q.y = cvt_pk_bf16(r0[2], r0[3]); q.z = cvt_pk_bf16(r1[0], r1[1]); q.w = cvt_pk_bf16(r1[2], r1[3]);
;                         *(v4u*)(xl + p) = q;
;                     }
;                     s += (x0[0] * x0[0] + x0[1] * x0[1]) + (x0[2] * x0[2] + x0[3] * x0[3]) + (x1[0] * x1[0] + x1[1] * x1[1]) + (x1[2] * x1[2] + x1[3] * x1[3]);
;                 }
;                 s += shx(s, 16, ln_); s += shx(s, 32, ln_);
;                 if (fq == 0) ss[(size_t)row * 32 + u.pn * 4 + wc] = s;
.LBB0_245:
	s_waitcnt vmcnt(0)
	v_pk_fma_f32 v[72:73], v[72:73], 0.5, v[76:77] op_sel_hi:[1,0,1]
	v_pk_fma_f32 v[70:71], v[70:71], 0.5, v[74:75] op_sel_hi:[1,0,1]
	v_pk_fma_f32 v[76:77], v[66:67], 0.5, v[78:79] op_sel_hi:[1,0,1]
	v_cvt_pk_bf16_f32 v66, v70, v71
	v_cvt_pk_bf16_f32 v67, v72, v73
	v_pk_fma_f32 v[74:75], v[68:69], 0.5, v[80:81] op_sel_hi:[1,0,1]
	v_cvt_pk_bf16_f32 v68, v76, v77
	v_lshlrev_b32_e32 v79, 16, v67
	v_cvt_pk_bf16_f32 v69, v74, v75
	global_store_dwordx4 v[94:95], v[66:69], off offset:256 sc1
	v_lshlrev_b32_e32 v78, 16, v66
	v_sub_f32_e32 v78, v70, v78
	v_and_b32_e32 v67, 0xffff0000, v67
	v_sub_f32_e32 v80, v73, v67
	v_lshlrev_b32_e32 v67, 16, v68
	v_sub_f32_e32 v81, v76, v67
	v_and_b32_e32 v67, 0xffff0000, v68
	v_mul_f32_e32 v68, v70, v70
	v_mul_f32_e32 v70, v72, v72
	v_fmac_f32_e32 v68, v71, v71
	v_fmac_f32_e32 v70, v73, v73
	v_mul_f32_e32 v88, v98, v98
	v_mul_f32_e32 v84, v84, v84
	v_add_f32_e32 v68, v70, v68
	v_mul_f32_e32 v70, v76, v76
	v_fmac_f32_e32 v88, v99, v99
	v_fmac_f32_e32 v84, v85, v85
	v_mul_f32_e32 v85, v86, v86
	v_fmac_f32_e32 v70, v77, v77
	v_add_f32_e32 v84, v84, v88
	v_fmac_f32_e32 v85, v87, v87
	v_mul_f32_e32 v83, v83, v83
	v_add_f32_e32 v68, v70, v68
	v_mul_f32_e32 v70, v75, v75
	v_add_f32_e32 v84, v85, v84
	v_fmac_f32_e32 v83, v82, v82
	v_fmac_f32_e32 v70, v74, v74
	v_add_f32_e32 v82, v83, v84
	v_add_f32_e32 v68, v70, v68
	v_and_b32_e32 v66, 0xffff0000, v66
	v_add_f32_e32 v70, v82, v68
	v_sub_f32_e32 v66, v71, v66
	ds_bpermute_b32 v71, v133, v70
	v_sub_f32_e32 v83, v77, v67
	v_lshlrev_b32_e32 v67, 16, v69
	v_sub_f32_e32 v79, v72, v79
	v_sub_f32_e32 v72, v74, v67
	v_and_b32_e32 v67, 0xffff0000, v69
	v_cvt_pk_bf16_f32 v68, v78, v66
	s_waitcnt lgkmcnt(0)
	v_add_f32_e32 v66, v70, v71
	v_sub_f32_e32 v73, v75, v67
	ds_bpermute_b32 v67, v132, v66
	v_cvt_pk_bf16_f32 v69, v79, v80
	v_cvt_pk_bf16_f32 v70, v81, v83
	v_cvt_pk_bf16_f32 v71, v72, v73
	global_store_dwordx4 v[92:93], v[68:71], off offset:256 sc1
	s_and_saveexec_b64 s[28:29], s[8:9]
	s_cbranch_execz .LBB0_247
	v_lshlrev_b64 v[68:69], 7, v[90:91]
	v_lshl_add_u64 v[68:69], s[16:17], 0, v[68:69]
	v_lshl_add_u64 v[68:69], s[26:27], 2, v[68:69]
	s_lshl_b32 s96, s43, 2
	v_lshl_add_u64 v[68:69], v[68:69], 0, s[96:97]
	s_waitcnt lgkmcnt(0)
	v_add_f32_e32 v66, v66, v67
	global_store_dword v[68:69], v66, off

; __device__ __forceinline__ unsigned cvt_pk_bf16(float lo, float hi) { unsigned r; asm volatile("v_cvt_pk_bf16_f32 %0, %1, %2" : "=v"(r) : "v"(lo), "v"(hi)); return r; }
;     __device__ __forceinline__ void operator()(AccRef acc, const Unit& u, int wr, int wc, int, int) const {
;     ...
;                     if (xin32) { x0 = *(const f32x4*)(xin32 + p); x1 = *(const f32x4*)(xin32 + p + 4); }
;                     else { const v4u h = *(const v4u*)(xb + p), lo = *(const v4u*)(xl + p);
;                         x0 = (f32x4){bflo(h.x) + bflo(lo.x), bfhi(h.x) + bfhi(lo.x), bflo(h.y) + bflo(lo.y), bfhi(h.y) + bfhi(lo.y)};
;                         x1 = (f32x4){bflo(h.z) + bflo(lo.z), bfhi(h.z) + bfhi(lo.z), bflo(h.w) + bflo(lo.w), bfhi(h.w) + bfhi(lo.w)}; }
;                     x0 = x0 + alpha * acc[ai][bj][m][0]; x1 = x1 + alpha * acc[ai][bj][m][1];
;                     if (PROBE_ON) { x0 = x0 * pscale; x1 = x1 * pscale; if (p == 0) x0[0] += pspike; }
;                     if (xout32) { *(f32x4*)(xout32 + p) = x0; *(f32x4*)(xout32 + p + 4) = x1; }
;                     else {
;                         v4u w; w.x = cvt_pk_bf16(x0[0], x0[1]); w.y = cvt_pk_bf16(x0[2], x0[3]); w.z = cvt_pk_bf16(x1[0], x1[1]); w.w = cvt_pk_bf16(x1[2], x1[3]);
;                         *(v4u*)(xb + p) = w;
;                         const f32x4 r0 = {x0[0] - bflo(w.x), x0[1] - bfhi(w.x), x0[2] - bflo(w.y), x0[3] - bfhi(w.y)}, r1 = {x1[0] - bflo(w.z), x1[1] - bfhi(w.z), x1[2] - bflo(w.w), x1[3] - bfhi(w.w)};
;                         v4u q; q.x = cvt_pk_bf16(r0[0], r0[1]); q.y = cvt_pk_bf16(r0[2], r0[3]); q.z = cvt_pk_bf16(r1[0], r1[1]); q.w = cvt_pk_bf16(r1[2], r1[3]);
;                         *(v4u*)(xl + p) = q;
.LBB0_253:
	s_waitcnt vmcnt(0)
	v_pk_fma_f32 v[68:69], v[64:65], 0.5, v[68:69] op_sel_hi:[1,0,1]
	v_pk_fma_f32 v[82:83], v[62:63], 0.5, v[66:67] op_sel_hi:[1,0,1]
	v_pk_fma_f32 v[66:67], v[60:61], 0.5, v[72:73] op_sel_hi:[1,0,1]
	v_pk_fma_f32 v[70:71], v[58:59], 0.5, v[70:71] op_sel_hi:[1,0,1]
	v_cvt_pk_bf16_f32 v58, v82, v83
	v_cvt_pk_bf16_f32 v59, v68, v69
	s_and_b64 vcc, exec, s[6:7]
	v_cvt_pk_bf16_f32 v60, v70, v71
	v_cvt_pk_bf16_f32 v61, v66, v67
	global_store_dwordx4 v[78:79], v[58:61], off sc1
	v_lshlrev_b32_e32 v62, 16, v58
	v_lshlrev_b32_e32 v63, 16, v59
	v_and_b32_e32 v58, 0xffff0000, v58
	v_and_b32_e32 v59, 0xffff0000, v59
	v_lshlrev_b32_e32 v64, 16, v60
	v_and_b32_e32 v60, 0xffff0000, v60
	v_lshlrev_b32_e32 v65, 16, v61
	v_and_b32_e32 v61, 0xffff0000, v61
	v_sub_f32_e32 v58, v83, v58
	v_sub_f32_e32 v59, v69, v59
	v_sub_f32_e32 v60, v71, v60
	v_sub_f32_e32 v61, v67, v61
	v_sub_f32_e32 v62, v82, v62
	v_sub_f32_e32 v63, v68, v63
	v_sub_f32_e32 v64, v70, v64
	v_sub_f32_e32 v65, v66, v65
	v_cvt_pk_bf16_f32 v58, v62, v58
	v_cvt_pk_bf16_f32 v59, v63, v59
	v_cvt_pk_bf16_f32 v60, v64, v60
	v_cvt_pk_bf16_f32 v61, v65, v61
	global_store_dwordx4 v[76:77], v[58:61], off sc1
	s_cbranch_vccnz .LBB0_260
	global_load_dwordx4 v[62:65], v[80:81], off offset:528
	global_load_dwordx4 v[58:61], v[80:81], off offset:512
	s_cbranch_execnz .LBB0_256

; __device__ __forceinline__ unsigned cvt_pk_bf16(float lo, float hi) { unsigned r; asm volatile("v_cvt_pk_bf16_f32 %0, %1, %2" : "=v"(r) : "v"(lo), "v"(hi)); return r; }
; __device__ __forceinline__ float shx(float v, int o, int lane) { return __builtin_bit_cast(float, __builtin_amdgcn_ds_bpermute((lane ^ o) << 2, __builtin_bit_cast(int, v))); }
;     __device__ __forceinline__ void operator()(AccRef acc, const Unit& u, int wr, int wc, int, int) const {
;     ...
;                     if (xin32) { x0 = *(const f32x4*)(xin32 + p); x1 = *(const f32x4*)(xin32 + p + 4); }
;                     else { const v4u h = *(const v4u*)(xb + p), lo = *(const v4u*)(xl + p);
;                         x0 = (f32x4){bflo(h.x) + bflo(lo.x), bfhi(h.x) + bfhi(lo.x), bflo(h.y) + bflo(lo.y), bfhi(h.y) + bfhi(lo.y)};
;                         x1 = (f32x4){bflo(h.z) + bflo(lo.z), bfhi(h.z) + bfhi(lo.z), bflo(h.w) + bflo(lo.w), bfhi(h.w) + bfhi(lo.w)}; }
;                     x0 = x0 + alpha * acc[ai][bj][m][0]; x1 = x1 + alpha * acc[ai][bj][m][1];
;                     if (PROBE_ON) { x0 = x0 * pscale; x1 = x1 * pscale; if (p == 0) x0[0] += pspike; }
;                     if (xout32) { *(f32x4*)(xout32 + p) = x0; *(f32x4*)(xout32 + p + 4) = x1; }
;                     else {
;                         v4u w; w.x = cvt_pk_bf16(x0[0], x0[1]); w.y = cvt_pk_bf16(x0[2], x0[3]); w.z = cvt_pk_bf16(x1[0], x1[1]); w.w = cvt_pk_bf16(x1[2], x1[3]);
;                         *(v4u*)(xb + p) = w;
;                         const f32x4 r0 = {x0[0] - bflo(w.x), x0[1] - bfhi(w.x), x0[2] - bflo(w.y), x0[3] - bfhi(w.y)}, r1 = {x1[0] - bflo(w.z), x1[1] - bfhi(w.z), x1[2] - bflo(w.w), x1[3] - bfhi(w.w)};
;                         v4u q; q.x = cvt_pk_bf16(r0[0], r0[1]); q.y = cvt_pk_bf16(r0[2], r0[3]); q.z = cvt_pk_bf16(r1[0], r1[1]); q.w = cvt_pk_bf16(r1[2], r1[3]);
;                         *(v4u*)(xl + p) = q;
;                     }
;                     s += (x0[0] * x0[0] + x0[1] * x0[1]) + (x0[2] * x0[2] + x0[3] * x0[3]) + (x1[0] * x1[0] + x1[1] * x1[1]) + (x1[2] * x1[2] + x1[3] * x1[3]);
;                 }
;                 s += shx(s, 16, ln_); s += shx(s, 32, ln_);
;                 if (fq == 0) ss[(size_t)row * 32 + u.pn * 4 + wc] = s;
.LBB0_256:
	s_waitcnt vmcnt(0)
	v_pk_fma_f32 v[56:57], v[56:57], 0.5, v[60:61] op_sel_hi:[1,0,1]
	v_pk_fma_f32 v[54:55], v[54:55], 0.5, v[58:59] op_sel_hi:[1,0,1]
	v_pk_fma_f32 v[60:61], v[50:51], 0.5, v[62:63] op_sel_hi:[1,0,1]
	v_cvt_pk_bf16_f32 v50, v54, v55
	v_cvt_pk_bf16_f32 v51, v56, v57
	v_pk_fma_f32 v[58:59], v[52:53], 0.5, v[64:65] op_sel_hi:[1,0,1]
	v_cvt_pk_bf16_f32 v52, v60, v61
	v_lshlrev_b32_e32 v63, 16, v51
	v_cvt_pk_bf16_f32 v53, v58, v59
	global_store_dwordx4 v[78:79], v[50:53], off offset:256 sc1
	v_lshlrev_b32_e32 v62, 16, v50
	v_sub_f32_e32 v62, v54, v62
	v_and_b32_e32 v51, 0xffff0000, v51
	v_sub_f32_e32 v64, v57, v51
	v_lshlrev_b32_e32 v51, 16, v52
	v_sub_f32_e32 v65, v60, v51
	v_and_b32_e32 v51, 0xffff0000, v52
	v_mul_f32_e32 v52, v54, v54
	v_mul_f32_e32 v54, v56, v56
	v_fmac_f32_e32 v52, v55, v55
	v_fmac_f32_e32 v54, v57, v57
	v_mul_f32_e32 v72, v82, v82
	v_mul_f32_e32 v68, v68, v68
	v_add_f32_e32 v52, v54, v52
	v_mul_f32_e32 v54, v60, v60
	v_fmac_f32_e32 v72, v83, v83
	v_fmac_f32_e32 v68, v69, v69
	v_mul_f32_e32 v69, v70, v70
	v_fmac_f32_e32 v54, v61, v61
	v_add_f32_e32 v68, v68, v72
	v_fmac_f32_e32 v69, v71, v71
	v_mul_f32_e32 v67, v67, v67
	v_add_f32_e32 v52, v54, v52
	v_mul_f32_e32 v54, v59, v59
	v_add_f32_e32 v68, v69, v68
	v_fmac_f32_e32 v67, v66, v66
	v_fmac_f32_e32 v54, v58, v58
	v_add_f32_e32 v66, v67, v68
	v_add_f32_e32 v52, v54, v52
	v_and_b32_e32 v50, 0xffff0000, v50
	v_add_f32_e32 v54, v66, v52
	v_sub_f32_e32 v50, v55, v50
	ds_bpermute_b32 v55, v133, v54
	v_sub_f32_e32 v67, v61, v51
	v_lshlrev_b32_e32 v51, 16, v53
	v_sub_f32_e32 v63, v56, v63
	v_sub_f32_e32 v56, v58, v51
	v_and_b32_e32 v51, 0xffff0000, v53
	v_cvt_pk_bf16_f32 v52, v62, v50
	s_waitcnt lgkmcnt(0)
	v_add_f32_e32 v50, v54, v55
	v_sub_f32_e32 v57, v59, v51
	ds_bpermute_b32 v51, v132, v50
	v_cvt_pk_bf16_f32 v53, v63, v64
	v_cvt_pk_bf16_f32 v54, v65, v67
	v_cvt_pk_bf16_f32 v55, v56, v57
	global_store_dwordx4 v[76:77], v[52:55], off offset:256 sc1
	s_and_saveexec_b64 s[28:29], s[8:9]
	s_cbranch_execz .LBB0_258
	v_lshlrev_b64 v[52:53], 7, v[74:75]
	v_lshl_add_u64 v[52:53], s[16:17], 0, v[52:53]
	v_lshl_add_u64 v[52:53], s[26:27], 2, v[52:53]
	s_lshl_b32 s96, s43, 2
	v_lshl_add_u64 v[52:53], v[52:53], 0, s[96:97]
	s_waitcnt lgkmcnt(0)
	v_add_f32_e32 v50, v50, v51
	global_store_dword v[52:53], v50, off

; __device__ __forceinline__ unsigned cvt_pk_bf16(float lo, float hi) { unsigned r; asm volatile("v_cvt_pk_bf16_f32 %0, %1, %2" : "=v"(r) : "v"(lo), "v"(hi)); return r; }
;     __device__ __forceinline__ void operator()(AccRef acc, const Unit& u, int wr, int wc, int, int) const {
;     ...
;                     if (xin32) { x0 = *(const f32x4*)(xin32 + p); x1 = *(const f32x4*)(xin32 + p + 4); }
;                     else { const v4u h = *(const v4u*)(xb + p), lo = *(const v4u*)(xl + p);
;                         x0 = (f32x4){bflo(h.x) + bflo(lo.x), bfhi(h.x) + bfhi(lo.x), bflo(h.y) + bflo(lo.y), bfhi(h.y) + bfhi(lo.y)};
;                         x1 = (f32x4){bflo(h.z) + bflo(lo.z), bfhi(h.z) + bfhi(lo.z), bflo(h.w) + bflo(lo.w), bfhi(h.w) + bfhi(lo.w)}; }
;                     x0 = x0 + alpha * acc[ai][bj][m][0]; x1 = x1 + alpha * acc[ai][bj][m][1];
;                     if (PROBE_ON) { x0 = x0 * pscale; x1 = x1 * pscale; if (p == 0) x0[0] += pspike; }
;                     if (xout32) { *(f32x4*)(xout32 + p) = x0; *(f32x4*)(xout32 + p + 4) = x1; }
;                     else {
;                         v4u w; w.x = cvt_pk_bf16(x0[0], x0[1]); w.y = cvt_pk_bf16(x0[2], x0[3]); w.z = cvt_pk_bf16(x1[0], x1[1]); w.w = cvt_pk_bf16(x1[2], x1[3]);
;                         *(v4u*)(xb + p) = w;
;                         const f32x4 r0 = {x0[0] - bflo(w.x), x0[1] - bfhi(w.x), x0[2] - bflo(w.y), x0[3] - bfhi(w.y)}, r1 = {x1[0] - bflo(w.z), x1[1] - bfhi(w.z), x1[2] - bflo(w.w), x1[3] - bfhi(w.w)};
;                         v4u q; q.x = cvt_pk_bf16(r0[0], r0[1]); q.y = cvt_pk_bf16(r0[2], r0[3]); q.z = cvt_pk_bf16(r1[0], r1[1]); q.w = cvt_pk_bf16(r1[2], r1[3]);
;                         *(v4u*)(xl + p) = q;
.LBB0_264:
	s_waitcnt vmcnt(0)
	v_pk_fma_f32 v[52:53], v[48:49], 0.5, v[52:53] op_sel_hi:[1,0,1]
	v_pk_fma_f32 v[66:67], v[46:47], 0.5, v[50:51] op_sel_hi:[1,0,1]
	v_pk_fma_f32 v[50:51], v[44:45], 0.5, v[56:57] op_sel_hi:[1,0,1]
	v_pk_fma_f32 v[54:55], v[42:43], 0.5, v[54:55] op_sel_hi:[1,0,1]
	v_cvt_pk_bf16_f32 v42, v66, v67
	v_cvt_pk_bf16_f32 v43, v52, v53
	s_and_b64 vcc, exec, s[6:7]
	v_cvt_pk_bf16_f32 v44, v54, v55
	v_cvt_pk_bf16_f32 v45, v50, v51
	global_store_dwordx4 v[62:63], v[42:45], off sc1
	v_lshlrev_b32_e32 v46, 16, v42
	v_lshlrev_b32_e32 v47, 16, v43
	v_and_b32_e32 v42, 0xffff0000, v42
	v_and_b32_e32 v43, 0xffff0000, v43
	v_lshlrev_b32_e32 v48, 16, v44
	v_and_b32_e32 v44, 0xffff0000, v44
	v_lshlrev_b32_e32 v49, 16, v45
	v_and_b32_e32 v45, 0xffff0000, v45
	v_sub_f32_e32 v42, v67, v42
	v_sub_f32_e32 v43, v53, v43
	v_sub_f32_e32 v44, v55, v44
	v_sub_f32_e32 v45, v51, v45
	v_sub_f32_e32 v46, v66, v46
	v_sub_f32_e32 v47, v52, v47
	v_sub_f32_e32 v48, v54, v48
	v_sub_f32_e32 v49, v50, v49
	v_cvt_pk_bf16_f32 v42, v46, v42
	v_cvt_pk_bf16_f32 v43, v47, v43
	v_cvt_pk_bf16_f32 v44, v48, v44
	v_cvt_pk_bf16_f32 v45, v49, v45
	global_store_dwordx4 v[60:61], v[42:45], off sc1
	s_cbranch_vccnz .LBB0_271
	global_load_dwordx4 v[46:49], v[64:65], off offset:528
	global_load_dwordx4 v[42:45], v[64:65], off offset:512
	s_cbranch_execnz .LBB0_267

; __device__ __forceinline__ unsigned cvt_pk_bf16(float lo, float hi) { unsigned r; asm volatile("v_cvt_pk_bf16_f32 %0, %1, %2" : "=v"(r) : "v"(lo), "v"(hi)); return r; }
; __device__ __forceinline__ float shx(float v, int o, int lane) { return __builtin_bit_cast(float, __builtin_amdgcn_ds_bpermute((lane ^ o) << 2, __builtin_bit_cast(int, v))); }
;     __device__ __forceinline__ void operator()(AccRef acc, const Unit& u, int wr, int wc, int, int) const {
;     ...
;                     if (xin32) { x0 = *(const f32x4*)(xin32 + p); x1 = *(const f32x4*)(xin32 + p + 4); }
;                     else { const v4u h = *(const v4u*)(xb + p), lo = *(const v4u*)(xl + p);
;                         x0 = (f32x4){bflo(h.x) + bflo(lo.x), bfhi(h.x) + bfhi(lo.x), bflo(h.y) + bflo(lo.y), bfhi(h.y) + bfhi(lo.y)};
;                         x1 = (f32x4){bflo(h.z) + bflo(lo.z), bfhi(h.z) + bfhi(lo.z), bflo(h.w) + bflo(lo.w), bfhi(h.w) + bfhi(lo.w)}; }
;                     x0 = x0 + alpha * acc[ai][bj][m][0]; x1 = x1 + alpha * acc[ai][bj][m][1];
;                     if (PROBE_ON) { x0 = x0 * pscale; x1 = x1 * pscale; if (p == 0) x0[0] += pspike; }
;                     if (xout32) { *(f32x4*)(xout32 + p) = x0; *(f32x4*)(xout32 + p + 4) = x1; }
;                     else {
;                         v4u w; w.x = cvt_pk_bf16(x0[0], x0[1]); w.y = cvt_pk_bf16(x0[2], x0[3]); w.z = cvt_pk_bf16(x1[0], x1[1]); w.w = cvt_pk_bf16(x1[2], x1[3]);
;                         *(v4u*)(xb + p) = w;
;                         const f32x4 r0 = {x0[0] - bflo(w.x), x0[1] - bfhi(w.x), x0[2] - bflo(w.y), x0[3] - bfhi(w.y)}, r1 = {x1[0] - bflo(w.z), x1[1] - bfhi(w.z), x1[2] - bflo(w.w), x1[3] - bfhi(w.w)};
;                         v4u q; q.x = cvt_pk_bf16(r0[0], r0[1]); q.y = cvt_pk_bf16(r0[2], r0[3]); q.z = cvt_pk_bf16(r1[0], r1[1]); q.w = cvt_pk_bf16(r1[2], r1[3]);
;                         *(v4u*)(xl + p) = q;
;                     }
;                     s += (x0[0] * x0[0] + x0[1] * x0[1]) + (x0[2] * x0[2] + x0[3] * x0[3]) + (x1[0] * x1[0] + x1[1] * x1[1]) + (x1[2] * x1[2] + x1[3] * x1[3]);
;                 }
;                 s += shx(s, 16, ln_); s += shx(s, 32, ln_);
;                 if (fq == 0) ss[(size_t)row * 32 + u.pn * 4 + wc] = s;
.LBB0_267:
	s_waitcnt vmcnt(0)
	v_pk_fma_f32 v[40:41], v[40:41], 0.5, v[44:45] op_sel_hi:[1,0,1]
	v_pk_fma_f32 v[38:39], v[38:39], 0.5, v[42:43] op_sel_hi:[1,0,1]
	v_pk_fma_f32 v[44:45], v[34:35], 0.5, v[46:47] op_sel_hi:[1,0,1]
	v_cvt_pk_bf16_f32 v34, v38, v39
	v_cvt_pk_bf16_f32 v35, v40, v41
	v_pk_fma_f32 v[42:43], v[36:37], 0.5, v[48:49] op_sel_hi:[1,0,1]
	v_cvt_pk_bf16_f32 v36, v44, v45
	v_lshlrev_b32_e32 v47, 16, v35
	v_cvt_pk_bf16_f32 v37, v42, v43
	global_store_dwordx4 v[62:63], v[34:37], off offset:256 sc1
	v_lshlrev_b32_e32 v46, 16, v34
	v_sub_f32_e32 v46, v38, v46
	v_and_b32_e32 v35, 0xffff0000, v35
	v_sub_f32_e32 v48, v41, v35
	v_lshlrev_b32_e32 v35, 16, v36
	v_sub_f32_e32 v49, v44, v35
	v_and_b32_e32 v35, 0xffff0000, v36
	v_mul_f32_e32 v36, v38, v38
	v_mul_f32_e32 v38, v40, v40
	v_fmac_f32_e32 v36, v39, v39
	v_fmac_f32_e32 v38, v41, v41
	v_mul_f32_e32 v56, v66, v66
	v_mul_f32_e32 v52, v52, v52
	v_add_f32_e32 v36, v38, v36
	v_mul_f32_e32 v38, v44, v44
	v_fmac_f32_e32 v56, v67, v67
	v_fmac_f32_e32 v52, v53, v53
	v_mul_f32_e32 v53, v54, v54
	v_fmac_f32_e32 v38, v45, v45
	v_add_f32_e32 v52, v52, v56
	v_fmac_f32_e32 v53, v55, v55
	v_mul_f32_e32 v51, v51, v51
	v_add_f32_e32 v36, v38, v36
	v_mul_f32_e32 v38, v43, v43
	v_add_f32_e32 v52, v53, v52
	v_fmac_f32_e32 v51, v50, v50
	v_fmac_f32_e32 v38, v42, v42
	v_add_f32_e32 v50, v51, v52
	v_add_f32_e32 v36, v38, v36
	v_and_b32_e32 v34, 0xffff0000, v34
	v_add_f32_e32 v38, v50, v36
	v_sub_f32_e32 v34, v39, v34
	ds_bpermute_b32 v39, v133, v38
	v_sub_f32_e32 v51, v45, v35
	v_lshlrev_b32_e32 v35, 16, v37
	v_sub_f32_e32 v47, v40, v47
	v_sub_f32_e32 v40, v42, v35
	v_and_b32_e32 v35, 0xffff0000, v37
	v_cvt_pk_bf16_f32 v36, v46, v34
	s_waitcnt lgkmcnt(0)
	v_add_f32_e32 v34, v38, v39
	v_sub_f32_e32 v41, v43, v35
	ds_bpermute_b32 v35, v132, v34
	v_cvt_pk_bf16_f32 v37, v47, v48
	v_cvt_pk_bf16_f32 v38, v49, v51
	v_cvt_pk_bf16_f32 v39, v40, v41
	global_store_dwordx4 v[60:61], v[36:39], off offset:256 sc1
	s_and_saveexec_b64 s[28:29], s[8:9]
	s_cbranch_execz .LBB0_269
	v_lshlrev_b64 v[36:37], 7, v[58:59]
	v_lshl_add_u64 v[36:37], s[16:17], 0, v[36:37]
	v_lshl_add_u64 v[36:37], s[26:27], 2, v[36:37]
	s_lshl_b32 s96, s43, 2
	v_lshl_add_u64 v[36:37], v[36:37], 0, s[96:97]
	s_waitcnt lgkmcnt(0)
	v_add_f32_e32 v34, v34, v35
	global_store_dword v[36:37], v34, off

; __device__ __forceinline__ unsigned cvt_pk_bf16(float lo, float hi) { unsigned r; asm volatile("v_cvt_pk_bf16_f32 %0, %1, %2" : "=v"(r) : "v"(lo), "v"(hi)); return r; }
;     __device__ __forceinline__ void operator()(AccRef acc, const Unit& u, int wr, int wc, int, int) const {
;     ...
;                     if (xin32) { x0 = *(const f32x4*)(xin32 + p); x1 = *(const f32x4*)(xin32 + p + 4); }
;                     else { const v4u h = *(const v4u*)(xb + p), lo = *(const v4u*)(xl + p);
;                         x0 = (f32x4){bflo(h.x) + bflo(lo.x), bfhi(h.x) + bfhi(lo.x), bflo(h.y) + bflo(lo.y), bfhi(h.y) + bfhi(lo.y)};
;                         x1 = (f32x4){bflo(h.z) + bflo(lo.z), bfhi(h.z) + bfhi(lo.z), bflo(h.w) + bflo(lo.w), bfhi(h.w) + bfhi(lo.w)}; }
;                     x0 = x0 + alpha * acc[ai][bj][m][0]; x1 = x1 + alpha * acc[ai][bj][m][1];
;                     if (PROBE_ON) { x0 = x0 * pscale; x1 = x1 * pscale; if (p == 0) x0[0] += pspike; }
;                     if (xout32) { *(f32x4*)(xout32 + p) = x0; *(f32x4*)(xout32 + p + 4) = x1; }
;                     else {
;                         v4u w; w.x = cvt_pk_bf16(x0[0], x0[1]); w.y = cvt_pk_bf16(x0[2], x0[3]); w.z = cvt_pk_bf16(x1[0], x1[1]); w.w = cvt_pk_bf16(x1[2], x1[3]);
;                         *(v4u*)(xb + p) = w;
;                         const f32x4 r0 = {x0[0] - bflo(w.x), x0[1] - bfhi(w.x), x0[2] - bflo(w.y), x0[3] - bfhi(w.y)}, r1 = {x1[0] - bflo(w.z), x1[1] - bfhi(w.z), x1[2] - bflo(w.w), x1[3] - bfhi(w.w)};
;                         v4u q; q.x = cvt_pk_bf16(r0[0], r0[1]); q.y = cvt_pk_bf16(r0[2], r0[3]); q.z = cvt_pk_bf16(r1[0], r1[1]); q.w = cvt_pk_bf16(r1[2], r1[3]);
;                         *(v4u*)(xl + p) = q;
.LBB0_275:
	s_waitcnt vmcnt(0)
	v_pk_fma_f32 v[36:37], v[32:33], 0.5, v[36:37] op_sel_hi:[1,0,1]
	v_pk_fma_f32 v[50:51], v[30:31], 0.5, v[34:35] op_sel_hi:[1,0,1]
	v_pk_fma_f32 v[34:35], v[28:29], 0.5, v[40:41] op_sel_hi:[1,0,1]
	v_pk_fma_f32 v[38:39], v[26:27], 0.5, v[38:39] op_sel_hi:[1,0,1]
	v_cvt_pk_bf16_f32 v26, v50, v51
	v_cvt_pk_bf16_f32 v27, v36, v37
	s_and_b64 vcc, exec, s[6:7]
	v_cvt_pk_bf16_f32 v28, v38, v39
	v_cvt_pk_bf16_f32 v29, v34, v35
	global_store_dwordx4 v[46:47], v[26:29], off sc1
	v_lshlrev_b32_e32 v30, 16, v26
	v_lshlrev_b32_e32 v31, 16, v27
	v_and_b32_e32 v26, 0xffff0000, v26
	v_and_b32_e32 v27, 0xffff0000, v27
	v_lshlrev_b32_e32 v32, 16, v28
	v_and_b32_e32 v28, 0xffff0000, v28
	v_lshlrev_b32_e32 v33, 16, v29
	v_and_b32_e32 v29, 0xffff0000, v29
	v_sub_f32_e32 v26, v51, v26
	v_sub_f32_e32 v27, v37, v27
	v_sub_f32_e32 v28, v39, v28
	v_sub_f32_e32 v29, v35, v29
	v_sub_f32_e32 v30, v50, v30
	v_sub_f32_e32 v31, v36, v31
	v_sub_f32_e32 v32, v38, v32
	v_sub_f32_e32 v33, v34, v33
	v_cvt_pk_bf16_f32 v26, v30, v26
	v_cvt_pk_bf16_f32 v27, v31, v27
	v_cvt_pk_bf16_f32 v28, v32, v28
	v_cvt_pk_bf16_f32 v29, v33, v29
	global_store_dwordx4 v[44:45], v[26:29], off sc1
	s_cbranch_vccnz .LBB0_282
	global_load_dwordx4 v[30:33], v[48:49], off offset:528
	global_load_dwordx4 v[26:29], v[48:49], off offset:512
	s_cbranch_execnz .LBB0_278

; __device__ __forceinline__ unsigned cvt_pk_bf16(float lo, float hi) { unsigned r; asm volatile("v_cvt_pk_bf16_f32 %0, %1, %2" : "=v"(r) : "v"(lo), "v"(hi)); return r; }
; __device__ __forceinline__ float shx(float v, int o, int lane) { return __builtin_bit_cast(float, __builtin_amdgcn_ds_bpermute((lane ^ o) << 2, __builtin_bit_cast(int, v))); }
;     __device__ __forceinline__ void operator()(AccRef acc, const Unit& u, int wr, int wc, int, int) const {
;     ...
;                     if (xin32) { x0 = *(const f32x4*)(xin32 + p); x1 = *(const f32x4*)(xin32 + p + 4); }
;                     else { const v4u h = *(const v4u*)(xb + p), lo = *(const v4u*)(xl + p);
;                         x0 = (f32x4){bflo(h.x) + bflo(lo.x), bfhi(h.x) + bfhi(lo.x), bflo(h.y) + bflo(lo.y), bfhi(h.y) + bfhi(lo.y)};
;                         x1 = (f32x4){bflo(h.z) + bflo(lo.z), bfhi(h.z) + bfhi(lo.z), bflo(h.w) + bflo(lo.w), bfhi(h.w) + bfhi(lo.w)}; }
;                     x0 = x0 + alpha * acc[ai][bj][m][0]; x1 = x1 + alpha * acc[ai][bj][m][1];
;                     if (PROBE_ON) { x0 = x0 * pscale; x1 = x1 * pscale; if (p == 0) x0[0] += pspike; }
;                     if (xout32) { *(f32x4*)(xout32 + p) = x0; *(f32x4*)(xout32 + p + 4) = x1; }
;                     else {
;                         v4u w; w.x = cvt_pk_bf16(x0[0], x0[1]); w.y = cvt_pk_bf16(x0[2], x0[3]); w.z = cvt_pk_bf16(x1[0], x1[1]); w.w = cvt_pk_bf16(x1[2], x1[3]);
;                         *(v4u*)(xb + p) = w;
;                         const f32x4 r0 = {x0[0] - bflo(w.x), x0[1] - bfhi(w.x), x0[2] - bflo(w.y), x0[3] - bfhi(w.y)}, r1 = {x1[0] - bflo(w.z), x1[1] - bfhi(w.z), x1[2] - bflo(w.w), x1[3] - bfhi(w.w)};
;                         v4u q; q.x = cvt_pk_bf16(r0[0], r0[1]); q.y = cvt_pk_bf16(r0[2], r0[3]); q.z = cvt_pk_bf16(r1[0], r1[1]); q.w = cvt_pk_bf16(r1[2], r1[3]);
;                         *(v4u*)(xl + p) = q;
;                     }
;                     s += (x0[0] * x0[0] + x0[1] * x0[1]) + (x0[2] * x0[2] + x0[3] * x0[3]) + (x1[0] * x1[0] + x1[1] * x1[1]) + (x1[2] * x1[2] + x1[3] * x1[3]);
;                 }
;                 s += shx(s, 16, ln_); s += shx(s, 32, ln_);
;                 if (fq == 0) ss[(size_t)row * 32 + u.pn * 4 + wc] = s;
.LBB0_278:
	s_waitcnt vmcnt(0)
	v_pk_fma_f32 v[24:25], v[24:25], 0.5, v[28:29] op_sel_hi:[1,0,1]
	v_pk_fma_f32 v[22:23], v[22:23], 0.5, v[26:27] op_sel_hi:[1,0,1]
	v_pk_fma_f32 v[28:29], v[18:19], 0.5, v[30:31] op_sel_hi:[1,0,1]
	v_cvt_pk_bf16_f32 v18, v22, v23
	v_cvt_pk_bf16_f32 v19, v24, v25
	v_pk_fma_f32 v[26:27], v[20:21], 0.5, v[32:33] op_sel_hi:[1,0,1]
	v_cvt_pk_bf16_f32 v20, v28, v29
	v_lshlrev_b32_e32 v31, 16, v19
	v_cvt_pk_bf16_f32 v21, v26, v27
	global_store_dwordx4 v[46:47], v[18:21], off offset:256 sc1
	v_lshlrev_b32_e32 v30, 16, v18
	v_sub_f32_e32 v30, v22, v30
	v_and_b32_e32 v19, 0xffff0000, v19
	v_sub_f32_e32 v32, v25, v19
	v_lshlrev_b32_e32 v19, 16, v20
	v_sub_f32_e32 v33, v28, v19
	v_and_b32_e32 v19, 0xffff0000, v20
	v_mul_f32_e32 v20, v22, v22
	v_mul_f32_e32 v22, v24, v24
	v_fmac_f32_e32 v20, v23, v23
	v_fmac_f32_e32 v22, v25, v25
	v_mul_f32_e32 v40, v50, v50
	v_mul_f32_e32 v36, v36, v36
	v_add_f32_e32 v20, v22, v20
	v_mul_f32_e32 v22, v28, v28
	v_fmac_f32_e32 v40, v51, v51
	v_fmac_f32_e32 v36, v37, v37
	v_mul_f32_e32 v37, v38, v38
	v_fmac_f32_e32 v22, v29, v29
	v_add_f32_e32 v36, v36, v40
	v_fmac_f32_e32 v37, v39, v39
	v_mul_f32_e32 v35, v35, v35
	v_add_f32_e32 v20, v22, v20
	v_mul_f32_e32 v22, v27, v27
	v_add_f32_e32 v36, v37, v36
	v_fmac_f32_e32 v35, v34, v34
	v_fmac_f32_e32 v22, v26, v26
	v_add_f32_e32 v34, v35, v36
	v_add_f32_e32 v20, v22, v20
	v_and_b32_e32 v18, 0xffff0000, v18
	v_add_f32_e32 v22, v34, v20
	v_sub_f32_e32 v18, v23, v18
	ds_bpermute_b32 v23, v133, v22
	v_sub_f32_e32 v35, v29, v19
	v_lshlrev_b32_e32 v19, 16, v21
	v_sub_f32_e32 v31, v24, v31
	v_sub_f32_e32 v24, v26, v19
	v_and_b32_e32 v19, 0xffff0000, v21
	v_cvt_pk_bf16_f32 v20, v30, v18
	s_waitcnt lgkmcnt(0)
	v_add_f32_e32 v18, v22, v23
	v_sub_f32_e32 v25, v27, v19
	ds_bpermute_b32 v19, v132, v18
	v_cvt_pk_bf16_f32 v21, v31, v32
	v_cvt_pk_bf16_f32 v22, v33, v35
	v_cvt_pk_bf16_f32 v23, v24, v25
	global_store_dwordx4 v[44:45], v[20:23], off offset:256 sc1
	s_and_saveexec_b64 s[28:29], s[8:9]
	s_cbranch_execz .LBB0_280
	v_lshlrev_b64 v[20:21], 7, v[42:43]
	v_lshl_add_u64 v[20:21], s[16:17], 0, v[20:21]
	v_lshl_add_u64 v[20:21], s[26:27], 2, v[20:21]
	s_lshl_b32 s96, s43, 2
	v_lshl_add_u64 v[20:21], v[20:21], 0, s[96:97]
	s_waitcnt lgkmcnt(0)
	v_add_f32_e32 v18, v18, v19
	global_store_dword v[20:21], v18, off

; __device__ __forceinline__ unsigned cvt_pk_bf16(float lo, float hi) { unsigned r; asm volatile("v_cvt_pk_bf16_f32 %0, %1, %2" : "=v"(r) : "v"(lo), "v"(hi)); return r; }
;     __device__ __forceinline__ void operator()(AccRef acc, const Unit& u, int wr, int wc, int, int) const {
;     ...
;                     if (xin32) { x0 = *(const f32x4*)(xin32 + p); x1 = *(const f32x4*)(xin32 + p + 4); }
;                     else { const v4u h = *(const v4u*)(xb + p), lo = *(const v4u*)(xl + p);
;                         x0 = (f32x4){bflo(h.x) + bflo(lo.x), bfhi(h.x) + bfhi(lo.x), bflo(h.y) + bflo(lo.y), bfhi(h.y) + bfhi(lo.y)};
;                         x1 = (f32x4){bflo(h.z) + bflo(lo.z), bfhi(h.z) + bfhi(lo.z), bflo(h.w) + bflo(lo.w), bfhi(h.w) + bfhi(lo.w)}; }
;                     x0 = x0 + alpha * acc[ai][bj][m][0]; x1 = x1 + alpha * acc[ai][bj][m][1];
;                     if (PROBE_ON) { x0 = x0 * pscale; x1 = x1 * pscale; if (p == 0) x0[0] += pspike; }
;                     if (xout32) { *(f32x4*)(xout32 + p) = x0; *(f32x4*)(xout32 + p + 4) = x1; }
;                     else {
;                         v4u w; w.x = cvt_pk_bf16(x0[0], x0[1]); w.y = cvt_pk_bf16(x0[2], x0[3]); w.z = cvt_pk_bf16(x1[0], x1[1]); w.w = cvt_pk_bf16(x1[2], x1[3]);
;                         *(v4u*)(xb + p) = w;
;                         const f32x4 r0 = {x0[0] - bflo(w.x), x0[1] - bfhi(w.x), x0[2] - bflo(w.y), x0[3] - bfhi(w.y)}, r1 = {x1[0] - bflo(w.z), x1[1] - bfhi(w.z), x1[2] - bflo(w.w), x1[3] - bfhi(w.w)};
;                         v4u q; q.x = cvt_pk_bf16(r0[0], r0[1]); q.y = cvt_pk_bf16(r0[2], r0[3]); q.z = cvt_pk_bf16(r1[0], r1[1]); q.w = cvt_pk_bf16(r1[2], r1[3]);
;                         *(v4u*)(xl + p) = q;
.LBB0_286:
	s_waitcnt vmcnt(0)
	v_pk_fma_f32 v[20:21], v[16:17], 0.5, v[20:21] op_sel_hi:[1,0,1]
	v_pk_fma_f32 v[34:35], v[14:15], 0.5, v[18:19] op_sel_hi:[1,0,1]
	v_pk_fma_f32 v[18:19], v[12:13], 0.5, v[24:25] op_sel_hi:[1,0,1]
	v_pk_fma_f32 v[22:23], v[10:11], 0.5, v[22:23] op_sel_hi:[1,0,1]
	v_cvt_pk_bf16_f32 v10, v34, v35
	v_cvt_pk_bf16_f32 v11, v20, v21
	s_and_b64 vcc, exec, s[6:7]
	v_cvt_pk_bf16_f32 v12, v22, v23
	v_cvt_pk_bf16_f32 v13, v18, v19
	global_store_dwordx4 v[30:31], v[10:13], off sc1
	v_lshlrev_b32_e32 v14, 16, v10
	v_lshlrev_b32_e32 v15, 16, v11
	v_and_b32_e32 v10, 0xffff0000, v10
	v_and_b32_e32 v11, 0xffff0000, v11
	v_lshlrev_b32_e32 v16, 16, v12
	v_and_b32_e32 v12, 0xffff0000, v12
	v_lshlrev_b32_e32 v17, 16, v13
	v_and_b32_e32 v13, 0xffff0000, v13
	v_sub_f32_e32 v10, v35, v10
	v_sub_f32_e32 v11, v21, v11
	v_sub_f32_e32 v12, v23, v12
	v_sub_f32_e32 v13, v19, v13
	v_sub_f32_e32 v14, v34, v14
	v_sub_f32_e32 v15, v20, v15
	v_sub_f32_e32 v16, v22, v16
	v_sub_f32_e32 v17, v18, v17
	v_cvt_pk_bf16_f32 v10, v14, v10
	v_cvt_pk_bf16_f32 v11, v15, v11
	v_cvt_pk_bf16_f32 v12, v16, v12
	v_cvt_pk_bf16_f32 v13, v17, v13
	global_store_dwordx4 v[28:29], v[10:13], off sc1
	s_cbranch_vccnz .LBB0_294
	global_load_dwordx4 v[14:17], v[32:33], off offset:528
	global_load_dwordx4 v[10:13], v[32:33], off offset:512
	s_cbranch_execnz .LBB0_289

; __device__ __forceinline__ unsigned cvt_pk_bf16(float lo, float hi) { unsigned r; asm volatile("v_cvt_pk_bf16_f32 %0, %1, %2" : "=v"(r) : "v"(lo), "v"(hi)); return r; }
; __device__ __forceinline__ float shx(float v, int o, int lane) { return __builtin_bit_cast(float, __builtin_amdgcn_ds_bpermute((lane ^ o) << 2, __builtin_bit_cast(int, v))); }
;     __device__ __forceinline__ void operator()(AccRef acc, const Unit& u, int wr, int wc, int, int) const {
;     ...
;                     if (xin32) { x0 = *(const f32x4*)(xin32 + p); x1 = *(const f32x4*)(xin32 + p + 4); }
;                     else { const v4u h = *(const v4u*)(xb + p), lo = *(const v4u*)(xl + p);
;                         x0 = (f32x4){bflo(h.x) + bflo(lo.x), bfhi(h.x) + bfhi(lo.x), bflo(h.y) + bflo(lo.y), bfhi(h.y) + bfhi(lo.y)};
;                         x1 = (f32x4){bflo(h.z) + bflo(lo.z), bfhi(h.z) + bfhi(lo.z), bflo(h.w) + bflo(lo.w), bfhi(h.w) + bfhi(lo.w)}; }
;                     x0 = x0 + alpha * acc[ai][bj][m][0]; x1 = x1 + alpha * acc[ai][bj][m][1];
;                     if (PROBE_ON) { x0 = x0 * pscale; x1 = x1 * pscale; if (p == 0) x0[0] += pspike; }
;                     if (xout32) { *(f32x4*)(xout32 + p) = x0; *(f32x4*)(xout32 + p + 4) = x1; }
;                     else {
;                         v4u w; w.x = cvt_pk_bf16(x0[0], x0[1]); w.y = cvt_pk_bf16(x0[2], x0[3]); w.z = cvt_pk_bf16(x1[0], x1[1]); w.w = cvt_pk_bf16(x1[2], x1[3]);
;                         *(v4u*)(xb + p) = w;
;                         const f32x4 r0 = {x0[0] - bflo(w.x), x0[1] - bfhi(w.x), x0[2] - bflo(w.y), x0[3] - bfhi(w.y)}, r1 = {x1[0] - bflo(w.z), x1[1] - bfhi(w.z), x1[2] - bflo(w.w), x1[3] - bfhi(w.w)};
;                         v4u q; q.x = cvt_pk_bf16(r0[0], r0[1]); q.y = cvt_pk_bf16(r0[2], r0[3]); q.z = cvt_pk_bf16(r1[0], r1[1]); q.w = cvt_pk_bf16(r1[2], r1[3]);
;                         *(v4u*)(xl + p) = q;
;                     }
;                     s += (x0[0] * x0[0] + x0[1] * x0[1]) + (x0[2] * x0[2] + x0[3] * x0[3]) + (x1[0] * x1[0] + x1[1] * x1[1]) + (x1[2] * x1[2] + x1[3] * x1[3]);
;                 }
;                 s += shx(s, 16, ln_); s += shx(s, 32, ln_);
;                 if (fq == 0) ss[(size_t)row * 32 + u.pn * 4 + wc] = s;
.LBB0_289:
	s_waitcnt vmcnt(0)
	v_pk_fma_f32 v[6:7], v[6:7], 0.5, v[12:13] op_sel_hi:[1,0,1]
	v_pk_fma_f32 v[4:5], v[4:5], 0.5, v[10:11] op_sel_hi:[1,0,1]
	v_pk_fma_f32 v[12:13], v[0:1], 0.5, v[14:15] op_sel_hi:[1,0,1]
	v_cvt_pk_bf16_f32 v0, v4, v5
	v_cvt_pk_bf16_f32 v1, v6, v7
	v_pk_fma_f32 v[10:11], v[2:3], 0.5, v[16:17] op_sel_hi:[1,0,1]
	v_cvt_pk_bf16_f32 v2, v12, v13
	v_lshlrev_b32_e32 v15, 16, v1
	v_cvt_pk_bf16_f32 v3, v10, v11
	global_store_dwordx4 v[30:31], v[0:3], off offset:256 sc1
	v_lshlrev_b32_e32 v14, 16, v0
	v_sub_f32_e32 v14, v4, v14
	v_and_b32_e32 v1, 0xffff0000, v1
	v_sub_f32_e32 v16, v7, v1
	v_lshlrev_b32_e32 v1, 16, v2
	v_sub_f32_e32 v17, v12, v1
	v_and_b32_e32 v1, 0xffff0000, v2
	v_mul_f32_e32 v2, v4, v4
	v_mul_f32_e32 v4, v6, v6
	v_fmac_f32_e32 v2, v5, v5
	v_fmac_f32_e32 v4, v7, v7
	v_mul_f32_e32 v24, v34, v34
	v_mul_f32_e32 v20, v20, v20
	v_add_f32_e32 v2, v4, v2
	v_mul_f32_e32 v4, v12, v12
	v_fmac_f32_e32 v24, v35, v35
	v_fmac_f32_e32 v20, v21, v21
	v_mul_f32_e32 v21, v22, v22
	v_fmac_f32_e32 v4, v13, v13
	v_add_f32_e32 v20, v20, v24
	v_fmac_f32_e32 v21, v23, v23
	v_mul_f32_e32 v19, v19, v19
	v_add_f32_e32 v2, v4, v2
	v_mul_f32_e32 v4, v11, v11
	v_add_f32_e32 v20, v21, v20
	v_fmac_f32_e32 v19, v18, v18
	v_fmac_f32_e32 v4, v10, v10
	v_add_f32_e32 v18, v19, v20
	v_add_f32_e32 v2, v4, v2
	v_and_b32_e32 v0, 0xffff0000, v0
	v_add_f32_e32 v4, v18, v2
	v_sub_f32_e32 v0, v5, v0
	ds_bpermute_b32 v5, v133, v4
	v_sub_f32_e32 v19, v13, v1
	v_lshlrev_b32_e32 v1, 16, v3
	v_sub_f32_e32 v15, v6, v15
	v_sub_f32_e32 v6, v10, v1
	v_and_b32_e32 v1, 0xffff0000, v3
	v_cvt_pk_bf16_f32 v2, v14, v0
	s_waitcnt lgkmcnt(0)
	v_add_f32_e32 v0, v4, v5
	v_sub_f32_e32 v7, v11, v1
	ds_bpermute_b32 v1, v132, v0
	v_cvt_pk_bf16_f32 v3, v15, v16
	v_cvt_pk_bf16_f32 v4, v17, v19
	v_cvt_pk_bf16_f32 v5, v6, v7
	global_store_dwordx4 v[28:29], v[2:5], off offset:256 sc1
	s_and_saveexec_b64 s[6:7], s[8:9]
	s_cbranch_execz .LBB0_291
	v_lshlrev_b64 v[2:3], 7, v[26:27]
	v_lshl_add_u64 v[2:3], s[16:17], 0, v[2:3]
	v_lshl_add_u64 v[2:3], s[26:27], 2, v[2:3]
	s_lshl_b32 s96, s43, 2
	v_lshl_add_u64 v[2:3], v[2:3], 0, s[96:97]
	s_waitcnt lgkmcnt(0)
	v_add_f32_e32 v0, v0, v1
	global_store_dword v[2:3], v0, off

; __device__ __forceinline__ unsigned cvt_pk_bf16(float lo, float hi) { unsigned r; asm volatile("v_cvt_pk_bf16_f32 %0, %1, %2" : "=v"(r) : "v"(lo), "v"(hi)); return r; }
;     __device__ __forceinline__ void operator()(AccMut acc, const Unit& u, int wr, int wc, int, int) const {
;     ...
;                     f32x4 x0 = acc[ai][bj][m][0], x1 = acc[ai][bj][m][1];
;                     x0 = (f32x4){x0[0] * sc[0], x0[1] * sc[1], x0[2] * sc[2], x0[3] * sc[3]}; x1 = (f32x4){x1[0] * sc[4], x1[1] * sc[5], x1[2] * sc[6], x1[3] * sc[7]};
;                     if (u.seg < 2) { acc[ai][bj][m][0] = x0; acc[ai][bj][m][1] = x1; }
;                     else { v4u w; w.x = cvt_pk_bf16(x0[0], x0[1]); w.y = cvt_pk_bf16(x0[2], x0[3]); w.z = cvt_pk_bf16(x1[0], x1[1]); w.w = cvt_pk_bf16(x1[2], x1[3]); *(v4u*)(MGB + (size_t)row * D + col) = w; }
.LBB0_918:
	v_ashrrev_i32_e32 v155, 31, v154
	v_lshlrev_b64 v[152:153], 12, v[154:155]
	v_lshl_add_u64 v[152:153], s[10:11], 0, v[152:153]
	v_pk_mul_f32 v[0:1], v[134:135], v[0:1]
	v_pk_mul_f32 v[2:3], v[136:137], v[2:3]
	v_pk_mul_f32 v[4:5], v[130:131], v[4:5]
	v_pk_mul_f32 v[6:7], v[132:133], v[6:7]
	s_and_b64 vcc, exec, s[22:23]
	v_lshl_add_u64 v[158:159], v[150:151], 1, v[152:153]
	s_cbranch_vccz .LBB0_920
	v_cvt_pk_bf16_f32 v0, v0, v1
	v_cvt_pk_bf16_f32 v1, v2, v3
	v_cvt_pk_bf16_f32 v2, v4, v5
	v_cvt_pk_bf16_f32 v3, v6, v7
	global_store_dwordx4 v[158:159], v[0:3], off sc1
	s_branch .LBB0_921

; __device__ __forceinline__ unsigned cvt_pk_bf16(float lo, float hi) { unsigned r; asm volatile("v_cvt_pk_bf16_f32 %0, %1, %2" : "=v"(r) : "v"(lo), "v"(hi)); return r; }
;     __device__ __forceinline__ void operator()(AccMut acc, const Unit& u, int wr, int wc, int, int) const {
;     ...
;                     f32x4 x0 = acc[ai][bj][m][0], x1 = acc[ai][bj][m][1];
;                     x0 = (f32x4){x0[0] * sc[0], x0[1] * sc[1], x0[2] * sc[2], x0[3] * sc[3]}; x1 = (f32x4){x1[0] * sc[4], x1[1] * sc[5], x1[2] * sc[6], x1[3] * sc[7]};
;                     if (u.seg < 2) { acc[ai][bj][m][0] = x0; acc[ai][bj][m][1] = x1; }
;                     else { v4u w; w.x = cvt_pk_bf16(x0[0], x0[1]); w.y = cvt_pk_bf16(x0[2], x0[3]); w.z = cvt_pk_bf16(x1[0], x1[1]); w.w = cvt_pk_bf16(x1[2], x1[3]); *(v4u*)(MGB + (size_t)row * D + col) = w; }
.LBB0_925:
	s_nop 0
	v_pk_mul_f32 v[0:1], v[102:103], v[0:1]
	v_pk_mul_f32 v[2:3], v[104:105], v[2:3]
	v_pk_mul_f32 v[4:5], v[98:99], v[4:5]
	s_and_b64 vcc, exec, s[6:7]
	v_pk_mul_f32 v[6:7], v[100:101], v[6:7]
	s_cbranch_vccnz .LBB0_927
	s_mov_b64 s[22:23], 0
	v_cvt_pk_bf16_f32 v0, v0, v1
	v_cvt_pk_bf16_f32 v1, v2, v3
	v_cvt_pk_bf16_f32 v2, v4, v5
	v_cvt_pk_bf16_f32 v3, v6, v7
	global_store_dwordx4 v[158:159], v[0:3], off offset:256 sc1
	s_branch .LBB0_928

; __device__ __forceinline__ unsigned cvt_pk_bf16(float lo, float hi) { unsigned r; asm volatile("v_cvt_pk_bf16_f32 %0, %1, %2" : "=v"(r) : "v"(lo), "v"(hi)); return r; }
;     __device__ __forceinline__ void operator()(AccMut acc, const Unit& u, int wr, int wc, int, int) const {
;     ...
;                     f32x4 x0 = acc[ai][bj][m][0], x1 = acc[ai][bj][m][1];
;                     x0 = (f32x4){x0[0] * sc[0], x0[1] * sc[1], x0[2] * sc[2], x0[3] * sc[3]}; x1 = (f32x4){x1[0] * sc[4], x1[1] * sc[5], x1[2] * sc[6], x1[3] * sc[7]};
;                     if (u.seg < 2) { acc[ai][bj][m][0] = x0; acc[ai][bj][m][1] = x1; }
;                     else { v4u w; w.x = cvt_pk_bf16(x0[0], x0[1]); w.y = cvt_pk_bf16(x0[2], x0[3]); w.z = cvt_pk_bf16(x1[0], x1[1]); w.w = cvt_pk_bf16(x1[2], x1[3]); *(v4u*)(MGB + (size_t)row * D + col) = w; }
.LBB0_932:
	v_ashrrev_i32_e32 v159, 31, v158
	v_lshlrev_b64 v[158:159], 12, v[158:159]
	v_lshl_add_u64 v[158:159], s[10:11], 0, v[158:159]
	v_pk_mul_f32 v[0:1], v[126:127], v[0:1]
	v_pk_mul_f32 v[2:3], v[128:129], v[2:3]
	v_pk_mul_f32 v[4:5], v[122:123], v[4:5]
	v_pk_mul_f32 v[6:7], v[124:125], v[6:7]
	s_and_b64 vcc, exec, s[6:7]
	v_lshl_add_u64 v[158:159], v[150:151], 1, v[158:159]
	s_cbranch_vccnz .LBB0_934
	s_mov_b64 s[22:23], 0
	v_cvt_pk_bf16_f32 v0, v0, v1
	v_cvt_pk_bf16_f32 v1, v2, v3
	v_cvt_pk_bf16_f32 v2, v4, v5
	v_cvt_pk_bf16_f32 v3, v6, v7
	global_store_dwordx4 v[158:159], v[0:3], off sc1
	s_andn2_b64 vcc, exec, s[22:23]
	s_and_b64 vcc, exec, s[6:7]
	s_mov_b64 s[2:3], -1
	s_cbranch_vccnz .LBB0_936
	s_branch .LBB0_935

; __device__ __forceinline__ unsigned cvt_pk_bf16(float lo, float hi) { unsigned r; asm volatile("v_cvt_pk_bf16_f32 %0, %1, %2" : "=v"(r) : "v"(lo), "v"(hi)); return r; }
;     __device__ __forceinline__ void operator()(AccMut acc, const Unit& u, int wr, int wc, int, int) const {
;     ...
;                     f32x4 x0 = acc[ai][bj][m][0], x1 = acc[ai][bj][m][1];
;                     x0 = (f32x4){x0[0] * sc[0], x0[1] * sc[1], x0[2] * sc[2], x0[3] * sc[3]}; x1 = (f32x4){x1[0] * sc[4], x1[1] * sc[5], x1[2] * sc[6], x1[3] * sc[7]};
;                     if (u.seg < 2) { acc[ai][bj][m][0] = x0; acc[ai][bj][m][1] = x1; }
;                     else { v4u w; w.x = cvt_pk_bf16(x0[0], x0[1]); w.y = cvt_pk_bf16(x0[2], x0[3]); w.z = cvt_pk_bf16(x1[0], x1[1]); w.w = cvt_pk_bf16(x1[2], x1[3]); *(v4u*)(MGB + (size_t)row * D + col) = w; }
.LBB0_938:
	s_nop 0
	v_pk_mul_f32 v[0:1], v[94:95], v[0:1]
	v_pk_mul_f32 v[2:3], v[96:97], v[2:3]
	v_pk_mul_f32 v[4:5], v[90:91], v[4:5]
	s_and_b64 vcc, exec, s[6:7]
	v_pk_mul_f32 v[6:7], v[92:93], v[6:7]
	s_cbranch_vccnz .LBB0_940
	s_mov_b64 s[22:23], 0
	v_cvt_pk_bf16_f32 v0, v0, v1
	v_cvt_pk_bf16_f32 v1, v2, v3
	v_cvt_pk_bf16_f32 v2, v4, v5
	v_cvt_pk_bf16_f32 v3, v6, v7
	global_store_dwordx4 v[158:159], v[0:3], off offset:256 sc1
	s_branch .LBB0_941

; __device__ __forceinline__ unsigned cvt_pk_bf16(float lo, float hi) { unsigned r; asm volatile("v_cvt_pk_bf16_f32 %0, %1, %2" : "=v"(r) : "v"(lo), "v"(hi)); return r; }
;     __device__ __forceinline__ void operator()(AccMut acc, const Unit& u, int wr, int wc, int, int) const {
;     ...
;                     f32x4 x0 = acc[ai][bj][m][0], x1 = acc[ai][bj][m][1];
;                     x0 = (f32x4){x0[0] * sc[0], x0[1] * sc[1], x0[2] * sc[2], x0[3] * sc[3]}; x1 = (f32x4){x1[0] * sc[4], x1[1] * sc[5], x1[2] * sc[6], x1[3] * sc[7]};
;                     if (u.seg < 2) { acc[ai][bj][m][0] = x0; acc[ai][bj][m][1] = x1; }
;                     else { v4u w; w.x = cvt_pk_bf16(x0[0], x0[1]); w.y = cvt_pk_bf16(x0[2], x0[3]); w.z = cvt_pk_bf16(x1[0], x1[1]); w.w = cvt_pk_bf16(x1[2], x1[3]); *(v4u*)(MGB + (size_t)row * D + col) = w; }
.LBB0_945:
	v_ashrrev_i32_e32 v159, 31, v158
	v_lshlrev_b64 v[158:159], 12, v[158:159]
	v_lshl_add_u64 v[158:159], s[10:11], 0, v[158:159]
	v_pk_mul_f32 v[0:1], v[118:119], v[0:1]
	v_pk_mul_f32 v[2:3], v[120:121], v[2:3]
	v_pk_mul_f32 v[4:5], v[114:115], v[4:5]
	v_pk_mul_f32 v[6:7], v[116:117], v[6:7]
	s_and_b64 vcc, exec, s[6:7]
	v_lshl_add_u64 v[158:159], v[150:151], 1, v[158:159]
	s_cbranch_vccnz .LBB0_947
	s_mov_b64 s[22:23], 0
	v_cvt_pk_bf16_f32 v0, v0, v1
	v_cvt_pk_bf16_f32 v1, v2, v3
	v_cvt_pk_bf16_f32 v2, v4, v5
	v_cvt_pk_bf16_f32 v3, v6, v7
	global_store_dwordx4 v[158:159], v[0:3], off sc1
	s_andn2_b64 vcc, exec, s[22:23]
	s_and_b64 vcc, exec, s[6:7]
	s_mov_b64 s[2:3], -1
	s_cbranch_vccnz .LBB0_949
	s_branch .LBB0_948

; __device__ __forceinline__ unsigned cvt_pk_bf16(float lo, float hi) { unsigned r; asm volatile("v_cvt_pk_bf16_f32 %0, %1, %2" : "=v"(r) : "v"(lo), "v"(hi)); return r; }
;     __device__ __forceinline__ void operator()(AccMut acc, const Unit& u, int wr, int wc, int, int) const {
;     ...
;                     f32x4 x0 = acc[ai][bj][m][0], x1 = acc[ai][bj][m][1];
;                     x0 = (f32x4){x0[0] * sc[0], x0[1] * sc[1], x0[2] * sc[2], x0[3] * sc[3]}; x1 = (f32x4){x1[0] * sc[4], x1[1] * sc[5], x1[2] * sc[6], x1[3] * sc[7]};
;                     if (u.seg < 2) { acc[ai][bj][m][0] = x0; acc[ai][bj][m][1] = x1; }
;                     else { v4u w; w.x = cvt_pk_bf16(x0[0], x0[1]); w.y = cvt_pk_bf16(x0[2], x0[3]); w.z = cvt_pk_bf16(x1[0], x1[1]); w.w = cvt_pk_bf16(x1[2], x1[3]); *(v4u*)(MGB + (size_t)row * D + col) = w; }
.LBB0_951:
	s_nop 0
	v_pk_mul_f32 v[0:1], v[86:87], v[0:1]
	v_pk_mul_f32 v[2:3], v[88:89], v[2:3]
	v_pk_mul_f32 v[4:5], v[82:83], v[4:5]
	s_and_b64 vcc, exec, s[6:7]
	v_pk_mul_f32 v[6:7], v[84:85], v[6:7]
	s_cbranch_vccnz .LBB0_953
	s_mov_b64 s[22:23], 0
	v_cvt_pk_bf16_f32 v0, v0, v1
	v_cvt_pk_bf16_f32 v1, v2, v3
	v_cvt_pk_bf16_f32 v2, v4, v5
	v_cvt_pk_bf16_f32 v3, v6, v7
	global_store_dwordx4 v[158:159], v[0:3], off offset:256 sc1
	s_branch .LBB0_954

; __device__ __forceinline__ unsigned cvt_pk_bf16(float lo, float hi) { unsigned r; asm volatile("v_cvt_pk_bf16_f32 %0, %1, %2" : "=v"(r) : "v"(lo), "v"(hi)); return r; }
;     __device__ __forceinline__ void operator()(AccMut acc, const Unit& u, int wr, int wc, int, int) const {
;     ...
;                     f32x4 x0 = acc[ai][bj][m][0], x1 = acc[ai][bj][m][1];
;                     x0 = (f32x4){x0[0] * sc[0], x0[1] * sc[1], x0[2] * sc[2], x0[3] * sc[3]}; x1 = (f32x4){x1[0] * sc[4], x1[1] * sc[5], x1[2] * sc[6], x1[3] * sc[7]};
;                     if (u.seg < 2) { acc[ai][bj][m][0] = x0; acc[ai][bj][m][1] = x1; }
;                     else { v4u w; w.x = cvt_pk_bf16(x0[0], x0[1]); w.y = cvt_pk_bf16(x0[2], x0[3]); w.z = cvt_pk_bf16(x1[0], x1[1]); w.w = cvt_pk_bf16(x1[2], x1[3]); *(v4u*)(MGB + (size_t)row * D + col) = w; }
.LBB0_958:
	v_ashrrev_i32_e32 v159, 31, v158
	v_lshlrev_b64 v[158:159], 12, v[158:159]
	v_lshl_add_u64 v[158:159], s[10:11], 0, v[158:159]
	v_pk_mul_f32 v[0:1], v[110:111], v[0:1]
	v_pk_mul_f32 v[2:3], v[112:113], v[2:3]
	v_pk_mul_f32 v[4:5], v[106:107], v[4:5]
	v_pk_mul_f32 v[6:7], v[108:109], v[6:7]
	s_and_b64 vcc, exec, s[6:7]
	v_lshl_add_u64 v[158:159], v[150:151], 1, v[158:159]
	s_cbranch_vccnz .LBB0_960
	s_mov_b64 s[22:23], 0
	v_cvt_pk_bf16_f32 v0, v0, v1
	v_cvt_pk_bf16_f32 v1, v2, v3
	v_cvt_pk_bf16_f32 v2, v4, v5
	v_cvt_pk_bf16_f32 v3, v6, v7
	global_store_dwordx4 v[158:159], v[0:3], off sc1
	s_andn2_b64 vcc, exec, s[22:23]
	s_and_b64 vcc, exec, s[6:7]
	s_mov_b64 s[2:3], -1
	s_cbranch_vccnz .LBB0_962
	s_branch .LBB0_961

; __device__ __forceinline__ unsigned cvt_pk_bf16(float lo, float hi) { unsigned r; asm volatile("v_cvt_pk_bf16_f32 %0, %1, %2" : "=v"(r) : "v"(lo), "v"(hi)); return r; }
;     __device__ __forceinline__ void operator()(AccMut acc, const Unit& u, int wr, int wc, int, int) const {
;     ...
;                     f32x4 x0 = acc[ai][bj][m][0], x1 = acc[ai][bj][m][1];
;                     x0 = (f32x4){x0[0] * sc[0], x0[1] * sc[1], x0[2] * sc[2], x0[3] * sc[3]}; x1 = (f32x4){x1[0] * sc[4], x1[1] * sc[5], x1[2] * sc[6], x1[3] * sc[7]};
;                     if (u.seg < 2) { acc[ai][bj][m][0] = x0; acc[ai][bj][m][1] = x1; }
;                     else { v4u w; w.x = cvt_pk_bf16(x0[0], x0[1]); w.y = cvt_pk_bf16(x0[2], x0[3]); w.z = cvt_pk_bf16(x1[0], x1[1]); w.w = cvt_pk_bf16(x1[2], x1[3]); *(v4u*)(MGB + (size_t)row * D + col) = w; }
.LBB0_964:
	s_nop 0
	v_pk_mul_f32 v[0:1], v[78:79], v[0:1]
	v_pk_mul_f32 v[2:3], v[80:81], v[2:3]
	v_pk_mul_f32 v[4:5], v[74:75], v[4:5]
	s_and_b64 vcc, exec, s[6:7]
	v_pk_mul_f32 v[6:7], v[76:77], v[6:7]
	s_cbranch_vccnz .LBB0_966
	s_mov_b64 s[22:23], 0
	v_cvt_pk_bf16_f32 v0, v0, v1
	v_cvt_pk_bf16_f32 v1, v2, v3
	v_cvt_pk_bf16_f32 v2, v4, v5
	v_cvt_pk_bf16_f32 v3, v6, v7
	global_store_dwordx4 v[158:159], v[0:3], off offset:256 sc1
	s_branch .LBB0_967

; __device__ __forceinline__ unsigned cvt_pk_bf16(float lo, float hi) { unsigned r; asm volatile("v_cvt_pk_bf16_f32 %0, %1, %2" : "=v"(r) : "v"(lo), "v"(hi)); return r; }
;     __device__ __forceinline__ void operator()(AccMut acc, const Unit& u, int wr, int wc, int, int) const {
;     ...
;                     f32x4 x0 = acc[ai][bj][m][0], x1 = acc[ai][bj][m][1];
;                     x0 = (f32x4){x0[0] * sc[0], x0[1] * sc[1], x0[2] * sc[2], x0[3] * sc[3]}; x1 = (f32x4){x1[0] * sc[4], x1[1] * sc[5], x1[2] * sc[6], x1[3] * sc[7]};
;                     if (u.seg < 2) { acc[ai][bj][m][0] = x0; acc[ai][bj][m][1] = x1; }
;                     else { v4u w; w.x = cvt_pk_bf16(x0[0], x0[1]); w.y = cvt_pk_bf16(x0[2], x0[3]); w.z = cvt_pk_bf16(x1[0], x1[1]); w.w = cvt_pk_bf16(x1[2], x1[3]); *(v4u*)(MGB + (size_t)row * D + col) = w; }
.LBB0_971:
	v_ashrrev_i32_e32 v159, 31, v158
	v_lshlrev_b64 v[158:159], 12, v[158:159]
	v_lshl_add_u64 v[158:159], s[10:11], 0, v[158:159]
	v_pk_mul_f32 v[0:1], v[70:71], v[0:1]
	v_pk_mul_f32 v[2:3], v[72:73], v[2:3]
	v_pk_mul_f32 v[4:5], v[66:67], v[4:5]
	v_pk_mul_f32 v[6:7], v[68:69], v[6:7]
	s_and_b64 vcc, exec, s[6:7]
	v_lshl_add_u64 v[158:159], v[150:151], 1, v[158:159]
	s_cbranch_vccnz .LBB0_973
	s_mov_b64 s[22:23], 0
	v_cvt_pk_bf16_f32 v0, v0, v1
	v_cvt_pk_bf16_f32 v1, v2, v3
	v_cvt_pk_bf16_f32 v2, v4, v5
	v_cvt_pk_bf16_f32 v3, v6, v7
	global_store_dwordx4 v[158:159], v[0:3], off sc1
	s_andn2_b64 vcc, exec, s[22:23]
	s_and_b64 vcc, exec, s[6:7]
	s_mov_b64 s[2:3], -1
	s_cbranch_vccnz .LBB0_975
	s_branch .LBB0_974

; __device__ __forceinline__ unsigned cvt_pk_bf16(float lo, float hi) { unsigned r; asm volatile("v_cvt_pk_bf16_f32 %0, %1, %2" : "=v"(r) : "v"(lo), "v"(hi)); return r; }
;     __device__ __forceinline__ void operator()(AccMut acc, const Unit& u, int wr, int wc, int, int) const {
;     ...
;                     f32x4 x0 = acc[ai][bj][m][0], x1 = acc[ai][bj][m][1];
;                     x0 = (f32x4){x0[0] * sc[0], x0[1] * sc[1], x0[2] * sc[2], x0[3] * sc[3]}; x1 = (f32x4){x1[0] * sc[4], x1[1] * sc[5], x1[2] * sc[6], x1[3] * sc[7]};
;                     if (u.seg < 2) { acc[ai][bj][m][0] = x0; acc[ai][bj][m][1] = x1; }
;                     else { v4u w; w.x = cvt_pk_bf16(x0[0], x0[1]); w.y = cvt_pk_bf16(x0[2], x0[3]); w.z = cvt_pk_bf16(x1[0], x1[1]); w.w = cvt_pk_bf16(x1[2], x1[3]); *(v4u*)(MGB + (size_t)row * D + col) = w; }
.LBB0_977:
	s_nop 0
	v_pk_mul_f32 v[0:1], v[38:39], v[0:1]
	v_pk_mul_f32 v[2:3], v[40:41], v[2:3]
	v_pk_mul_f32 v[4:5], v[34:35], v[4:5]
	s_and_b64 vcc, exec, s[6:7]
	v_pk_mul_f32 v[6:7], v[36:37], v[6:7]
	s_cbranch_vccnz .LBB0_979
	s_mov_b64 s[22:23], 0
	v_cvt_pk_bf16_f32 v0, v0, v1
	v_cvt_pk_bf16_f32 v1, v2, v3
	v_cvt_pk_bf16_f32 v2, v4, v5
	v_cvt_pk_bf16_f32 v3, v6, v7
	global_store_dwordx4 v[158:159], v[0:3], off offset:256 sc1
	s_branch .LBB0_980

; __device__ __forceinline__ unsigned cvt_pk_bf16(float lo, float hi) { unsigned r; asm volatile("v_cvt_pk_bf16_f32 %0, %1, %2" : "=v"(r) : "v"(lo), "v"(hi)); return r; }
;     __device__ __forceinline__ void operator()(AccMut acc, const Unit& u, int wr, int wc, int, int) const {
;     ...
;                     f32x4 x0 = acc[ai][bj][m][0], x1 = acc[ai][bj][m][1];
;                     x0 = (f32x4){x0[0] * sc[0], x0[1] * sc[1], x0[2] * sc[2], x0[3] * sc[3]}; x1 = (f32x4){x1[0] * sc[4], x1[1] * sc[5], x1[2] * sc[6], x1[3] * sc[7]};
;                     if (u.seg < 2) { acc[ai][bj][m][0] = x0; acc[ai][bj][m][1] = x1; }
;                     else { v4u w; w.x = cvt_pk_bf16(x0[0], x0[1]); w.y = cvt_pk_bf16(x0[2], x0[3]); w.z = cvt_pk_bf16(x1[0], x1[1]); w.w = cvt_pk_bf16(x1[2], x1[3]); *(v4u*)(MGB + (size_t)row * D + col) = w; }
.LBB0_984:
	v_ashrrev_i32_e32 v159, 31, v158
	v_lshlrev_b64 v[158:159], 12, v[158:159]
	v_lshl_add_u64 v[158:159], s[10:11], 0, v[158:159]
	v_pk_mul_f32 v[0:1], v[62:63], v[0:1]
	v_pk_mul_f32 v[2:3], v[64:65], v[2:3]
	v_pk_mul_f32 v[4:5], v[58:59], v[4:5]
	v_pk_mul_f32 v[6:7], v[60:61], v[6:7]
	s_and_b64 vcc, exec, s[6:7]
	v_lshl_add_u64 v[158:159], v[150:151], 1, v[158:159]
	s_cbranch_vccnz .LBB0_986
	s_mov_b64 s[22:23], 0
	v_cvt_pk_bf16_f32 v0, v0, v1
	v_cvt_pk_bf16_f32 v1, v2, v3
	v_cvt_pk_bf16_f32 v2, v4, v5
	v_cvt_pk_bf16_f32 v3, v6, v7
	global_store_dwordx4 v[158:159], v[0:3], off sc1
	s_andn2_b64 vcc, exec, s[22:23]
	s_and_b64 vcc, exec, s[6:7]
	s_mov_b64 s[2:3], -1
	s_cbranch_vccnz .LBB0_988
	s_branch .LBB0_987

; __device__ __forceinline__ unsigned cvt_pk_bf16(float lo, float hi) { unsigned r; asm volatile("v_cvt_pk_bf16_f32 %0, %1, %2" : "=v"(r) : "v"(lo), "v"(hi)); return r; }
;     __device__ __forceinline__ void operator()(AccMut acc, const Unit& u, int wr, int wc, int, int) const {
;     ...
;                     f32x4 x0 = acc[ai][bj][m][0], x1 = acc[ai][bj][m][1];
;                     x0 = (f32x4){x0[0] * sc[0], x0[1] * sc[1], x0[2] * sc[2], x0[3] * sc[3]}; x1 = (f32x4){x1[0] * sc[4], x1[1] * sc[5], x1[2] * sc[6], x1[3] * sc[7]};
;                     if (u.seg < 2) { acc[ai][bj][m][0] = x0; acc[ai][bj][m][1] = x1; }
;                     else { v4u w; w.x = cvt_pk_bf16(x0[0], x0[1]); w.y = cvt_pk_bf16(x0[2], x0[3]); w.z = cvt_pk_bf16(x1[0], x1[1]); w.w = cvt_pk_bf16(x1[2], x1[3]); *(v4u*)(MGB + (size_t)row * D + col) = w; }
.LBB0_990:
	s_nop 0
	v_pk_mul_f32 v[0:1], v[30:31], v[0:1]
	v_pk_mul_f32 v[2:3], v[32:33], v[2:3]
	v_pk_mul_f32 v[4:5], v[26:27], v[4:5]
	s_and_b64 vcc, exec, s[6:7]
	v_pk_mul_f32 v[6:7], v[28:29], v[6:7]
	s_cbranch_vccnz .LBB0_992
	s_mov_b64 s[22:23], 0
	v_cvt_pk_bf16_f32 v0, v0, v1
	v_cvt_pk_bf16_f32 v1, v2, v3
	v_cvt_pk_bf16_f32 v2, v4, v5
	v_cvt_pk_bf16_f32 v3, v6, v7
	global_store_dwordx4 v[158:159], v[0:3], off offset:256 sc1
	s_branch .LBB0_993

; __device__ __forceinline__ unsigned cvt_pk_bf16(float lo, float hi) { unsigned r; asm volatile("v_cvt_pk_bf16_f32 %0, %1, %2" : "=v"(r) : "v"(lo), "v"(hi)); return r; }
;     __device__ __forceinline__ void operator()(AccMut acc, const Unit& u, int wr, int wc, int, int) const {
;     ...
;                     f32x4 x0 = acc[ai][bj][m][0], x1 = acc[ai][bj][m][1];
;                     x0 = (f32x4){x0[0] * sc[0], x0[1] * sc[1], x0[2] * sc[2], x0[3] * sc[3]}; x1 = (f32x4){x1[0] * sc[4], x1[1] * sc[5], x1[2] * sc[6], x1[3] * sc[7]};
;                     if (u.seg < 2) { acc[ai][bj][m][0] = x0; acc[ai][bj][m][1] = x1; }
;                     else { v4u w; w.x = cvt_pk_bf16(x0[0], x0[1]); w.y = cvt_pk_bf16(x0[2], x0[3]); w.z = cvt_pk_bf16(x1[0], x1[1]); w.w = cvt_pk_bf16(x1[2], x1[3]); *(v4u*)(MGB + (size_t)row * D + col) = w; }
.LBB0_997:
	v_ashrrev_i32_e32 v159, 31, v158
	v_lshlrev_b64 v[158:159], 12, v[158:159]
	v_lshl_add_u64 v[158:159], s[10:11], 0, v[158:159]
	v_pk_mul_f32 v[0:1], v[54:55], v[0:1]
	v_pk_mul_f32 v[2:3], v[56:57], v[2:3]
	v_pk_mul_f32 v[4:5], v[50:51], v[4:5]
	v_pk_mul_f32 v[6:7], v[52:53], v[6:7]
	s_and_b64 vcc, exec, s[6:7]
	v_lshl_add_u64 v[158:159], v[150:151], 1, v[158:159]
	s_cbranch_vccnz .LBB0_999
	s_mov_b64 s[22:23], 0
	v_cvt_pk_bf16_f32 v0, v0, v1
	v_cvt_pk_bf16_f32 v1, v2, v3
	v_cvt_pk_bf16_f32 v2, v4, v5
	v_cvt_pk_bf16_f32 v3, v6, v7
	global_store_dwordx4 v[158:159], v[0:3], off sc1
	s_andn2_b64 vcc, exec, s[22:23]
	s_and_b64 vcc, exec, s[6:7]
	s_mov_b64 s[2:3], -1
	s_cbranch_vccnz .LBB0_1001
	s_branch .LBB0_1000

; __device__ __forceinline__ unsigned cvt_pk_bf16(float lo, float hi) { unsigned r; asm volatile("v_cvt_pk_bf16_f32 %0, %1, %2" : "=v"(r) : "v"(lo), "v"(hi)); return r; }
;     __device__ __forceinline__ void operator()(AccMut acc, const Unit& u, int wr, int wc, int, int) const {
;     ...
;                     f32x4 x0 = acc[ai][bj][m][0], x1 = acc[ai][bj][m][1];
;                     x0 = (f32x4){x0[0] * sc[0], x0[1] * sc[1], x0[2] * sc[2], x0[3] * sc[3]}; x1 = (f32x4){x1[0] * sc[4], x1[1] * sc[5], x1[2] * sc[6], x1[3] * sc[7]};
;                     if (u.seg < 2) { acc[ai][bj][m][0] = x0; acc[ai][bj][m][1] = x1; }
;                     else { v4u w; w.x = cvt_pk_bf16(x0[0], x0[1]); w.y = cvt_pk_bf16(x0[2], x0[3]); w.z = cvt_pk_bf16(x1[0], x1[1]); w.w = cvt_pk_bf16(x1[2], x1[3]); *(v4u*)(MGB + (size_t)row * D + col) = w; }
.LBB0_1003:
	s_nop 0
	v_pk_mul_f32 v[0:1], v[22:23], v[0:1]
	v_pk_mul_f32 v[2:3], v[24:25], v[2:3]
	v_pk_mul_f32 v[4:5], v[18:19], v[4:5]
	s_and_b64 vcc, exec, s[6:7]
	v_pk_mul_f32 v[6:7], v[20:21], v[6:7]
	s_cbranch_vccnz .LBB0_1005
	s_mov_b64 s[22:23], 0
	v_cvt_pk_bf16_f32 v0, v0, v1
	v_cvt_pk_bf16_f32 v1, v2, v3
	v_cvt_pk_bf16_f32 v2, v4, v5
	v_cvt_pk_bf16_f32 v3, v6, v7
	global_store_dwordx4 v[158:159], v[0:3], off offset:256 sc1
	s_branch .LBB0_1006

; __device__ __forceinline__ unsigned cvt_pk_bf16(float lo, float hi) { unsigned r; asm volatile("v_cvt_pk_bf16_f32 %0, %1, %2" : "=v"(r) : "v"(lo), "v"(hi)); return r; }
;     __device__ __forceinline__ void operator()(AccMut acc, const Unit& u, int wr, int wc, int, int) const {
;     ...
;                     f32x4 x0 = acc[ai][bj][m][0], x1 = acc[ai][bj][m][1];
;                     x0 = (f32x4){x0[0] * sc[0], x0[1] * sc[1], x0[2] * sc[2], x0[3] * sc[3]}; x1 = (f32x4){x1[0] * sc[4], x1[1] * sc[5], x1[2] * sc[6], x1[3] * sc[7]};
;                     if (u.seg < 2) { acc[ai][bj][m][0] = x0; acc[ai][bj][m][1] = x1; }
;                     else { v4u w; w.x = cvt_pk_bf16(x0[0], x0[1]); w.y = cvt_pk_bf16(x0[2], x0[3]); w.z = cvt_pk_bf16(x1[0], x1[1]); w.w = cvt_pk_bf16(x1[2], x1[3]); *(v4u*)(MGB + (size_t)row * D + col) = w; }
.LBB0_1010:
	v_ashrrev_i32_e32 v157, 31, v156
	v_lshlrev_b64 v[156:157], 12, v[156:157]
	v_lshl_add_u64 v[156:157], s[10:11], 0, v[156:157]
	v_pk_mul_f32 v[0:1], v[46:47], v[0:1]
	v_pk_mul_f32 v[2:3], v[48:49], v[2:3]
	v_pk_mul_f32 v[4:5], v[42:43], v[4:5]
	v_pk_mul_f32 v[6:7], v[44:45], v[6:7]
	s_and_b64 vcc, exec, s[6:7]
	v_lshl_add_u64 v[150:151], v[150:151], 1, v[156:157]
	s_cbranch_vccnz .LBB0_1012
	s_mov_b64 s[22:23], 0
	v_cvt_pk_bf16_f32 v0, v0, v1
	v_cvt_pk_bf16_f32 v1, v2, v3
	v_cvt_pk_bf16_f32 v2, v4, v5
	v_cvt_pk_bf16_f32 v3, v6, v7
	global_store_dwordx4 v[150:151], v[0:3], off sc1
	s_andn2_b64 vcc, exec, s[22:23]
	s_and_b64 vcc, exec, s[6:7]
	s_mov_b64 s[2:3], -1
	s_cbranch_vccnz .LBB0_1014
	s_branch .LBB0_1013

; __device__ __forceinline__ unsigned cvt_pk_bf16(float lo, float hi) { unsigned r; asm volatile("v_cvt_pk_bf16_f32 %0, %1, %2" : "=v"(r) : "v"(lo), "v"(hi)); return r; }
;     __device__ __forceinline__ void operator()(AccMut acc, const Unit& u, int wr, int wc, int, int) const {
;     ...
;                     f32x4 x0 = acc[ai][bj][m][0], x1 = acc[ai][bj][m][1];
;                     x0 = (f32x4){x0[0] * sc[0], x0[1] * sc[1], x0[2] * sc[2], x0[3] * sc[3]}; x1 = (f32x4){x1[0] * sc[4], x1[1] * sc[5], x1[2] * sc[6], x1[3] * sc[7]};
;                     if (u.seg < 2) { acc[ai][bj][m][0] = x0; acc[ai][bj][m][1] = x1; }
;                     else { v4u w; w.x = cvt_pk_bf16(x0[0], x0[1]); w.y = cvt_pk_bf16(x0[2], x0[3]); w.z = cvt_pk_bf16(x1[0], x1[1]); w.w = cvt_pk_bf16(x1[2], x1[3]); *(v4u*)(MGB + (size_t)row * D + col) = w; }
.LBB0_1016:
	s_nop 0
	v_pk_mul_f32 v[0:1], v[14:15], v[0:1]
	v_pk_mul_f32 v[2:3], v[16:17], v[2:3]
	v_pk_mul_f32 v[4:5], v[10:11], v[4:5]
	s_and_b64 vcc, exec, s[6:7]
	v_pk_mul_f32 v[6:7], v[12:13], v[6:7]
	s_cbranch_vccnz .LBB0_1018
	s_mov_b64 s[22:23], 0
	v_cvt_pk_bf16_f32 v0, v0, v1
	v_cvt_pk_bf16_f32 v1, v2, v3
	v_cvt_pk_bf16_f32 v2, v4, v5
	v_cvt_pk_bf16_f32 v3, v6, v7
	global_store_dwordx4 v[150:151], v[0:3], off offset:256 sc1
	s_branch .LBB0_1019

;     __device__ __forceinline__ void operator()(AccRef acc, const Unit& u, int wr, int wc, int, int) const {
;         const int ln_ = fresh_lane(), fr = ln_ & 15, fq = ln_ >> 4;
;         const int row0 = u.pm * 256 + wr * 64 + fr, col0 = u.pn * 256 + wc * 32 + 8 * fq;
; #pragma unroll
;         for (int ai = 0; ai < 2; ++ai)
; #pragma unroll
;             for (int m = 0; m < 4; ++m) {
;                 const int row = row0 + ai * 128 + m * 16; float s = 0.f;
; #pragma unroll
;                 for (int bj = 0; bj < 2; ++bj) {
;                     const size_t p = (size_t)row * D + col0 + bj * 128;
;                     f32x4 x0, x1;
;                     if (xin32) { x0 = *(const f32x4*)(xin32 + p); x1 = *(const f32x4*)(xin32 + p + 4); }
;                     else { const v4u h = *(const v4u*)(xb + p), lo = *(const v4u*)(xl + p);
;                         x0 = (f32x4){bflo(h.x) + bflo(lo.x), bfhi(h.x) + bfhi(lo.x), bflo(h.y) + bflo(lo.y), bfhi(h.y) + bfhi(lo.y)};
;                         x1 = (f32x4){bflo(h.z) + bflo(lo.z), bfhi(h.z) + bfhi(lo.z), bflo(h.w) + bflo(lo.w), bfhi(h.w) + bfhi(lo.w)}; }
;                     x0 = x0 + alpha * acc[ai][bj][m][0]; x1 = x1 + alpha * acc[ai][bj][m][1];
;                     if (PROBE_ON) { x0 = x0 * pscale; x1 = x1 * pscale; if (p == 0) x0[0] += pspike; }
;                     if (xout32) { *(f32x4*)(xout32 + p) = x0; *(f32x4*)(xout32 + p + 4) = x1; }
;                     else {
;                         v4u w; w.x = cvt_pk_bf16(x0[0], x0[1]); w.y = cvt_pk_bf16(x0[2], x0[3]); w.z = cvt_pk_bf16(x1[0], x1[1]); w.w = cvt_pk_bf16(x1[2], x1[3]);
;                         *(v4u*)(xb + p) = w;
;                         const f32x4 r0 = {x0[0] - bflo(w.x), x0[1] - bfhi(w.x), x0[2] - bflo(w.y), x0[3] - bfhi(w.y)}, r1 = {x1[0] - bflo(w.z), x1[1] - bfhi(w.z), x1[2] - bflo(w.w), x1[3] - bfhi(w.w)};
;                         v4u q; q.x = cvt_pk_bf16(r0[0], r0[1]); q.y = cvt_pk_bf16(r0[2], r0[3]); q.z = cvt_pk_bf16(r1[0], r1[1]); q.w = cvt_pk_bf16(r1[2], r1[3]);
;                         *(v4u*)(xl + p) = q;
;                     }
;                     s += (x0[0] * x0[0] + x0[1] * x0[1]) + (x0[2] * x0[2] + x0[3] * x0[3]) + (x1[0] * x1[0] + x1[1] * x1[1]) + (x1[2] * x1[2] + x1[3] * x1[3]);
;                 }
;                 s += shx(s, 16, ln_); s += shx(s, 32, ln_);
.LBB0_1081:
	s_lshl_b32 s2, s24, 8
	s_add_i32 s2, s2, s47
	v_mbcnt_lo_u32_b32 v143, -1, 0
	v_mbcnt_hi_u32_b32 v143, -1, v143
	s_nop 0
	v_and_or_b32 v142, v143, 15, s2
	s_lshl_b32 s2, s22, 8
	v_ashrrev_i32_e32 v140, 1, v143
	s_or_b32 s2, s2, s48
	v_and_b32_e32 v140, -8, v140
	v_add_u32_e32 v140, s2, v140
	v_lshlrev_b32_e32 v144, 2, v143
	v_cmp_gt_u32_e32 vcc, 16, v143
	v_ashrrev_i32_e32 v143, 31, v142
	v_ashrrev_i32_e32 v141, 31, v140
	v_xor_b32_e32 v151, 64, v144
	v_xor_b32_e32 v150, 0x80, v144
	v_lshlrev_b64 v[144:145], 11, v[142:143]
	v_lshl_add_u64 v[144:145], v[144:145], 0, v[140:141]
	v_lshlrev_b64 v[144:145], 1, v[144:145]
	v_lshl_add_u64 v[146:147], s[6:7], 0, v[144:145]
	v_lshl_add_u64 v[144:145], s[8:9], 0, v[144:145]
	global_load_dwordx4 v[152:155], v[146:147], off
	global_load_dwordx4 v[156:159], v[144:145], off
	s_lshl_b32 s22, s22, 2
	s_ashr_i32 s23, s22, 31
	s_waitcnt vmcnt(0)
	v_lshlrev_b32_e32 v160, 16, v152
	v_and_b32_e32 v161, 0xffff0000, v152
	v_lshlrev_b32_e32 v162, 16, v156
	v_and_b32_e32 v163, 0xffff0000, v156
	v_lshlrev_b32_e32 v152, 16, v153
	v_and_b32_e32 v153, 0xffff0000, v153
	v_lshlrev_b32_e32 v156, 16, v157
	v_and_b32_e32 v157, 0xffff0000, v157
	v_pk_add_f32 v[160:161], v[160:161], v[162:163]
	v_pk_add_f32 v[152:153], v[152:153], v[156:157]
	v_lshlrev_b32_e32 v156, 16, v154
	v_and_b32_e32 v157, 0xffff0000, v154
	v_lshlrev_b32_e32 v162, 16, v158
	v_and_b32_e32 v163, 0xffff0000, v158
	v_lshlrev_b32_e32 v154, 16, v155
	v_and_b32_e32 v155, 0xffff0000, v155
	v_lshlrev_b32_e32 v158, 16, v159
	v_and_b32_e32 v159, 0xffff0000, v159
	v_pk_add_f32 v[156:157], v[156:157], v[162:163]
	v_pk_add_f32 v[154:155], v[154:155], v[158:159]
	v_pk_add_f32 v[128:129], v[128:129], v[152:153]
	v_pk_add_f32 v[126:127], v[126:127], v[160:161]
	v_pk_add_f32 v[152:153], v[124:125], v[154:155]
	v_pk_add_f32 v[154:155], v[122:123], v[156:157]
	v_cvt_pk_bf16_f32 v122, v126, v127
	v_cvt_pk_bf16_f32 v123, v128, v129
	s_nop 0
	v_cvt_pk_bf16_f32 v124, v154, v155
	v_cvt_pk_bf16_f32 v125, v152, v153
	global_store_dwordx4 v[146:147], v[122:125], off sc1
	v_lshlrev_b32_e32 v156, 16, v122
	v_lshlrev_b32_e32 v157, 16, v123
	v_and_b32_e32 v122, 0xffff0000, v122
	v_and_b32_e32 v123, 0xffff0000, v123
	v_sub_f32_e32 v122, v127, v122
	v_sub_f32_e32 v123, v129, v123
	v_lshlrev_b32_e32 v158, 16, v124
	v_and_b32_e32 v124, 0xffff0000, v124
	v_lshlrev_b32_e32 v159, 16, v125
	v_and_b32_e32 v125, 0xffff0000, v125
	v_sub_f32_e32 v156, v126, v156
	v_sub_f32_e32 v157, v128, v157
	v_sub_f32_e32 v124, v155, v124
	v_sub_f32_e32 v125, v153, v125
	v_cvt_pk_bf16_f32 v122, v156, v122
	v_cvt_pk_bf16_f32 v123, v157, v123
	v_sub_f32_e32 v158, v154, v158
	v_sub_f32_e32 v159, v152, v159
	v_cvt_pk_bf16_f32 v124, v158, v124
	v_cvt_pk_bf16_f32 v125, v159, v125
	global_store_dwordx4 v[144:145], v[122:125], off sc1
	s_nop 1
	v_mul_f32_e32 v122, v126, v126
	v_mul_f32_e32 v123, v128, v128
	v_fmac_f32_e32 v122, v127, v127
	v_fmac_f32_e32 v123, v129, v129
	v_add_f32_e32 v122, v123, v122
	v_mul_f32_e32 v123, v154, v154
	v_fmac_f32_e32 v123, v155, v155
	v_add_f32_e32 v122, v123, v122
	v_mul_f32_e32 v123, v153, v153
	v_fmac_f32_e32 v123, v152, v152
	v_add_f32_e32 v156, v123, v122
	global_load_dwordx4 v[122:125], v[146:147], off offset:256
	global_load_dwordx4 v[126:129], v[144:145], off offset:256
	s_waitcnt vmcnt(1)
	v_lshlrev_b32_e32 v152, 16, v122
	v_and_b32_e32 v153, 0xffff0000, v122
	s_waitcnt vmcnt(0)
	v_lshlrev_b32_e32 v154, 16, v126
	v_and_b32_e32 v155, 0xffff0000, v126
	v_lshlrev_b32_e32 v122, 16, v123
	v_and_b32_e32 v123, 0xffff0000, v123
	v_lshlrev_b32_e32 v126, 16, v127
	v_and_b32_e32 v127, 0xffff0000, v127
	v_pk_add_f32 v[152:153], v[152:153], v[154:155]
	v_pk_add_f32 v[122:123], v[122:123], v[126:127]
	v_lshlrev_b32_e32 v126, 16, v124
	v_and_b32_e32 v127, 0xffff0000, v124
	v_lshlrev_b32_e32 v154, 16, v128
	v_and_b32_e32 v155, 0xffff0000, v128
	v_lshlrev_b32_e32 v124, 16, v125
	v_and_b32_e32 v125, 0xffff0000, v125
	v_lshlrev_b32_e32 v128, 16, v129
	v_and_b32_e32 v129, 0xffff0000, v129
	v_pk_add_f32 v[126:127], v[126:127], v[154:155]
	v_pk_add_f32 v[124:125], v[124:125], v[128:129]
	v_pk_add_f32 v[120:121], v[120:121], v[122:123]
	v_pk_add_f32 v[118:119], v[118:119], v[152:153]
	v_pk_add_f32 v[122:123], v[116:117], v[124:125]
	v_pk_add_f32 v[124:125], v[114:115], v[126:127]
	v_cvt_pk_bf16_f32 v114, v118, v119
	v_cvt_pk_bf16_f32 v115, v120, v121
	s_nop 0
	v_cvt_pk_bf16_f32 v116, v124, v125
	v_cvt_pk_bf16_f32 v117, v122, v123
	global_store_dwordx4 v[146:147], v[114:117], off offset:256 sc1
	v_lshlrev_b32_e32 v126, 16, v114
	v_lshlrev_b32_e32 v127, 16, v115
	v_and_b32_e32 v114, 0xffff0000, v114
	v_and_b32_e32 v115, 0xffff0000, v115
	v_sub_f32_e32 v114, v119, v114
	v_sub_f32_e32 v115, v121, v115
	v_lshlrev_b32_e32 v128, 16, v116
	v_and_b32_e32 v116, 0xffff0000, v116
	v_lshlrev_b32_e32 v129, 16, v117
	v_and_b32_e32 v117, 0xffff0000, v117
	v_sub_f32_e32 v126, v118, v126
	v_sub_f32_e32 v127, v120, v127
	v_sub_f32_e32 v116, v125, v116
	v_sub_f32_e32 v117, v123, v117
	v_cvt_pk_bf16_f32 v114, v126, v114
	v_cvt_pk_bf16_f32 v115, v127, v115
	v_sub_f32_e32 v128, v124, v128
	v_sub_f32_e32 v129, v122, v129
	v_cvt_pk_bf16_f32 v116, v128, v116
	v_cvt_pk_bf16_f32 v117, v129, v117
	global_store_dwordx4 v[144:145], v[114:117], off offset:256 sc1
	s_nop 1
	v_mul_f32_e32 v114, v118, v118
	v_mul_f32_e32 v115, v120, v120
	v_fmac_f32_e32 v114, v119, v119
	v_fmac_f32_e32 v115, v121, v121
	v_add_f32_e32 v114, v115, v114
	v_mul_f32_e32 v115, v124, v124
	v_fmac_f32_e32 v115, v125, v125
	v_add_f32_e32 v114, v115, v114
	v_mul_f32_e32 v115, v123, v123
	v_fmac_f32_e32 v115, v122, v122
	v_add_f32_e32 v114, v115, v114
	v_add_f32_e32 v114, v156, v114
	ds_bpermute_b32 v115, v151, v114
	s_waitcnt lgkmcnt(0)
	v_add_f32_e32 v114, v114, v115
	ds_bpermute_b32 v115, v150, v114
	s_and_saveexec_b64 s[24:25], vcc
	s_cbranch_execz .LBB0_1083
	v_lshlrev_b64 v[116:117], 7, v[142:143]
	v_lshl_add_u64 v[116:117], s[10:11], 0, v[116:117]
	v_lshl_add_u64 v[116:117], s[22:23], 2, v[116:117]
	s_lshl_b32 s96, s46, 2
	v_lshl_add_u64 v[116:117], v[116:117], 0, s[96:97]
	s_waitcnt lgkmcnt(0)
	v_add_f32_e32 v114, v114, v115
	global_store_dword v[116:117], v114, off
; __device__ __forceinline__ unsigned cvt_pk_bf16(float lo, float hi) { unsigned r; asm volatile("v_cvt_pk_bf16_f32 %0, %1, %2" : "=v"(r) : "v"(lo), "v"(hi)); return r; }
;     __device__ __forceinline__ void operator()(AccRef acc, const Unit& u, int wr, int wc, int, int) const {
;     ...
;                 const int row = row0 + ai * 128 + m * 16; float s = 0.f;
; #pragma unroll
;                 for (int bj = 0; bj < 2; ++bj) {
;                     const size_t p = (size_t)row * D + col0 + bj * 128;
;                     f32x4 x0, x1;
;                     if (xin32) { x0 = *(const f32x4*)(xin32 + p); x1 = *(const f32x4*)(xin32 + p + 4); }
;                     else { const v4u h = *(const v4u*)(xb + p), lo = *(const v4u*)(xl + p);
;                         x0 = (f32x4){bflo(h.x) + bflo(lo.x), bfhi(h.x) + bfhi(lo.x), bflo(h.y) + bflo(lo.y), bfhi(h.y) + bfhi(lo.y)};
;                         x1 = (f32x4){bflo(h.z) + bflo(lo.z), bfhi(h.z) + bfhi(lo.z), bflo(h.w) + bflo(lo.w), bfhi(h.w) + bfhi(lo.w)}; }
;                     x0 = x0 + alpha * acc[ai][bj][m][0]; x1 = x1 + alpha * acc[ai][bj][m][1];
;                     if (PROBE_ON) { x0 = x0 * pscale; x1 = x1 * pscale; if (p == 0) x0[0] += pspike; }
;                     if (xout32) { *(f32x4*)(xout32 + p) = x0; *(f32x4*)(xout32 + p + 4) = x1; }
;                     else {
;                         v4u w; w.x = cvt_pk_bf16(x0[0], x0[1]); w.y = cvt_pk_bf16(x0[2], x0[3]); w.z = cvt_pk_bf16(x1[0], x1[1]); w.w = cvt_pk_bf16(x1[2], x1[3]);
;                         *(v4u*)(xb + p) = w;
;                         const f32x4 r0 = {x0[0] - bflo(w.x), x0[1] - bfhi(w.x), x0[2] - bflo(w.y), x0[3] - bfhi(w.y)}, r1 = {x1[0] - bflo(w.z), x1[1] - bfhi(w.z), x1[2] - bflo(w.w), x1[3] - bfhi(w.w)};
;                         v4u q; q.x = cvt_pk_bf16(r0[0], r0[1]); q.y = cvt_pk_bf16(r0[2], r0[3]); q.z = cvt_pk_bf16(r1[0], r1[1]); q.w = cvt_pk_bf16(r1[2], r1[3]);
;                         *(v4u*)(xl + p) = q;
;                     }
;                     s += (x0[0] * x0[0] + x0[1] * x0[1]) + (x0[2] * x0[2] + x0[3] * x0[3]) + (x1[0] * x1[0] + x1[1] * x1[1]) + (x1[2] * x1[2] + x1[3] * x1[3]);
;                 }
;                 s += shx(s, 16, ln_); s += shx(s, 32, ln_);
;                 if (fq == 0) ss[(size_t)row * 32 + u.pn * 4 + wc] = s;
.LBB0_1083:
	s_or_b64 exec, exec, s[24:25]
	v_or_b32_e32 v114, 16, v142
	s_waitcnt lgkmcnt(0)
	v_ashrrev_i32_e32 v115, 31, v114
	v_lshlrev_b64 v[116:117], 11, v[114:115]
	v_lshl_add_u64 v[116:117], v[116:117], 0, v[140:141]
	v_lshlrev_b64 v[116:117], 1, v[116:117]
	v_lshl_add_u64 v[118:119], s[6:7], 0, v[116:117]
	v_lshl_add_u64 v[116:117], s[8:9], 0, v[116:117]
	global_load_dwordx4 v[120:123], v[118:119], off
	global_load_dwordx4 v[124:127], v[116:117], off
	s_waitcnt vmcnt(1)
	v_lshlrev_b32_e32 v128, 16, v120
	v_and_b32_e32 v129, 0xffff0000, v120
	s_waitcnt vmcnt(0)
	v_lshlrev_b32_e32 v144, 16, v124
	v_and_b32_e32 v145, 0xffff0000, v124
	v_lshlrev_b32_e32 v120, 16, v121
	v_and_b32_e32 v121, 0xffff0000, v121
	v_lshlrev_b32_e32 v124, 16, v125
	v_and_b32_e32 v125, 0xffff0000, v125
	v_pk_add_f32 v[128:129], v[128:129], v[144:145]
	v_pk_add_f32 v[120:121], v[120:121], v[124:125]
	v_lshlrev_b32_e32 v124, 16, v122
	v_and_b32_e32 v125, 0xffff0000, v122
	v_lshlrev_b32_e32 v144, 16, v126
	v_and_b32_e32 v145, 0xffff0000, v126
	v_lshlrev_b32_e32 v122, 16, v123
	v_and_b32_e32 v123, 0xffff0000, v123
	v_lshlrev_b32_e32 v126, 16, v127
	v_and_b32_e32 v127, 0xffff0000, v127
	v_pk_add_f32 v[124:125], v[124:125], v[144:145]
	v_pk_add_f32 v[122:123], v[122:123], v[126:127]
	v_pk_add_f32 v[112:113], v[112:113], v[120:121]
	v_pk_add_f32 v[110:111], v[110:111], v[128:129]
	v_pk_add_f32 v[120:121], v[108:109], v[122:123]
	v_pk_add_f32 v[122:123], v[106:107], v[124:125]
	v_cvt_pk_bf16_f32 v106, v110, v111
	v_cvt_pk_bf16_f32 v107, v112, v113
	s_nop 0
	v_cvt_pk_bf16_f32 v108, v122, v123
	v_cvt_pk_bf16_f32 v109, v120, v121
	global_store_dwordx4 v[118:119], v[106:109], off sc1
	v_lshlrev_b32_e32 v124, 16, v106
	v_lshlrev_b32_e32 v125, 16, v107
	v_and_b32_e32 v106, 0xffff0000, v106
	v_and_b32_e32 v107, 0xffff0000, v107
	v_sub_f32_e32 v106, v111, v106
	v_sub_f32_e32 v107, v113, v107
	v_lshlrev_b32_e32 v126, 16, v108
	v_and_b32_e32 v108, 0xffff0000, v108
	v_lshlrev_b32_e32 v127, 16, v109
	v_and_b32_e32 v109, 0xffff0000, v109
	v_sub_f32_e32 v124, v110, v124
	v_sub_f32_e32 v125, v112, v125
	v_sub_f32_e32 v108, v123, v108
	v_sub_f32_e32 v109, v121, v109
	v_cvt_pk_bf16_f32 v106, v124, v106
	v_cvt_pk_bf16_f32 v107, v125, v107
	v_sub_f32_e32 v126, v122, v126
	v_sub_f32_e32 v127, v120, v127
	v_cvt_pk_bf16_f32 v108, v126, v108
	v_cvt_pk_bf16_f32 v109, v127, v109
	global_store_dwordx4 v[116:117], v[106:109], off sc1
	s_nop 1
	v_mul_f32_e32 v106, v110, v110
	v_mul_f32_e32 v107, v112, v112
	v_fmac_f32_e32 v106, v111, v111
	v_fmac_f32_e32 v107, v113, v113
	v_add_f32_e32 v106, v107, v106
	v_mul_f32_e32 v107, v122, v122
	v_fmac_f32_e32 v107, v123, v123
	v_add_f32_e32 v106, v107, v106
	v_mul_f32_e32 v107, v121, v121
	v_fmac_f32_e32 v107, v120, v120
	v_add_f32_e32 v124, v107, v106
	global_load_dwordx4 v[106:109], v[118:119], off offset:256
	global_load_dwordx4 v[110:113], v[116:117], off offset:256
	s_waitcnt vmcnt(1)
	v_lshlrev_b32_e32 v120, 16, v106
	v_and_b32_e32 v121, 0xffff0000, v106
	s_waitcnt vmcnt(0)
	v_lshlrev_b32_e32 v122, 16, v110
	v_and_b32_e32 v123, 0xffff0000, v110
	v_lshlrev_b32_e32 v106, 16, v107
	v_and_b32_e32 v107, 0xffff0000, v107
	v_lshlrev_b32_e32 v110, 16, v111
	v_and_b32_e32 v111, 0xffff0000, v111
	v_pk_add_f32 v[120:121], v[120:121], v[122:123]
	v_pk_add_f32 v[106:107], v[106:107], v[110:111]
	v_lshlrev_b32_e32 v110, 16, v108
	v_and_b32_e32 v111, 0xffff0000, v108
	v_lshlrev_b32_e32 v122, 16, v112
	v_and_b32_e32 v123, 0xffff0000, v112
	v_lshlrev_b32_e32 v108, 16, v109
	v_and_b32_e32 v109, 0xffff0000, v109
	v_lshlrev_b32_e32 v112, 16, v113
	v_and_b32_e32 v113, 0xffff0000, v113
	v_pk_add_f32 v[110:111], v[110:111], v[122:123]
	v_pk_add_f32 v[108:109], v[108:109], v[112:113]
	v_pk_add_f32 v[104:105], v[104:105], v[106:107]
	v_pk_add_f32 v[102:103], v[102:103], v[120:121]
	v_pk_add_f32 v[106:107], v[100:101], v[108:109]
	v_pk_add_f32 v[108:109], v[98:99], v[110:111]
	v_cvt_pk_bf16_f32 v98, v102, v103
	v_cvt_pk_bf16_f32 v99, v104, v105
	s_nop 0
	v_cvt_pk_bf16_f32 v100, v108, v109
	v_cvt_pk_bf16_f32 v101, v106, v107
	global_store_dwordx4 v[118:119], v[98:101], off offset:256 sc1
	v_lshlrev_b32_e32 v110, 16, v98
	v_lshlrev_b32_e32 v111, 16, v99
	v_and_b32_e32 v98, 0xffff0000, v98
	v_and_b32_e32 v99, 0xffff0000, v99
	v_sub_f32_e32 v98, v103, v98
	v_sub_f32_e32 v99, v105, v99
	v_lshlrev_b32_e32 v112, 16, v100
	v_and_b32_e32 v100, 0xffff0000, v100
	v_lshlrev_b32_e32 v113, 16, v101
	v_and_b32_e32 v101, 0xffff0000, v101
	v_sub_f32_e32 v110, v102, v110
	v_sub_f32_e32 v111, v104, v111
	v_sub_f32_e32 v100, v109, v100
	v_sub_f32_e32 v101, v107, v101
	v_cvt_pk_bf16_f32 v98, v110, v98
	v_cvt_pk_bf16_f32 v99, v111, v99
	v_sub_f32_e32 v112, v108, v112
	v_sub_f32_e32 v113, v106, v113
	v_cvt_pk_bf16_f32 v100, v112, v100
	v_cvt_pk_bf16_f32 v101, v113, v101
	global_store_dwordx4 v[116:117], v[98:101], off offset:256 sc1
	s_nop 1
	v_mul_f32_e32 v98, v102, v102
	v_mul_f32_e32 v99, v104, v104
	v_fmac_f32_e32 v98, v103, v103
	v_fmac_f32_e32 v99, v105, v105
	v_add_f32_e32 v98, v99, v98
	v_mul_f32_e32 v99, v108, v108
	v_fmac_f32_e32 v99, v109, v109
	v_add_f32_e32 v98, v99, v98
	v_mul_f32_e32 v99, v107, v107
	v_fmac_f32_e32 v99, v106, v106
	v_add_f32_e32 v98, v99, v98
	v_add_f32_e32 v98, v124, v98
	ds_bpermute_b32 v99, v151, v98
	s_waitcnt lgkmcnt(0)
	v_add_f32_e32 v98, v98, v99
	ds_bpermute_b32 v99, v150, v98
	s_and_saveexec_b64 s[24:25], vcc
	s_cbranch_execz .LBB0_1085
	v_lshlrev_b64 v[100:101], 7, v[114:115]
	v_lshl_add_u64 v[100:101], s[10:11], 0, v[100:101]
	v_lshl_add_u64 v[100:101], s[22:23], 2, v[100:101]
	s_lshl_b32 s96, s46, 2
	v_lshl_add_u64 v[100:101], v[100:101], 0, s[96:97]
	s_waitcnt lgkmcnt(0)
	v_add_f32_e32 v98, v98, v99
	global_store_dword v[100:101], v98, off
; __device__ __forceinline__ unsigned cvt_pk_bf16(float lo, float hi) { unsigned r; asm volatile("v_cvt_pk_bf16_f32 %0, %1, %2" : "=v"(r) : "v"(lo), "v"(hi)); return r; }
;     __device__ __forceinline__ void operator()(AccRef acc, const Unit& u, int wr, int wc, int, int) const {
;     ...
;                 const int row = row0 + ai * 128 + m * 16; float s = 0.f;
; #pragma unroll
;                 for (int bj = 0; bj < 2; ++bj) {
;                     const size_t p = (size_t)row * D + col0 + bj * 128;
;                     f32x4 x0, x1;
;                     if (xin32) { x0 = *(const f32x4*)(xin32 + p); x1 = *(const f32x4*)(xin32 + p + 4); }
;                     else { const v4u h = *(const v4u*)(xb + p), lo = *(const v4u*)(xl + p);
;                         x0 = (f32x4){bflo(h.x) + bflo(lo.x), bfhi(h.x) + bfhi(lo.x), bflo(h.y) + bflo(lo.y), bfhi(h.y) + bfhi(lo.y)};
;                         x1 = (f32x4){bflo(h.z) + bflo(lo.z), bfhi(h.z) + bfhi(lo.z), bflo(h.w) + bflo(lo.w), bfhi(h.w) + bfhi(lo.w)}; }
;                     x0 = x0 + alpha * acc[ai][bj][m][0]; x1 = x1 + alpha * acc[ai][bj][m][1];
;                     if (PROBE_ON) { x0 = x0 * pscale; x1 = x1 * pscale; if (p == 0) x0[0] += pspike; }
;                     if (xout32) { *(f32x4*)(xout32 + p) = x0; *(f32x4*)(xout32 + p + 4) = x1; }
;                     else {
;                         v4u w; w.x = cvt_pk_bf16(x0[0], x0[1]); w.y = cvt_pk_bf16(x0[2], x0[3]); w.z = cvt_pk_bf16(x1[0], x1[1]); w.w = cvt_pk_bf16(x1[2], x1[3]);
;                         *(v4u*)(xb + p) = w;
;                         const f32x4 r0 = {x0[0] - bflo(w.x), x0[1] - bfhi(w.x), x0[2] - bflo(w.y), x0[3] - bfhi(w.y)}, r1 = {x1[0] - bflo(w.z), x1[1] - bfhi(w.z), x1[2] - bflo(w.w), x1[3] - bfhi(w.w)};
;                         v4u q; q.x = cvt_pk_bf16(r0[0], r0[1]); q.y = cvt_pk_bf16(r0[2], r0[3]); q.z = cvt_pk_bf16(r1[0], r1[1]); q.w = cvt_pk_bf16(r1[2], r1[3]);
;                         *(v4u*)(xl + p) = q;
;                     }
;                     s += (x0[0] * x0[0] + x0[1] * x0[1]) + (x0[2] * x0[2] + x0[3] * x0[3]) + (x1[0] * x1[0] + x1[1] * x1[1]) + (x1[2] * x1[2] + x1[3] * x1[3]);
;                 }
;                 s += shx(s, 16, ln_); s += shx(s, 32, ln_);
;                 if (fq == 0) ss[(size_t)row * 32 + u.pn * 4 + wc] = s;
.LBB0_1085:
	s_or_b64 exec, exec, s[24:25]
	v_or_b32_e32 v98, 32, v142
	s_waitcnt lgkmcnt(0)
	v_ashrrev_i32_e32 v99, 31, v98
	v_lshlrev_b64 v[100:101], 11, v[98:99]
	v_lshl_add_u64 v[100:101], v[100:101], 0, v[140:141]
	v_lshlrev_b64 v[100:101], 1, v[100:101]
	v_lshl_add_u64 v[102:103], s[6:7], 0, v[100:101]
	v_lshl_add_u64 v[100:101], s[8:9], 0, v[100:101]
	global_load_dwordx4 v[104:107], v[102:103], off
	global_load_dwordx4 v[108:111], v[100:101], off
	s_waitcnt vmcnt(1)
	v_lshlrev_b32_e32 v112, 16, v104
	v_and_b32_e32 v113, 0xffff0000, v104
	s_waitcnt vmcnt(0)
	v_lshlrev_b32_e32 v114, 16, v108
	v_and_b32_e32 v115, 0xffff0000, v108
	v_lshlrev_b32_e32 v104, 16, v105
	v_and_b32_e32 v105, 0xffff0000, v105
	v_lshlrev_b32_e32 v108, 16, v109
	v_and_b32_e32 v109, 0xffff0000, v109
	v_pk_add_f32 v[112:113], v[112:113], v[114:115]
	v_pk_add_f32 v[104:105], v[104:105], v[108:109]
	v_lshlrev_b32_e32 v108, 16, v106
	v_and_b32_e32 v109, 0xffff0000, v106
	v_lshlrev_b32_e32 v114, 16, v110
	v_and_b32_e32 v115, 0xffff0000, v110
	v_lshlrev_b32_e32 v106, 16, v107
	v_and_b32_e32 v107, 0xffff0000, v107
	v_lshlrev_b32_e32 v110, 16, v111
	v_and_b32_e32 v111, 0xffff0000, v111
	v_pk_add_f32 v[108:109], v[108:109], v[114:115]
	v_pk_add_f32 v[106:107], v[106:107], v[110:111]
	v_pk_add_f32 v[96:97], v[96:97], v[104:105]
	v_pk_add_f32 v[94:95], v[94:95], v[112:113]
	v_pk_add_f32 v[104:105], v[92:93], v[106:107]
	v_pk_add_f32 v[106:107], v[90:91], v[108:109]
	v_cvt_pk_bf16_f32 v90, v94, v95
	v_cvt_pk_bf16_f32 v91, v96, v97
	s_nop 0
	v_cvt_pk_bf16_f32 v92, v106, v107
	v_cvt_pk_bf16_f32 v93, v104, v105
	global_store_dwordx4 v[102:103], v[90:93], off sc1
	v_lshlrev_b32_e32 v108, 16, v90
	v_lshlrev_b32_e32 v109, 16, v91
	v_and_b32_e32 v90, 0xffff0000, v90
	v_and_b32_e32 v91, 0xffff0000, v91
	v_sub_f32_e32 v90, v95, v90
	v_sub_f32_e32 v91, v97, v91
	v_lshlrev_b32_e32 v110, 16, v92
	v_and_b32_e32 v92, 0xffff0000, v92
	v_lshlrev_b32_e32 v111, 16, v93
	v_and_b32_e32 v93, 0xffff0000, v93
	v_sub_f32_e32 v108, v94, v108
	v_sub_f32_e32 v109, v96, v109
	v_sub_f32_e32 v92, v107, v92
	v_sub_f32_e32 v93, v105, v93
	v_cvt_pk_bf16_f32 v90, v108, v90
	v_cvt_pk_bf16_f32 v91, v109, v91
	v_sub_f32_e32 v110, v106, v110
	v_sub_f32_e32 v111, v104, v111
	v_cvt_pk_bf16_f32 v92, v110, v92
	v_cvt_pk_bf16_f32 v93, v111, v93
	global_store_dwordx4 v[100:101], v[90:93], off sc1
	s_nop 1
	v_mul_f32_e32 v90, v94, v94
	v_mul_f32_e32 v91, v96, v96
	v_fmac_f32_e32 v90, v95, v95
	v_fmac_f32_e32 v91, v97, v97
	v_add_f32_e32 v90, v91, v90
	v_mul_f32_e32 v91, v106, v106
	v_fmac_f32_e32 v91, v107, v107
	v_add_f32_e32 v90, v91, v90
	v_mul_f32_e32 v91, v105, v105
	v_fmac_f32_e32 v91, v104, v104
	v_add_f32_e32 v108, v91, v90
	global_load_dwordx4 v[90:93], v[102:103], off offset:256
	global_load_dwordx4 v[94:97], v[100:101], off offset:256
	s_waitcnt vmcnt(1)
	v_lshlrev_b32_e32 v104, 16, v90
	v_and_b32_e32 v105, 0xffff0000, v90
	s_waitcnt vmcnt(0)
	v_lshlrev_b32_e32 v106, 16, v94
	v_and_b32_e32 v107, 0xffff0000, v94
	v_lshlrev_b32_e32 v90, 16, v91
	v_and_b32_e32 v91, 0xffff0000, v91
	v_lshlrev_b32_e32 v94, 16, v95
	v_and_b32_e32 v95, 0xffff0000, v95
	v_pk_add_f32 v[104:105], v[104:105], v[106:107]
	v_pk_add_f32 v[90:91], v[90:91], v[94:95]
	v_lshlrev_b32_e32 v94, 16, v92
	v_and_b32_e32 v95, 0xffff0000, v92
	v_lshlrev_b32_e32 v106, 16, v96
	v_and_b32_e32 v107, 0xffff0000, v96
	v_lshlrev_b32_e32 v92, 16, v93
	v_and_b32_e32 v93, 0xffff0000, v93
	v_lshlrev_b32_e32 v96, 16, v97
	v_and_b32_e32 v97, 0xffff0000, v97
	v_pk_add_f32 v[94:95], v[94:95], v[106:107]
	v_pk_add_f32 v[92:93], v[92:93], v[96:97]
	v_pk_add_f32 v[88:89], v[88:89], v[90:91]
	v_pk_add_f32 v[86:87], v[86:87], v[104:105]
	v_pk_add_f32 v[90:91], v[84:85], v[92:93]
	v_pk_add_f32 v[92:93], v[82:83], v[94:95]
	v_cvt_pk_bf16_f32 v82, v86, v87
	v_cvt_pk_bf16_f32 v83, v88, v89
	s_nop 0
	v_cvt_pk_bf16_f32 v84, v92, v93
	v_cvt_pk_bf16_f32 v85, v90, v91
	global_store_dwordx4 v[102:103], v[82:85], off offset:256 sc1
	v_lshlrev_b32_e32 v94, 16, v82
	v_lshlrev_b32_e32 v95, 16, v83
	v_and_b32_e32 v82, 0xffff0000, v82
	v_and_b32_e32 v83, 0xffff0000, v83
	v_sub_f32_e32 v82, v87, v82
	v_sub_f32_e32 v83, v89, v83
	v_lshlrev_b32_e32 v96, 16, v84
	v_and_b32_e32 v84, 0xffff0000, v84
	v_lshlrev_b32_e32 v97, 16, v85
	v_and_b32_e32 v85, 0xffff0000, v85
	v_sub_f32_e32 v94, v86, v94
	v_sub_f32_e32 v95, v88, v95
	v_sub_f32_e32 v84, v93, v84
	v_sub_f32_e32 v85, v91, v85
	v_cvt_pk_bf16_f32 v82, v94, v82
	v_cvt_pk_bf16_f32 v83, v95, v83
	v_sub_f32_e32 v96, v92, v96
	v_sub_f32_e32 v97, v90, v97
	v_cvt_pk_bf16_f32 v84, v96, v84
	v_cvt_pk_bf16_f32 v85, v97, v85
	global_store_dwordx4 v[100:101], v[82:85], off offset:256 sc1
	s_nop 1
	v_mul_f32_e32 v82, v86, v86
	v_mul_f32_e32 v83, v88, v88
	v_fmac_f32_e32 v82, v87, v87
	v_fmac_f32_e32 v83, v89, v89
	v_add_f32_e32 v82, v83, v82
	v_mul_f32_e32 v83, v92, v92
	v_fmac_f32_e32 v83, v93, v93
	v_add_f32_e32 v82, v83, v82
	v_mul_f32_e32 v83, v91, v91
	v_fmac_f32_e32 v83, v90, v90
	v_add_f32_e32 v82, v83, v82
	v_add_f32_e32 v82, v108, v82
	ds_bpermute_b32 v83, v151, v82
	s_waitcnt lgkmcnt(0)
	v_add_f32_e32 v82, v82, v83
	ds_bpermute_b32 v83, v150, v82
	s_and_saveexec_b64 s[24:25], vcc
	s_cbranch_execz .LBB0_1087
	v_lshlrev_b64 v[84:85], 7, v[98:99]
	v_lshl_add_u64 v[84:85], s[10:11], 0, v[84:85]
	v_lshl_add_u64 v[84:85], s[22:23], 2, v[84:85]
	s_lshl_b32 s96, s46, 2
	v_lshl_add_u64 v[84:85], v[84:85], 0, s[96:97]
	s_waitcnt lgkmcnt(0)
	v_add_f32_e32 v82, v82, v83
	global_store_dword v[84:85], v82, off
; __device__ __forceinline__ unsigned cvt_pk_bf16(float lo, float hi) { unsigned r; asm volatile("v_cvt_pk_bf16_f32 %0, %1, %2" : "=v"(r) : "v"(lo), "v"(hi)); return r; }
;     __device__ __forceinline__ void operator()(AccRef acc, const Unit& u, int wr, int wc, int, int) const {
;     ...
;                 const int row = row0 + ai * 128 + m * 16; float s = 0.f;
; #pragma unroll
;                 for (int bj = 0; bj < 2; ++bj) {
;                     const size_t p = (size_t)row * D + col0 + bj * 128;
;                     f32x4 x0, x1;
;                     if (xin32) { x0 = *(const f32x4*)(xin32 + p); x1 = *(const f32x4*)(xin32 + p + 4); }
;                     else { const v4u h = *(const v4u*)(xb + p), lo = *(const v4u*)(xl + p);
;                         x0 = (f32x4){bflo(h.x) + bflo(lo.x), bfhi(h.x) + bfhi(lo.x), bflo(h.y) + bflo(lo.y), bfhi(h.y) + bfhi(lo.y)};
;                         x1 = (f32x4){bflo(h.z) + bflo(lo.z), bfhi(h.z) + bfhi(lo.z), bflo(h.w) + bflo(lo.w), bfhi(h.w) + bfhi(lo.w)}; }
;                     x0 = x0 + alpha * acc[ai][bj][m][0]; x1 = x1 + alpha * acc[ai][bj][m][1];
;                     if (PROBE_ON) { x0 = x0 * pscale; x1 = x1 * pscale; if (p == 0) x0[0] += pspike; }
;                     if (xout32) { *(f32x4*)(xout32 + p) = x0; *(f32x4*)(xout32 + p + 4) = x1; }
;                     else {
;                         v4u w; w.x = cvt_pk_bf16(x0[0], x0[1]); w.y = cvt_pk_bf16(x0[2], x0[3]); w.z = cvt_pk_bf16(x1[0], x1[1]); w.w = cvt_pk_bf16(x1[2], x1[3]);
;                         *(v4u*)(xb + p) = w;
;                         const f32x4 r0 = {x0[0] - bflo(w.x), x0[1] - bfhi(w.x), x0[2] - bflo(w.y), x0[3] - bfhi(w.y)}, r1 = {x1[0] - bflo(w.z), x1[1] - bfhi(w.z), x1[2] - bflo(w.w), x1[3] - bfhi(w.w)};
;                         v4u q; q.x = cvt_pk_bf16(r0[0], r0[1]); q.y = cvt_pk_bf16(r0[2], r0[3]); q.z = cvt_pk_bf16(r1[0], r1[1]); q.w = cvt_pk_bf16(r1[2], r1[3]);
;                         *(v4u*)(xl + p) = q;
;                     }
;                     s += (x0[0] * x0[0] + x0[1] * x0[1]) + (x0[2] * x0[2] + x0[3] * x0[3]) + (x1[0] * x1[0] + x1[1] * x1[1]) + (x1[2] * x1[2] + x1[3] * x1[3]);
;                 }
;                 s += shx(s, 16, ln_); s += shx(s, 32, ln_);
;                 if (fq == 0) ss[(size_t)row * 32 + u.pn * 4 + wc] = s;
.LBB0_1087:
	s_or_b64 exec, exec, s[24:25]
	v_or_b32_e32 v82, 48, v142
	s_waitcnt lgkmcnt(0)
	v_ashrrev_i32_e32 v83, 31, v82
	v_lshlrev_b64 v[84:85], 11, v[82:83]
	v_lshl_add_u64 v[84:85], v[84:85], 0, v[140:141]
	v_lshlrev_b64 v[84:85], 1, v[84:85]
	v_lshl_add_u64 v[86:87], s[6:7], 0, v[84:85]
	v_lshl_add_u64 v[84:85], s[8:9], 0, v[84:85]
	global_load_dwordx4 v[88:91], v[86:87], off
	global_load_dwordx4 v[92:95], v[84:85], off
	s_waitcnt vmcnt(1)
	v_lshlrev_b32_e32 v96, 16, v88
	v_and_b32_e32 v97, 0xffff0000, v88
	s_waitcnt vmcnt(0)
	v_lshlrev_b32_e32 v98, 16, v92
	v_and_b32_e32 v99, 0xffff0000, v92
	v_lshlrev_b32_e32 v88, 16, v89
	v_and_b32_e32 v89, 0xffff0000, v89
	v_lshlrev_b32_e32 v92, 16, v93
	v_and_b32_e32 v93, 0xffff0000, v93
	v_pk_add_f32 v[96:97], v[96:97], v[98:99]
	v_pk_add_f32 v[88:89], v[88:89], v[92:93]
	v_lshlrev_b32_e32 v92, 16, v90
	v_and_b32_e32 v93, 0xffff0000, v90
	v_lshlrev_b32_e32 v98, 16, v94
	v_and_b32_e32 v99, 0xffff0000, v94
	v_lshlrev_b32_e32 v90, 16, v91
	v_and_b32_e32 v91, 0xffff0000, v91
	v_lshlrev_b32_e32 v94, 16, v95
	v_and_b32_e32 v95, 0xffff0000, v95
	v_pk_add_f32 v[92:93], v[92:93], v[98:99]
	v_pk_add_f32 v[90:91], v[90:91], v[94:95]
	v_pk_add_f32 v[80:81], v[80:81], v[88:89]
	v_pk_add_f32 v[78:79], v[78:79], v[96:97]
	v_pk_add_f32 v[88:89], v[76:77], v[90:91]
	v_pk_add_f32 v[90:91], v[74:75], v[92:93]
	v_cvt_pk_bf16_f32 v74, v78, v79
	v_cvt_pk_bf16_f32 v75, v80, v81
	s_nop 0
	v_cvt_pk_bf16_f32 v76, v90, v91
	v_cvt_pk_bf16_f32 v77, v88, v89
	global_store_dwordx4 v[86:87], v[74:77], off sc1
	v_lshlrev_b32_e32 v92, 16, v74
	v_lshlrev_b32_e32 v93, 16, v75
	v_and_b32_e32 v74, 0xffff0000, v74
	v_and_b32_e32 v75, 0xffff0000, v75
	v_sub_f32_e32 v74, v79, v74
	v_sub_f32_e32 v75, v81, v75
	v_lshlrev_b32_e32 v94, 16, v76
	v_and_b32_e32 v76, 0xffff0000, v76
	v_lshlrev_b32_e32 v95, 16, v77
	v_and_b32_e32 v77, 0xffff0000, v77
	v_sub_f32_e32 v92, v78, v92
	v_sub_f32_e32 v93, v80, v93
	v_sub_f32_e32 v76, v91, v76
	v_sub_f32_e32 v77, v89, v77
	v_cvt_pk_bf16_f32 v74, v92, v74
	v_cvt_pk_bf16_f32 v75, v93, v75
	v_sub_f32_e32 v94, v90, v94
	v_sub_f32_e32 v95, v88, v95
	v_cvt_pk_bf16_f32 v76, v94, v76
	v_cvt_pk_bf16_f32 v77, v95, v77
	global_store_dwordx4 v[84:85], v[74:77], off sc1
	s_nop 1
	v_mul_f32_e32 v74, v78, v78
	v_mul_f32_e32 v75, v80, v80
	v_fmac_f32_e32 v74, v79, v79
	v_fmac_f32_e32 v75, v81, v81
	v_add_f32_e32 v74, v75, v74
	v_mul_f32_e32 v75, v90, v90
	v_fmac_f32_e32 v75, v91, v91
	v_add_f32_e32 v74, v75, v74
	v_mul_f32_e32 v75, v89, v89
	v_fmac_f32_e32 v75, v88, v88
	v_add_f32_e32 v92, v75, v74
	global_load_dwordx4 v[74:77], v[86:87], off offset:256
	global_load_dwordx4 v[78:81], v[84:85], off offset:256
	s_waitcnt vmcnt(1)
	v_lshlrev_b32_e32 v88, 16, v74
	v_and_b32_e32 v89, 0xffff0000, v74
	s_waitcnt vmcnt(0)
	v_lshlrev_b32_e32 v90, 16, v78
	v_and_b32_e32 v91, 0xffff0000, v78
	v_lshlrev_b32_e32 v74, 16, v75
	v_and_b32_e32 v75, 0xffff0000, v75
	v_lshlrev_b32_e32 v78, 16, v79
	v_and_b32_e32 v79, 0xffff0000, v79
	v_pk_add_f32 v[88:89], v[88:89], v[90:91]
	v_pk_add_f32 v[74:75], v[74:75], v[78:79]
	v_lshlrev_b32_e32 v78, 16, v76
	v_and_b32_e32 v79, 0xffff0000, v76
	v_lshlrev_b32_e32 v90, 16, v80
	v_and_b32_e32 v91, 0xffff0000, v80
	v_lshlrev_b32_e32 v76, 16, v77
	v_and_b32_e32 v77, 0xffff0000, v77
	v_lshlrev_b32_e32 v80, 16, v81
	v_and_b32_e32 v81, 0xffff0000, v81
	v_pk_add_f32 v[78:79], v[78:79], v[90:91]
	v_pk_add_f32 v[76:77], v[76:77], v[80:81]
	v_pk_add_f32 v[72:73], v[72:73], v[74:75]
	v_pk_add_f32 v[70:71], v[70:71], v[88:89]
	v_pk_add_f32 v[74:75], v[68:69], v[76:77]
	v_pk_add_f32 v[76:77], v[66:67], v[78:79]
	v_cvt_pk_bf16_f32 v66, v70, v71
	v_cvt_pk_bf16_f32 v67, v72, v73
	s_nop 0
	v_cvt_pk_bf16_f32 v68, v76, v77
	v_cvt_pk_bf16_f32 v69, v74, v75
	global_store_dwordx4 v[86:87], v[66:69], off offset:256 sc1
	v_lshlrev_b32_e32 v78, 16, v66
	v_lshlrev_b32_e32 v79, 16, v67
	v_and_b32_e32 v66, 0xffff0000, v66
	v_and_b32_e32 v67, 0xffff0000, v67
	v_sub_f32_e32 v66, v71, v66
	v_sub_f32_e32 v67, v73, v67
	v_lshlrev_b32_e32 v80, 16, v68
	v_and_b32_e32 v68, 0xffff0000, v68
	v_lshlrev_b32_e32 v81, 16, v69
	v_and_b32_e32 v69, 0xffff0000, v69
	v_sub_f32_e32 v78, v70, v78
	v_sub_f32_e32 v79, v72, v79
	v_sub_f32_e32 v68, v77, v68
	v_sub_f32_e32 v69, v75, v69
	v_cvt_pk_bf16_f32 v66, v78, v66
	v_cvt_pk_bf16_f32 v67, v79, v67
	v_sub_f32_e32 v80, v76, v80
	v_sub_f32_e32 v81, v74, v81
	v_cvt_pk_bf16_f32 v68, v80, v68
	v_cvt_pk_bf16_f32 v69, v81, v69
	global_store_dwordx4 v[84:85], v[66:69], off offset:256 sc1
	s_nop 1
	v_mul_f32_e32 v66, v70, v70
	v_mul_f32_e32 v67, v72, v72
	v_fmac_f32_e32 v66, v71, v71
	v_fmac_f32_e32 v67, v73, v73
	v_add_f32_e32 v66, v67, v66
	v_mul_f32_e32 v67, v76, v76
	v_fmac_f32_e32 v67, v77, v77
	v_add_f32_e32 v66, v67, v66
	v_mul_f32_e32 v67, v75, v75
	v_fmac_f32_e32 v67, v74, v74
	v_add_f32_e32 v66, v67, v66
	v_add_f32_e32 v66, v92, v66
	ds_bpermute_b32 v67, v151, v66
	s_waitcnt lgkmcnt(0)
	v_add_f32_e32 v66, v66, v67
	ds_bpermute_b32 v67, v150, v66
	s_and_saveexec_b64 s[24:25], vcc
	s_cbranch_execz .LBB0_1089
	v_lshlrev_b64 v[68:69], 7, v[82:83]
	v_lshl_add_u64 v[68:69], s[10:11], 0, v[68:69]
	v_lshl_add_u64 v[68:69], s[22:23], 2, v[68:69]
	s_lshl_b32 s96, s46, 2
	v_lshl_add_u64 v[68:69], v[68:69], 0, s[96:97]
	s_waitcnt lgkmcnt(0)
	v_add_f32_e32 v66, v66, v67
	global_store_dword v[68:69], v66, off
; __device__ __forceinline__ unsigned cvt_pk_bf16(float lo, float hi) { unsigned r; asm volatile("v_cvt_pk_bf16_f32 %0, %1, %2" : "=v"(r) : "v"(lo), "v"(hi)); return r; }
;     __device__ __forceinline__ void operator()(AccRef acc, const Unit& u, int wr, int wc, int, int) const {
;     ...
;                 const int row = row0 + ai * 128 + m * 16; float s = 0.f;
; #pragma unroll
;                 for (int bj = 0; bj < 2; ++bj) {
;                     const size_t p = (size_t)row * D + col0 + bj * 128;
;                     f32x4 x0, x1;
;                     if (xin32) { x0 = *(const f32x4*)(xin32 + p); x1 = *(const f32x4*)(xin32 + p + 4); }
;                     else { const v4u h = *(const v4u*)(xb + p), lo = *(const v4u*)(xl + p);
;                         x0 = (f32x4){bflo(h.x) + bflo(lo.x), bfhi(h.x) + bfhi(lo.x), bflo(h.y) + bflo(lo.y), bfhi(h.y) + bfhi(lo.y)};
;                         x1 = (f32x4){bflo(h.z) + bflo(lo.z), bfhi(h.z) + bfhi(lo.z), bflo(h.w) + bflo(lo.w), bfhi(h.w) + bfhi(lo.w)}; }
;                     x0 = x0 + alpha * acc[ai][bj][m][0]; x1 = x1 + alpha * acc[ai][bj][m][1];
;                     if (PROBE_ON) { x0 = x0 * pscale; x1 = x1 * pscale; if (p == 0) x0[0] += pspike; }
;                     if (xout32) { *(f32x4*)(xout32 + p) = x0; *(f32x4*)(xout32 + p + 4) = x1; }
;                     else {
;                         v4u w; w.x = cvt_pk_bf16(x0[0], x0[1]); w.y = cvt_pk_bf16(x0[2], x0[3]); w.z = cvt_pk_bf16(x1[0], x1[1]); w.w = cvt_pk_bf16(x1[2], x1[3]);
;                         *(v4u*)(xb + p) = w;
;                         const f32x4 r0 = {x0[0] - bflo(w.x), x0[1] - bfhi(w.x), x0[2] - bflo(w.y), x0[3] - bfhi(w.y)}, r1 = {x1[0] - bflo(w.z), x1[1] - bfhi(w.z), x1[2] - bflo(w.w), x1[3] - bfhi(w.w)};
;                         v4u q; q.x = cvt_pk_bf16(r0[0], r0[1]); q.y = cvt_pk_bf16(r0[2], r0[3]); q.z = cvt_pk_bf16(r1[0], r1[1]); q.w = cvt_pk_bf16(r1[2], r1[3]);
;                         *(v4u*)(xl + p) = q;
;                     }
;                     s += (x0[0] * x0[0] + x0[1] * x0[1]) + (x0[2] * x0[2] + x0[3] * x0[3]) + (x1[0] * x1[0] + x1[1] * x1[1]) + (x1[2] * x1[2] + x1[3] * x1[3]);
;                 }
;                 s += shx(s, 16, ln_); s += shx(s, 32, ln_);
;                 if (fq == 0) ss[(size_t)row * 32 + u.pn * 4 + wc] = s;
.LBB0_1089:
	s_or_b64 exec, exec, s[24:25]
	v_add_u32_e32 v66, 0x80, v142
	s_waitcnt lgkmcnt(0)
	v_ashrrev_i32_e32 v67, 31, v66
	v_lshlrev_b64 v[68:69], 11, v[66:67]
	v_lshl_add_u64 v[68:69], v[68:69], 0, v[140:141]
	v_lshlrev_b64 v[68:69], 1, v[68:69]
	v_lshl_add_u64 v[70:71], s[6:7], 0, v[68:69]
	v_lshl_add_u64 v[68:69], s[8:9], 0, v[68:69]
	global_load_dwordx4 v[72:75], v[70:71], off
	global_load_dwordx4 v[76:79], v[68:69], off
	s_waitcnt vmcnt(1)
	v_lshlrev_b32_e32 v80, 16, v72
	v_and_b32_e32 v81, 0xffff0000, v72
	s_waitcnt vmcnt(0)
	v_lshlrev_b32_e32 v82, 16, v76
	v_and_b32_e32 v83, 0xffff0000, v76
	v_lshlrev_b32_e32 v72, 16, v73
	v_and_b32_e32 v73, 0xffff0000, v73
	v_lshlrev_b32_e32 v76, 16, v77
	v_and_b32_e32 v77, 0xffff0000, v77
	v_pk_add_f32 v[80:81], v[80:81], v[82:83]
	v_pk_add_f32 v[72:73], v[72:73], v[76:77]
	v_lshlrev_b32_e32 v76, 16, v74
	v_and_b32_e32 v77, 0xffff0000, v74
	v_lshlrev_b32_e32 v82, 16, v78
	v_and_b32_e32 v83, 0xffff0000, v78
	v_lshlrev_b32_e32 v74, 16, v75
	v_and_b32_e32 v75, 0xffff0000, v75
	v_lshlrev_b32_e32 v78, 16, v79
	v_and_b32_e32 v79, 0xffff0000, v79
	v_pk_add_f32 v[76:77], v[76:77], v[82:83]
	v_pk_add_f32 v[74:75], v[74:75], v[78:79]
	v_pk_add_f32 v[64:65], v[64:65], v[72:73]
	v_pk_add_f32 v[62:63], v[62:63], v[80:81]
	v_pk_add_f32 v[72:73], v[60:61], v[74:75]
	v_pk_add_f32 v[74:75], v[58:59], v[76:77]
	v_cvt_pk_bf16_f32 v58, v62, v63
	v_cvt_pk_bf16_f32 v59, v64, v65
	s_nop 0
	v_cvt_pk_bf16_f32 v60, v74, v75
	v_cvt_pk_bf16_f32 v61, v72, v73
	global_store_dwordx4 v[70:71], v[58:61], off sc1
	v_lshlrev_b32_e32 v76, 16, v58
	v_lshlrev_b32_e32 v77, 16, v59
	v_and_b32_e32 v58, 0xffff0000, v58
	v_and_b32_e32 v59, 0xffff0000, v59
	v_sub_f32_e32 v58, v63, v58
	v_sub_f32_e32 v59, v65, v59
	v_lshlrev_b32_e32 v78, 16, v60
	v_and_b32_e32 v60, 0xffff0000, v60
	v_lshlrev_b32_e32 v79, 16, v61
	v_and_b32_e32 v61, 0xffff0000, v61
	v_sub_f32_e32 v76, v62, v76
	v_sub_f32_e32 v77, v64, v77
	v_sub_f32_e32 v60, v75, v60
	v_sub_f32_e32 v61, v73, v61
	v_cvt_pk_bf16_f32 v58, v76, v58
	v_cvt_pk_bf16_f32 v59, v77, v59
	v_sub_f32_e32 v78, v74, v78
	v_sub_f32_e32 v79, v72, v79
	v_cvt_pk_bf16_f32 v60, v78, v60
	v_cvt_pk_bf16_f32 v61, v79, v61
	global_store_dwordx4 v[68:69], v[58:61], off sc1
	s_nop 1
	v_mul_f32_e32 v58, v62, v62
	v_mul_f32_e32 v59, v64, v64
	v_fmac_f32_e32 v58, v63, v63
	v_fmac_f32_e32 v59, v65, v65
	v_add_f32_e32 v58, v59, v58
	v_mul_f32_e32 v59, v74, v74
	v_fmac_f32_e32 v59, v75, v75
	v_add_f32_e32 v58, v59, v58
	v_mul_f32_e32 v59, v73, v73
	v_fmac_f32_e32 v59, v72, v72
	v_add_f32_e32 v76, v59, v58
	global_load_dwordx4 v[58:61], v[70:71], off offset:256
	global_load_dwordx4 v[62:65], v[68:69], off offset:256
	s_waitcnt vmcnt(1)
	v_lshlrev_b32_e32 v72, 16, v58
	v_and_b32_e32 v73, 0xffff0000, v58
	s_waitcnt vmcnt(0)
	v_lshlrev_b32_e32 v74, 16, v62
	v_and_b32_e32 v75, 0xffff0000, v62
	v_lshlrev_b32_e32 v58, 16, v59
	v_and_b32_e32 v59, 0xffff0000, v59
	v_lshlrev_b32_e32 v62, 16, v63
	v_and_b32_e32 v63, 0xffff0000, v63
	v_pk_add_f32 v[72:73], v[72:73], v[74:75]
	v_pk_add_f32 v[58:59], v[58:59], v[62:63]
	v_lshlrev_b32_e32 v62, 16, v60
	v_and_b32_e32 v63, 0xffff0000, v60
	v_lshlrev_b32_e32 v74, 16, v64
	v_and_b32_e32 v75, 0xffff0000, v64
	v_lshlrev_b32_e32 v60, 16, v61
	v_and_b32_e32 v61, 0xffff0000, v61
	v_lshlrev_b32_e32 v64, 16, v65
	v_and_b32_e32 v65, 0xffff0000, v65
	v_pk_add_f32 v[62:63], v[62:63], v[74:75]
	v_pk_add_f32 v[60:61], v[60:61], v[64:65]
	v_pk_add_f32 v[56:57], v[56:57], v[58:59]
	v_pk_add_f32 v[54:55], v[54:55], v[72:73]
	v_pk_add_f32 v[58:59], v[52:53], v[60:61]
	v_pk_add_f32 v[60:61], v[50:51], v[62:63]
	v_cvt_pk_bf16_f32 v50, v54, v55
	v_cvt_pk_bf16_f32 v51, v56, v57
	s_nop 0
	v_cvt_pk_bf16_f32 v52, v60, v61
	v_cvt_pk_bf16_f32 v53, v58, v59
	global_store_dwordx4 v[70:71], v[50:53], off offset:256 sc1
	v_lshlrev_b32_e32 v62, 16, v50
	v_lshlrev_b32_e32 v63, 16, v51
	v_and_b32_e32 v50, 0xffff0000, v50
	v_and_b32_e32 v51, 0xffff0000, v51
	v_sub_f32_e32 v50, v55, v50
	v_sub_f32_e32 v51, v57, v51
	v_lshlrev_b32_e32 v64, 16, v52
	v_and_b32_e32 v52, 0xffff0000, v52
	v_lshlrev_b32_e32 v65, 16, v53
	v_and_b32_e32 v53, 0xffff0000, v53
	v_sub_f32_e32 v62, v54, v62
	v_sub_f32_e32 v63, v56, v63
	v_sub_f32_e32 v52, v61, v52
	v_sub_f32_e32 v53, v59, v53
	v_cvt_pk_bf16_f32 v50, v62, v50
	v_cvt_pk_bf16_f32 v51, v63, v51
	v_sub_f32_e32 v64, v60, v64
	v_sub_f32_e32 v65, v58, v65
	v_cvt_pk_bf16_f32 v52, v64, v52
	v_cvt_pk_bf16_f32 v53, v65, v53
	global_store_dwordx4 v[68:69], v[50:53], off offset:256 sc1
	s_nop 1
	v_mul_f32_e32 v50, v54, v54
	v_mul_f32_e32 v51, v56, v56
	v_fmac_f32_e32 v50, v55, v55
	v_fmac_f32_e32 v51, v57, v57
	v_add_f32_e32 v50, v51, v50
	v_mul_f32_e32 v51, v60, v60
	v_fmac_f32_e32 v51, v61, v61
	v_add_f32_e32 v50, v51, v50
	v_mul_f32_e32 v51, v59, v59
	v_fmac_f32_e32 v51, v58, v58
	v_add_f32_e32 v50, v51, v50
	v_add_f32_e32 v50, v76, v50
	ds_bpermute_b32 v51, v151, v50
	s_waitcnt lgkmcnt(0)
	v_add_f32_e32 v50, v50, v51
	ds_bpermute_b32 v51, v150, v50
	s_and_saveexec_b64 s[24:25], vcc
	s_cbranch_execz .LBB0_1091
	v_lshlrev_b64 v[52:53], 7, v[66:67]
	v_lshl_add_u64 v[52:53], s[10:11], 0, v[52:53]
	v_lshl_add_u64 v[52:53], s[22:23], 2, v[52:53]
	s_lshl_b32 s96, s46, 2
	v_lshl_add_u64 v[52:53], v[52:53], 0, s[96:97]
	s_waitcnt lgkmcnt(0)
	v_add_f32_e32 v50, v50, v51
	global_store_dword v[52:53], v50, off
; __device__ __forceinline__ unsigned cvt_pk_bf16(float lo, float hi) { unsigned r; asm volatile("v_cvt_pk_bf16_f32 %0, %1, %2" : "=v"(r) : "v"(lo), "v"(hi)); return r; }
;     __device__ __forceinline__ void operator()(AccRef acc, const Unit& u, int wr, int wc, int, int) const {
;     ...
;                 const int row = row0 + ai * 128 + m * 16; float s = 0.f;
; #pragma unroll
;                 for (int bj = 0; bj < 2; ++bj) {
;                     const size_t p = (size_t)row * D + col0 + bj * 128;
;                     f32x4 x0, x1;
;                     if (xin32) { x0 = *(const f32x4*)(xin32 + p); x1 = *(const f32x4*)(xin32 + p + 4); }
;                     else { const v4u h = *(const v4u*)(xb + p), lo = *(const v4u*)(xl + p);
;                         x0 = (f32x4){bflo(h.x) + bflo(lo.x), bfhi(h.x) + bfhi(lo.x), bflo(h.y) + bflo(lo.y), bfhi(h.y) + bfhi(lo.y)};
;                         x1 = (f32x4){bflo(h.z) + bflo(lo.z), bfhi(h.z) + bfhi(lo.z), bflo(h.w) + bflo(lo.w), bfhi(h.w) + bfhi(lo.w)}; }
;                     x0 = x0 + alpha * acc[ai][bj][m][0]; x1 = x1 + alpha * acc[ai][bj][m][1];
;                     if (PROBE_ON) { x0 = x0 * pscale; x1 = x1 * pscale; if (p == 0) x0[0] += pspike; }
;                     if (xout32) { *(f32x4*)(xout32 + p) = x0; *(f32x4*)(xout32 + p + 4) = x1; }
;                     else {
;                         v4u w; w.x = cvt_pk_bf16(x0[0], x0[1]); w.y = cvt_pk_bf16(x0[2], x0[3]); w.z = cvt_pk_bf16(x1[0], x1[1]); w.w = cvt_pk_bf16(x1[2], x1[3]);
;                         *(v4u*)(xb + p) = w;
;                         const f32x4 r0 = {x0[0] - bflo(w.x), x0[1] - bfhi(w.x), x0[2] - bflo(w.y), x0[3] - bfhi(w.y)}, r1 = {x1[0] - bflo(w.z), x1[1] - bfhi(w.z), x1[2] - bflo(w.w), x1[3] - bfhi(w.w)};
;                         v4u q; q.x = cvt_pk_bf16(r0[0], r0[1]); q.y = cvt_pk_bf16(r0[2], r0[3]); q.z = cvt_pk_bf16(r1[0], r1[1]); q.w = cvt_pk_bf16(r1[2], r1[3]);
;                         *(v4u*)(xl + p) = q;
;                     }
;                     s += (x0[0] * x0[0] + x0[1] * x0[1]) + (x0[2] * x0[2] + x0[3] * x0[3]) + (x1[0] * x1[0] + x1[1] * x1[1]) + (x1[2] * x1[2] + x1[3] * x1[3]);
;                 }
;                 s += shx(s, 16, ln_); s += shx(s, 32, ln_);
;                 if (fq == 0) ss[(size_t)row * 32 + u.pn * 4 + wc] = s;
.LBB0_1091:
	s_or_b64 exec, exec, s[24:25]
	v_add_u32_e32 v50, 0x90, v142
	s_waitcnt lgkmcnt(0)
	v_ashrrev_i32_e32 v51, 31, v50
	v_lshlrev_b64 v[52:53], 11, v[50:51]
	v_lshl_add_u64 v[52:53], v[52:53], 0, v[140:141]
	v_lshlrev_b64 v[52:53], 1, v[52:53]
	v_lshl_add_u64 v[54:55], s[6:7], 0, v[52:53]
	v_lshl_add_u64 v[52:53], s[8:9], 0, v[52:53]
	global_load_dwordx4 v[56:59], v[54:55], off
	global_load_dwordx4 v[60:63], v[52:53], off
	s_waitcnt vmcnt(1)
	v_lshlrev_b32_e32 v64, 16, v56
	v_and_b32_e32 v65, 0xffff0000, v56
	s_waitcnt vmcnt(0)
	v_lshlrev_b32_e32 v66, 16, v60
	v_and_b32_e32 v67, 0xffff0000, v60
	v_lshlrev_b32_e32 v56, 16, v57
	v_and_b32_e32 v57, 0xffff0000, v57
	v_lshlrev_b32_e32 v60, 16, v61
	v_and_b32_e32 v61, 0xffff0000, v61
	v_pk_add_f32 v[64:65], v[64:65], v[66:67]
	v_pk_add_f32 v[56:57], v[56:57], v[60:61]
	v_lshlrev_b32_e32 v60, 16, v58
	v_and_b32_e32 v61, 0xffff0000, v58
	v_lshlrev_b32_e32 v66, 16, v62
	v_and_b32_e32 v67, 0xffff0000, v62
	v_lshlrev_b32_e32 v58, 16, v59
	v_and_b32_e32 v59, 0xffff0000, v59
	v_lshlrev_b32_e32 v62, 16, v63
	v_and_b32_e32 v63, 0xffff0000, v63
	v_pk_add_f32 v[60:61], v[60:61], v[66:67]
	v_pk_add_f32 v[58:59], v[58:59], v[62:63]
	v_pk_add_f32 v[48:49], v[48:49], v[56:57]
	v_pk_add_f32 v[46:47], v[46:47], v[64:65]
	v_pk_add_f32 v[56:57], v[44:45], v[58:59]
	v_pk_add_f32 v[58:59], v[42:43], v[60:61]
	v_cvt_pk_bf16_f32 v42, v46, v47
	v_cvt_pk_bf16_f32 v43, v48, v49
	s_nop 0
	v_cvt_pk_bf16_f32 v44, v58, v59
	v_cvt_pk_bf16_f32 v45, v56, v57
	global_store_dwordx4 v[54:55], v[42:45], off sc1
	v_lshlrev_b32_e32 v60, 16, v42
	v_lshlrev_b32_e32 v61, 16, v43
	v_and_b32_e32 v42, 0xffff0000, v42
	v_and_b32_e32 v43, 0xffff0000, v43
	v_sub_f32_e32 v42, v47, v42
	v_sub_f32_e32 v43, v49, v43
	v_lshlrev_b32_e32 v62, 16, v44
	v_and_b32_e32 v44, 0xffff0000, v44
	v_lshlrev_b32_e32 v63, 16, v45
	v_and_b32_e32 v45, 0xffff0000, v45
	v_sub_f32_e32 v60, v46, v60
	v_sub_f32_e32 v61, v48, v61
	v_sub_f32_e32 v44, v59, v44
	v_sub_f32_e32 v45, v57, v45
	v_cvt_pk_bf16_f32 v42, v60, v42
	v_cvt_pk_bf16_f32 v43, v61, v43
	v_sub_f32_e32 v62, v58, v62
	v_sub_f32_e32 v63, v56, v63
	v_cvt_pk_bf16_f32 v44, v62, v44
	v_cvt_pk_bf16_f32 v45, v63, v45
	global_store_dwordx4 v[52:53], v[42:45], off sc1
	s_nop 1
	v_mul_f32_e32 v42, v46, v46
	v_mul_f32_e32 v43, v48, v48
	v_fmac_f32_e32 v42, v47, v47
	v_fmac_f32_e32 v43, v49, v49
	v_add_f32_e32 v42, v43, v42
	v_mul_f32_e32 v43, v58, v58
	v_fmac_f32_e32 v43, v59, v59
	v_add_f32_e32 v42, v43, v42
	v_mul_f32_e32 v43, v57, v57
	v_fmac_f32_e32 v43, v56, v56
	v_add_f32_e32 v60, v43, v42
	global_load_dwordx4 v[42:45], v[54:55], off offset:256
	global_load_dwordx4 v[46:49], v[52:53], off offset:256
	s_waitcnt vmcnt(1)
	v_lshlrev_b32_e32 v56, 16, v42
	v_and_b32_e32 v57, 0xffff0000, v42
	s_waitcnt vmcnt(0)
	v_lshlrev_b32_e32 v58, 16, v46
	v_and_b32_e32 v59, 0xffff0000, v46
	v_lshlrev_b32_e32 v42, 16, v43
	v_and_b32_e32 v43, 0xffff0000, v43
	v_lshlrev_b32_e32 v46, 16, v47
	v_and_b32_e32 v47, 0xffff0000, v47
	v_pk_add_f32 v[56:57], v[56:57], v[58:59]
	v_pk_add_f32 v[42:43], v[42:43], v[46:47]
	v_lshlrev_b32_e32 v46, 16, v44
	v_and_b32_e32 v47, 0xffff0000, v44
	v_lshlrev_b32_e32 v58, 16, v48
	v_and_b32_e32 v59, 0xffff0000, v48
	v_lshlrev_b32_e32 v44, 16, v45
	v_and_b32_e32 v45, 0xffff0000, v45
	v_lshlrev_b32_e32 v48, 16, v49
	v_and_b32_e32 v49, 0xffff0000, v49
	v_pk_add_f32 v[46:47], v[46:47], v[58:59]
	v_pk_add_f32 v[44:45], v[44:45], v[48:49]
	v_pk_add_f32 v[40:41], v[40:41], v[42:43]
	v_pk_add_f32 v[38:39], v[38:39], v[56:57]
	v_pk_add_f32 v[42:43], v[36:37], v[44:45]
	v_pk_add_f32 v[44:45], v[34:35], v[46:47]
	v_cvt_pk_bf16_f32 v34, v38, v39
	v_cvt_pk_bf16_f32 v35, v40, v41
	s_nop 0
	v_cvt_pk_bf16_f32 v36, v44, v45
	v_cvt_pk_bf16_f32 v37, v42, v43
	global_store_dwordx4 v[54:55], v[34:37], off offset:256 sc1
	v_lshlrev_b32_e32 v46, 16, v34
	v_lshlrev_b32_e32 v47, 16, v35
	v_and_b32_e32 v34, 0xffff0000, v34
	v_and_b32_e32 v35, 0xffff0000, v35
	v_sub_f32_e32 v34, v39, v34
	v_sub_f32_e32 v35, v41, v35
	v_lshlrev_b32_e32 v48, 16, v36
	v_and_b32_e32 v36, 0xffff0000, v36
	v_lshlrev_b32_e32 v49, 16, v37
	v_and_b32_e32 v37, 0xffff0000, v37
	v_sub_f32_e32 v46, v38, v46
	v_sub_f32_e32 v47, v40, v47
	v_sub_f32_e32 v36, v45, v36
	v_sub_f32_e32 v37, v43, v37
	v_cvt_pk_bf16_f32 v34, v46, v34
	v_cvt_pk_bf16_f32 v35, v47, v35
	v_sub_f32_e32 v48, v44, v48
	v_sub_f32_e32 v49, v42, v49
	v_cvt_pk_bf16_f32 v36, v48, v36
	v_cvt_pk_bf16_f32 v37, v49, v37
	global_store_dwordx4 v[52:53], v[34:37], off offset:256 sc1
	s_nop 1
	v_mul_f32_e32 v34, v38, v38
	v_mul_f32_e32 v35, v40, v40
	v_fmac_f32_e32 v34, v39, v39
	v_fmac_f32_e32 v35, v41, v41
	v_add_f32_e32 v34, v35, v34
	v_mul_f32_e32 v35, v44, v44
	v_fmac_f32_e32 v35, v45, v45
	v_add_f32_e32 v34, v35, v34
	v_mul_f32_e32 v35, v43, v43
	v_fmac_f32_e32 v35, v42, v42
	v_add_f32_e32 v34, v35, v34
	v_add_f32_e32 v34, v60, v34
	ds_bpermute_b32 v35, v151, v34
	s_waitcnt lgkmcnt(0)
	v_add_f32_e32 v34, v34, v35
	ds_bpermute_b32 v35, v150, v34
	s_and_saveexec_b64 s[24:25], vcc
	s_cbranch_execz .LBB0_1093
	v_lshlrev_b64 v[36:37], 7, v[50:51]
	v_lshl_add_u64 v[36:37], s[10:11], 0, v[36:37]
	v_lshl_add_u64 v[36:37], s[22:23], 2, v[36:37]
	s_lshl_b32 s96, s46, 2
	v_lshl_add_u64 v[36:37], v[36:37], 0, s[96:97]
	s_waitcnt lgkmcnt(0)
	v_add_f32_e32 v34, v34, v35
	global_store_dword v[36:37], v34, off
; __device__ __forceinline__ unsigned cvt_pk_bf16(float lo, float hi) { unsigned r; asm volatile("v_cvt_pk_bf16_f32 %0, %1, %2" : "=v"(r) : "v"(lo), "v"(hi)); return r; }
;     __device__ __forceinline__ void operator()(AccRef acc, const Unit& u, int wr, int wc, int, int) const {
;     ...
;                 const int row = row0 + ai * 128 + m * 16; float s = 0.f;
; #pragma unroll
;                 for (int bj = 0; bj < 2; ++bj) {
;                     const size_t p = (size_t)row * D + col0 + bj * 128;
;                     f32x4 x0, x1;
;                     if (xin32) { x0 = *(const f32x4*)(xin32 + p); x1 = *(const f32x4*)(xin32 + p + 4); }
;                     else { const v4u h = *(const v4u*)(xb + p), lo = *(const v4u*)(xl + p);
;                         x0 = (f32x4){bflo(h.x) + bflo(lo.x), bfhi(h.x) + bfhi(lo.x), bflo(h.y) + bflo(lo.y), bfhi(h.y) + bfhi(lo.y)};
;                         x1 = (f32x4){bflo(h.z) + bflo(lo.z), bfhi(h.z) + bfhi(lo.z), bflo(h.w) + bflo(lo.w), bfhi(h.w) + bfhi(lo.w)}; }
;                     x0 = x0 + alpha * acc[ai][bj][m][0]; x1 = x1 + alpha * acc[ai][bj][m][1];
;                     if (PROBE_ON) { x0 = x0 * pscale; x1 = x1 * pscale; if (p == 0) x0[0] += pspike; }
;                     if (xout32) { *(f32x4*)(xout32 + p) = x0; *(f32x4*)(xout32 + p + 4) = x1; }
;                     else {
;                         v4u w; w.x = cvt_pk_bf16(x0[0], x0[1]); w.y = cvt_pk_bf16(x0[2], x0[3]); w.z = cvt_pk_bf16(x1[0], x1[1]); w.w = cvt_pk_bf16(x1[2], x1[3]);
;                         *(v4u*)(xb + p) = w;
;                         const f32x4 r0 = {x0[0] - bflo(w.x), x0[1] - bfhi(w.x), x0[2] - bflo(w.y), x0[3] - bfhi(w.y)}, r1 = {x1[0] - bflo(w.z), x1[1] - bfhi(w.z), x1[2] - bflo(w.w), x1[3] - bfhi(w.w)};
;                         v4u q; q.x = cvt_pk_bf16(r0[0], r0[1]); q.y = cvt_pk_bf16(r0[2], r0[3]); q.z = cvt_pk_bf16(r1[0], r1[1]); q.w = cvt_pk_bf16(r1[2], r1[3]);
;                         *(v4u*)(xl + p) = q;
;                     }
;                     s += (x0[0] * x0[0] + x0[1] * x0[1]) + (x0[2] * x0[2] + x0[3] * x0[3]) + (x1[0] * x1[0] + x1[1] * x1[1]) + (x1[2] * x1[2] + x1[3] * x1[3]);
;                 }
;                 s += shx(s, 16, ln_); s += shx(s, 32, ln_);
;                 if (fq == 0) ss[(size_t)row * 32 + u.pn * 4 + wc] = s;
.LBB0_1093:
	s_or_b64 exec, exec, s[24:25]
	v_add_u32_e32 v34, 0xa0, v142
	s_waitcnt lgkmcnt(0)
	v_ashrrev_i32_e32 v35, 31, v34
	v_lshlrev_b64 v[36:37], 11, v[34:35]
	v_lshl_add_u64 v[36:37], v[36:37], 0, v[140:141]
	v_lshlrev_b64 v[36:37], 1, v[36:37]
	v_lshl_add_u64 v[38:39], s[6:7], 0, v[36:37]
	v_lshl_add_u64 v[36:37], s[8:9], 0, v[36:37]
	global_load_dwordx4 v[40:43], v[38:39], off
	global_load_dwordx4 v[44:47], v[36:37], off
	s_waitcnt vmcnt(1)
	v_lshlrev_b32_e32 v48, 16, v40
	v_and_b32_e32 v49, 0xffff0000, v40
	s_waitcnt vmcnt(0)
	v_lshlrev_b32_e32 v50, 16, v44
	v_and_b32_e32 v51, 0xffff0000, v44
	v_lshlrev_b32_e32 v40, 16, v41
	v_and_b32_e32 v41, 0xffff0000, v41
	v_lshlrev_b32_e32 v44, 16, v45
	v_and_b32_e32 v45, 0xffff0000, v45
	v_pk_add_f32 v[48:49], v[48:49], v[50:51]
	v_pk_add_f32 v[40:41], v[40:41], v[44:45]
	v_lshlrev_b32_e32 v44, 16, v42
	v_and_b32_e32 v45, 0xffff0000, v42
	v_lshlrev_b32_e32 v50, 16, v46
	v_and_b32_e32 v51, 0xffff0000, v46
	v_lshlrev_b32_e32 v42, 16, v43
	v_and_b32_e32 v43, 0xffff0000, v43
	v_lshlrev_b32_e32 v46, 16, v47
	v_and_b32_e32 v47, 0xffff0000, v47
	v_pk_add_f32 v[44:45], v[44:45], v[50:51]
	v_pk_add_f32 v[42:43], v[42:43], v[46:47]
	v_pk_add_f32 v[32:33], v[32:33], v[40:41]
	v_pk_add_f32 v[30:31], v[30:31], v[48:49]
	v_pk_add_f32 v[40:41], v[28:29], v[42:43]
	v_pk_add_f32 v[42:43], v[26:27], v[44:45]
	v_cvt_pk_bf16_f32 v26, v30, v31
	v_cvt_pk_bf16_f32 v27, v32, v33
	s_nop 0
	v_cvt_pk_bf16_f32 v28, v42, v43
	v_cvt_pk_bf16_f32 v29, v40, v41
	global_store_dwordx4 v[38:39], v[26:29], off sc1
	v_lshlrev_b32_e32 v44, 16, v26
	v_lshlrev_b32_e32 v45, 16, v27
	v_and_b32_e32 v26, 0xffff0000, v26
	v_and_b32_e32 v27, 0xffff0000, v27
	v_sub_f32_e32 v26, v31, v26
	v_sub_f32_e32 v27, v33, v27
	v_lshlrev_b32_e32 v46, 16, v28
	v_and_b32_e32 v28, 0xffff0000, v28
	v_lshlrev_b32_e32 v47, 16, v29
	v_and_b32_e32 v29, 0xffff0000, v29
	v_sub_f32_e32 v44, v30, v44
	v_sub_f32_e32 v45, v32, v45
	v_sub_f32_e32 v28, v43, v28
	v_sub_f32_e32 v29, v41, v29
	v_cvt_pk_bf16_f32 v26, v44, v26
	v_cvt_pk_bf16_f32 v27, v45, v27
	v_sub_f32_e32 v46, v42, v46
	v_sub_f32_e32 v47, v40, v47
	v_cvt_pk_bf16_f32 v28, v46, v28
	v_cvt_pk_bf16_f32 v29, v47, v29
	global_store_dwordx4 v[36:37], v[26:29], off sc1
	s_nop 1
	v_mul_f32_e32 v26, v30, v30
	v_mul_f32_e32 v27, v32, v32
	v_fmac_f32_e32 v26, v31, v31
	v_fmac_f32_e32 v27, v33, v33
	v_add_f32_e32 v26, v27, v26
	v_mul_f32_e32 v27, v42, v42
	v_fmac_f32_e32 v27, v43, v43
	v_add_f32_e32 v26, v27, v26
	v_mul_f32_e32 v27, v41, v41
	v_fmac_f32_e32 v27, v40, v40
	v_add_f32_e32 v44, v27, v26
	global_load_dwordx4 v[26:29], v[38:39], off offset:256
	global_load_dwordx4 v[30:33], v[36:37], off offset:256
	s_waitcnt vmcnt(1)
	v_lshlrev_b32_e32 v40, 16, v26
	v_and_b32_e32 v41, 0xffff0000, v26
	s_waitcnt vmcnt(0)
	v_lshlrev_b32_e32 v42, 16, v30
	v_and_b32_e32 v43, 0xffff0000, v30
	v_lshlrev_b32_e32 v26, 16, v27
	v_and_b32_e32 v27, 0xffff0000, v27
	v_lshlrev_b32_e32 v30, 16, v31
	v_and_b32_e32 v31, 0xffff0000, v31
	v_pk_add_f32 v[40:41], v[40:41], v[42:43]
	v_pk_add_f32 v[26:27], v[26:27], v[30:31]
	v_lshlrev_b32_e32 v30, 16, v28
	v_and_b32_e32 v31, 0xffff0000, v28
	v_lshlrev_b32_e32 v42, 16, v32
	v_and_b32_e32 v43, 0xffff0000, v32
	v_lshlrev_b32_e32 v28, 16, v29
	v_and_b32_e32 v29, 0xffff0000, v29
	v_lshlrev_b32_e32 v32, 16, v33
	v_and_b32_e32 v33, 0xffff0000, v33
	v_pk_add_f32 v[30:31], v[30:31], v[42:43]
	v_pk_add_f32 v[28:29], v[28:29], v[32:33]
	v_pk_add_f32 v[24:25], v[24:25], v[26:27]
	v_pk_add_f32 v[22:23], v[22:23], v[40:41]
	v_pk_add_f32 v[26:27], v[20:21], v[28:29]
	v_pk_add_f32 v[28:29], v[18:19], v[30:31]
	v_cvt_pk_bf16_f32 v18, v22, v23
	v_cvt_pk_bf16_f32 v19, v24, v25
	s_nop 0
	v_cvt_pk_bf16_f32 v20, v28, v29
	v_cvt_pk_bf16_f32 v21, v26, v27
	global_store_dwordx4 v[38:39], v[18:21], off offset:256 sc1
	v_lshlrev_b32_e32 v30, 16, v18
	v_lshlrev_b32_e32 v31, 16, v19
	v_and_b32_e32 v18, 0xffff0000, v18
	v_and_b32_e32 v19, 0xffff0000, v19
	v_sub_f32_e32 v18, v23, v18
	v_sub_f32_e32 v19, v25, v19
	v_lshlrev_b32_e32 v32, 16, v20
	v_and_b32_e32 v20, 0xffff0000, v20
	v_lshlrev_b32_e32 v33, 16, v21
	v_and_b32_e32 v21, 0xffff0000, v21
	v_sub_f32_e32 v30, v22, v30
	v_sub_f32_e32 v31, v24, v31
	v_sub_f32_e32 v20, v29, v20
	v_sub_f32_e32 v21, v27, v21
	v_cvt_pk_bf16_f32 v18, v30, v18
	v_cvt_pk_bf16_f32 v19, v31, v19
	v_sub_f32_e32 v32, v28, v32
	v_sub_f32_e32 v33, v26, v33
	v_cvt_pk_bf16_f32 v20, v32, v20
	v_cvt_pk_bf16_f32 v21, v33, v21
	global_store_dwordx4 v[36:37], v[18:21], off offset:256 sc1
	s_nop 1
	v_mul_f32_e32 v18, v22, v22
	v_mul_f32_e32 v19, v24, v24
	v_fmac_f32_e32 v18, v23, v23
	v_fmac_f32_e32 v19, v25, v25
	v_add_f32_e32 v18, v19, v18
	v_mul_f32_e32 v19, v28, v28
	v_fmac_f32_e32 v19, v29, v29
	v_add_f32_e32 v18, v19, v18
	v_mul_f32_e32 v19, v27, v27
	v_fmac_f32_e32 v19, v26, v26
	v_add_f32_e32 v18, v19, v18
	v_add_f32_e32 v18, v44, v18
	ds_bpermute_b32 v19, v151, v18
	s_waitcnt lgkmcnt(0)
	v_add_f32_e32 v18, v18, v19
	ds_bpermute_b32 v19, v150, v18
	s_and_saveexec_b64 s[24:25], vcc
	s_cbranch_execz .LBB0_1095
	v_lshlrev_b64 v[20:21], 7, v[34:35]
	v_lshl_add_u64 v[20:21], s[10:11], 0, v[20:21]
	v_lshl_add_u64 v[20:21], s[22:23], 2, v[20:21]
	s_lshl_b32 s96, s46, 2
	v_lshl_add_u64 v[20:21], v[20:21], 0, s[96:97]
	s_waitcnt lgkmcnt(0)
	v_add_f32_e32 v18, v18, v19
	global_store_dword v[20:21], v18, off
; __device__ __forceinline__ unsigned cvt_pk_bf16(float lo, float hi) { unsigned r; asm volatile("v_cvt_pk_bf16_f32 %0, %1, %2" : "=v"(r) : "v"(lo), "v"(hi)); return r; }
;     __device__ __forceinline__ void operator()(AccRef acc, const Unit& u, int wr, int wc, int, int) const {
;     ...
;                 const int row = row0 + ai * 128 + m * 16; float s = 0.f;
; #pragma unroll
;                 for (int bj = 0; bj < 2; ++bj) {
;                     const size_t p = (size_t)row * D + col0 + bj * 128;
;                     f32x4 x0, x1;
;                     if (xin32) { x0 = *(const f32x4*)(xin32 + p); x1 = *(const f32x4*)(xin32 + p + 4); }
;                     else { const v4u h = *(const v4u*)(xb + p), lo = *(const v4u*)(xl + p);
;                         x0 = (f32x4){bflo(h.x) + bflo(lo.x), bfhi(h.x) + bfhi(lo.x), bflo(h.y) + bflo(lo.y), bfhi(h.y) + bfhi(lo.y)};
;                         x1 = (f32x4){bflo(h.z) + bflo(lo.z), bfhi(h.z) + bfhi(lo.z), bflo(h.w) + bflo(lo.w), bfhi(h.w) + bfhi(lo.w)}; }
;                     x0 = x0 + alpha * acc[ai][bj][m][0]; x1 = x1 + alpha * acc[ai][bj][m][1];
;                     if (PROBE_ON) { x0 = x0 * pscale; x1 = x1 * pscale; if (p == 0) x0[0] += pspike; }
;                     if (xout32) { *(f32x4*)(xout32 + p) = x0; *(f32x4*)(xout32 + p + 4) = x1; }
;                     else {
;                         v4u w; w.x = cvt_pk_bf16(x0[0], x0[1]); w.y = cvt_pk_bf16(x0[2], x0[3]); w.z = cvt_pk_bf16(x1[0], x1[1]); w.w = cvt_pk_bf16(x1[2], x1[3]);
;                         *(v4u*)(xb + p) = w;
;                         const f32x4 r0 = {x0[0] - bflo(w.x), x0[1] - bfhi(w.x), x0[2] - bflo(w.y), x0[3] - bfhi(w.y)}, r1 = {x1[0] - bflo(w.z), x1[1] - bfhi(w.z), x1[2] - bflo(w.w), x1[3] - bfhi(w.w)};
;                         v4u q; q.x = cvt_pk_bf16(r0[0], r0[1]); q.y = cvt_pk_bf16(r0[2], r0[3]); q.z = cvt_pk_bf16(r1[0], r1[1]); q.w = cvt_pk_bf16(r1[2], r1[3]);
;                         *(v4u*)(xl + p) = q;
;                     }
;                     s += (x0[0] * x0[0] + x0[1] * x0[1]) + (x0[2] * x0[2] + x0[3] * x0[3]) + (x1[0] * x1[0] + x1[1] * x1[1]) + (x1[2] * x1[2] + x1[3] * x1[3]);
;                 }
;                 s += shx(s, 16, ln_); s += shx(s, 32, ln_);
;                 if (fq == 0) ss[(size_t)row * 32 + u.pn * 4 + wc] = s;
.LBB0_1095:
	s_or_b64 exec, exec, s[24:25]
	v_add_u32_e32 v18, 0xb0, v142
	s_waitcnt lgkmcnt(0)
	v_ashrrev_i32_e32 v19, 31, v18
	v_lshlrev_b64 v[20:21], 11, v[18:19]
	v_lshl_add_u64 v[20:21], v[20:21], 0, v[140:141]
	v_lshlrev_b64 v[20:21], 1, v[20:21]
	v_lshl_add_u64 v[22:23], s[6:7], 0, v[20:21]
	v_lshl_add_u64 v[20:21], s[8:9], 0, v[20:21]
	global_load_dwordx4 v[24:27], v[22:23], off
	global_load_dwordx4 v[28:31], v[20:21], off
	s_waitcnt vmcnt(1)
	v_lshlrev_b32_e32 v32, 16, v24
	v_and_b32_e32 v33, 0xffff0000, v24
	s_waitcnt vmcnt(0)
	v_lshlrev_b32_e32 v34, 16, v28
	v_and_b32_e32 v35, 0xffff0000, v28
	v_lshlrev_b32_e32 v24, 16, v25
	v_and_b32_e32 v25, 0xffff0000, v25
	v_lshlrev_b32_e32 v28, 16, v29
	v_and_b32_e32 v29, 0xffff0000, v29
	v_pk_add_f32 v[32:33], v[32:33], v[34:35]
	v_pk_add_f32 v[24:25], v[24:25], v[28:29]
	v_lshlrev_b32_e32 v28, 16, v26
	v_and_b32_e32 v29, 0xffff0000, v26
	v_lshlrev_b32_e32 v34, 16, v30
	v_and_b32_e32 v35, 0xffff0000, v30
	v_lshlrev_b32_e32 v26, 16, v27
	v_and_b32_e32 v27, 0xffff0000, v27
	v_lshlrev_b32_e32 v30, 16, v31
	v_and_b32_e32 v31, 0xffff0000, v31
	v_pk_add_f32 v[28:29], v[28:29], v[34:35]
	v_pk_add_f32 v[26:27], v[26:27], v[30:31]
	v_pk_add_f32 v[16:17], v[16:17], v[24:25]
	v_pk_add_f32 v[14:15], v[14:15], v[32:33]
	v_pk_add_f32 v[24:25], v[12:13], v[26:27]
	v_pk_add_f32 v[26:27], v[10:11], v[28:29]
	v_cvt_pk_bf16_f32 v10, v14, v15
	v_cvt_pk_bf16_f32 v11, v16, v17
	s_nop 0
	v_cvt_pk_bf16_f32 v12, v26, v27
	v_cvt_pk_bf16_f32 v13, v24, v25
	global_store_dwordx4 v[22:23], v[10:13], off sc1
	v_lshlrev_b32_e32 v28, 16, v10
	v_lshlrev_b32_e32 v29, 16, v11
	v_and_b32_e32 v10, 0xffff0000, v10
	v_and_b32_e32 v11, 0xffff0000, v11
	v_sub_f32_e32 v10, v15, v10
	v_sub_f32_e32 v11, v17, v11
	v_lshlrev_b32_e32 v30, 16, v12
	v_and_b32_e32 v12, 0xffff0000, v12
	v_lshlrev_b32_e32 v31, 16, v13
	v_and_b32_e32 v13, 0xffff0000, v13
	v_sub_f32_e32 v28, v14, v28
	v_sub_f32_e32 v29, v16, v29
	v_sub_f32_e32 v12, v27, v12
	v_sub_f32_e32 v13, v25, v13
	v_cvt_pk_bf16_f32 v10, v28, v10
	v_cvt_pk_bf16_f32 v11, v29, v11
	v_sub_f32_e32 v30, v26, v30
	v_sub_f32_e32 v31, v24, v31
	v_cvt_pk_bf16_f32 v12, v30, v12
	v_cvt_pk_bf16_f32 v13, v31, v13
	global_store_dwordx4 v[20:21], v[10:13], off sc1
	s_nop 1
	v_mul_f32_e32 v10, v14, v14
	v_mul_f32_e32 v11, v16, v16
	v_fmac_f32_e32 v10, v15, v15
	v_fmac_f32_e32 v11, v17, v17
	v_add_f32_e32 v10, v11, v10
	v_mul_f32_e32 v11, v26, v26
	v_fmac_f32_e32 v11, v27, v27
	v_add_f32_e32 v10, v11, v10
	v_mul_f32_e32 v11, v25, v25
	v_fmac_f32_e32 v11, v24, v24
	v_add_f32_e32 v28, v11, v10
	global_load_dwordx4 v[10:13], v[22:23], off offset:256
	global_load_dwordx4 v[14:17], v[20:21], off offset:256
	s_waitcnt vmcnt(1)
	v_lshlrev_b32_e32 v24, 16, v10
	v_and_b32_e32 v25, 0xffff0000, v10
	s_waitcnt vmcnt(0)
	v_lshlrev_b32_e32 v26, 16, v14
	v_and_b32_e32 v27, 0xffff0000, v14
	v_lshlrev_b32_e32 v10, 16, v11
	v_and_b32_e32 v11, 0xffff0000, v11
	v_lshlrev_b32_e32 v14, 16, v15
	v_and_b32_e32 v15, 0xffff0000, v15
	v_pk_add_f32 v[24:25], v[24:25], v[26:27]
	v_pk_add_f32 v[10:11], v[10:11], v[14:15]
	v_lshlrev_b32_e32 v14, 16, v12
	v_and_b32_e32 v15, 0xffff0000, v12
	v_lshlrev_b32_e32 v26, 16, v16
	v_and_b32_e32 v27, 0xffff0000, v16
	v_lshlrev_b32_e32 v12, 16, v13
	v_and_b32_e32 v13, 0xffff0000, v13
	v_lshlrev_b32_e32 v16, 16, v17
	v_and_b32_e32 v17, 0xffff0000, v17
	v_pk_add_f32 v[14:15], v[14:15], v[26:27]
	v_pk_add_f32 v[12:13], v[12:13], v[16:17]
	v_pk_add_f32 v[6:7], v[6:7], v[10:11]
	v_pk_add_f32 v[4:5], v[4:5], v[24:25]
	v_pk_add_f32 v[10:11], v[2:3], v[12:13]
	v_pk_add_f32 v[12:13], v[0:1], v[14:15]
	v_cvt_pk_bf16_f32 v0, v4, v5
	v_cvt_pk_bf16_f32 v1, v6, v7
	s_nop 0
	v_cvt_pk_bf16_f32 v2, v12, v13
	v_cvt_pk_bf16_f32 v3, v10, v11
	global_store_dwordx4 v[22:23], v[0:3], off offset:256 sc1
	v_lshlrev_b32_e32 v14, 16, v0
	v_lshlrev_b32_e32 v15, 16, v1
	v_and_b32_e32 v0, 0xffff0000, v0
	v_and_b32_e32 v1, 0xffff0000, v1
	v_sub_f32_e32 v0, v5, v0
	v_sub_f32_e32 v1, v7, v1
	v_lshlrev_b32_e32 v16, 16, v2
	v_and_b32_e32 v2, 0xffff0000, v2
	v_lshlrev_b32_e32 v17, 16, v3
	v_and_b32_e32 v3, 0xffff0000, v3
	v_sub_f32_e32 v14, v4, v14
	v_sub_f32_e32 v15, v6, v15
	v_sub_f32_e32 v2, v13, v2
	v_sub_f32_e32 v3, v11, v3
	v_cvt_pk_bf16_f32 v0, v14, v0
	v_cvt_pk_bf16_f32 v1, v15, v1
	v_sub_f32_e32 v16, v12, v16
	v_sub_f32_e32 v17, v10, v17
	v_cvt_pk_bf16_f32 v2, v16, v2
	v_cvt_pk_bf16_f32 v3, v17, v3
	global_store_dwordx4 v[20:21], v[0:3], off offset:256 sc1
	s_nop 1
	v_mul_f32_e32 v0, v4, v4
	v_mul_f32_e32 v1, v6, v6
	v_fmac_f32_e32 v0, v5, v5
	v_fmac_f32_e32 v1, v7, v7
	v_add_f32_e32 v0, v1, v0
	v_mul_f32_e32 v1, v12, v12
	v_fmac_f32_e32 v1, v13, v13
	v_add_f32_e32 v0, v1, v0
	v_mul_f32_e32 v1, v11, v11
	v_fmac_f32_e32 v1, v10, v10
	v_add_f32_e32 v0, v1, v0
	v_add_f32_e32 v0, v28, v0
	ds_bpermute_b32 v1, v151, v0
	s_waitcnt lgkmcnt(0)
	v_add_f32_e32 v0, v0, v1
	ds_bpermute_b32 v1, v150, v0
	s_and_saveexec_b64 s[24:25], vcc
	s_cbranch_execz .LBB0_1097
	v_lshlrev_b64 v[2:3], 7, v[18:19]
	v_lshl_add_u64 v[2:3], s[10:11], 0, v[2:3]
	v_lshl_add_u64 v[2:3], s[22:23], 2, v[2:3]
	s_lshl_b32 s96, s46, 2
	v_lshl_add_u64 v[2:3], v[2:3], 0, s[96:97]
	s_waitcnt lgkmcnt(0)
	v_add_f32_e32 v0, v0, v1
	global_store_dword v[2:3], v0, off

;     __device__ __forceinline__ void operator()(AccRef acc, const Unit& u, int wr, int wc, int, int) const {
;         const int ln_ = fresh_lane(), fr = ln_ & 15, fq = ln_ >> 4;
;         const int row0 = u.pm * 256 + wr * 64 + fr, col0 = u.pn * 256 + wc * 32 + 8 * fq;
; #pragma unroll
;         for (int ai = 0; ai < 2; ++ai)
; #pragma unroll
;             for (int m = 0; m < 4; ++m) {
;                 const int row = row0 + ai * 128 + m * 16; float s = 0.f;
; #pragma unroll
;                 for (int bj = 0; bj < 2; ++bj) {
;                     const size_t p = (size_t)row * D + col0 + bj * 128;
;                     f32x4 x0, x1;
;                     if (xin32) { x0 = *(const f32x4*)(xin32 + p); x1 = *(const f32x4*)(xin32 + p + 4); }
;                     else { const v4u h = *(const v4u*)(xb + p), lo = *(const v4u*)(xl + p);
;                         x0 = (f32x4){bflo(h.x) + bflo(lo.x), bfhi(h.x) + bfhi(lo.x), bflo(h.y) + bflo(lo.y), bfhi(h.y) + bfhi(lo.y)};
;                         x1 = (f32x4){bflo(h.z) + bflo(lo.z), bfhi(h.z) + bfhi(lo.z), bflo(h.w) + bflo(lo.w), bfhi(h.w) + bfhi(lo.w)}; }
;                     x0 = x0 + alpha * acc[ai][bj][m][0]; x1 = x1 + alpha * acc[ai][bj][m][1];
;                     if (PROBE_ON) { x0 = x0 * pscale; x1 = x1 * pscale; if (p == 0) x0[0] += pspike; }
;                     if (xout32) { *(f32x4*)(xout32 + p) = x0; *(f32x4*)(xout32 + p + 4) = x1; }
;                     else {
;                         v4u w; w.x = cvt_pk_bf16(x0[0], x0[1]); w.y = cvt_pk_bf16(x0[2], x0[3]); w.z = cvt_pk_bf16(x1[0], x1[1]); w.w = cvt_pk_bf16(x1[2], x1[3]);
;                         *(v4u*)(xb + p) = w;
;                         const f32x4 r0 = {x0[0] - bflo(w.x), x0[1] - bfhi(w.x), x0[2] - bflo(w.y), x0[3] - bfhi(w.y)}, r1 = {x1[0] - bflo(w.z), x1[1] - bfhi(w.z), x1[2] - bflo(w.w), x1[3] - bfhi(w.w)};
;                         v4u q; q.x = cvt_pk_bf16(r0[0], r0[1]); q.y = cvt_pk_bf16(r0[2], r0[3]); q.z = cvt_pk_bf16(r1[0], r1[1]); q.w = cvt_pk_bf16(r1[2], r1[3]);
;                         *(v4u*)(xl + p) = q;
;                     }
;                     s += (x0[0] * x0[0] + x0[1] * x0[1]) + (x0[2] * x0[2] + x0[3] * x0[3]) + (x1[0] * x1[0] + x1[1] * x1[1]) + (x1[2] * x1[2] + x1[3] * x1[3]);
.LBB0_1213:
	s_lshl_b32 s2, s54, 8
	s_add_i32 s2, s2, s45
	v_mbcnt_lo_u32_b32 v152, -1, 0
	v_mbcnt_hi_u32_b32 v152, -1, v152
	v_cndmask_b32_e64 v153, 0, 1, s[20:21]
	v_and_or_b32 v142, v152, 15, s2
	s_lshl_b32 s2, s33, 8
	v_ashrrev_i32_e32 v140, 1, v152
	s_or_b32 s2, s2, s46
	v_and_b32_e32 v140, -8, v140
	v_add_u32_e32 v140, s2, v140
	v_ashrrev_i32_e32 v143, 31, v142
	v_ashrrev_i32_e32 v141, 31, v140
	v_lshlrev_b64 v[144:145], 11, v[142:143]
	v_lshl_add_u64 v[148:149], v[144:145], 0, v[140:141]
	v_lshlrev_b64 v[144:145], 1, v[148:149]
	v_lshl_add_u64 v[146:147], s[12:13], 0, v[144:145]
	v_lshl_add_u64 v[144:145], s[14:15], 0, v[144:145]
	global_load_dwordx4 v[154:157], v[146:147], off
	global_load_dwordx4 v[158:161], v[144:145], off
	v_cmp_ne_u32_e64 s[6:7], 1, v153
	s_andn2_b64 vcc, exec, s[20:21]
	v_lshl_add_u64 v[148:149], v[148:149], 2, s[0:1]
	s_waitcnt vmcnt(0)
	v_lshlrev_b32_e32 v162, 16, v154
	v_and_b32_e32 v163, 0xffff0000, v154
	v_lshlrev_b32_e32 v164, 16, v158
	v_and_b32_e32 v165, 0xffff0000, v158
	v_lshlrev_b32_e32 v154, 16, v155
	v_and_b32_e32 v155, 0xffff0000, v155
	v_lshlrev_b32_e32 v158, 16, v159
	v_and_b32_e32 v159, 0xffff0000, v159
	v_pk_add_f32 v[162:163], v[162:163], v[164:165]
	v_pk_add_f32 v[154:155], v[154:155], v[158:159]
	v_lshlrev_b32_e32 v158, 16, v156
	v_and_b32_e32 v159, 0xffff0000, v156
	v_lshlrev_b32_e32 v164, 16, v160
	v_and_b32_e32 v165, 0xffff0000, v160
	v_lshlrev_b32_e32 v156, 16, v157
	v_and_b32_e32 v157, 0xffff0000, v157
	v_lshlrev_b32_e32 v160, 16, v161
	v_and_b32_e32 v161, 0xffff0000, v161
	v_pk_add_f32 v[158:159], v[158:159], v[164:165]
	v_pk_add_f32 v[156:157], v[156:157], v[160:161]
	v_pk_fma_f32 v[128:129], v[128:129], 0.5, v[154:155] op_sel_hi:[1,0,1]
	v_pk_fma_f32 v[126:127], v[126:127], 0.5, v[162:163] op_sel_hi:[1,0,1]
	v_pk_fma_f32 v[124:125], v[124:125], 0.5, v[156:157] op_sel_hi:[1,0,1]
	v_pk_fma_f32 v[122:123], v[122:123], 0.5, v[158:159] op_sel_hi:[1,0,1]
	s_cbranch_vccnz .LBB0_1280
	global_store_dwordx4 v[148:149], v[126:129], off sc1
	global_store_dwordx4 v[148:149], v[122:125], off offset:16 sc1
	s_cbranch_execnz .LBB0_1216
.LBB0_1215:
	v_cvt_pk_bf16_f32 v154, v126, v127
	v_cvt_pk_bf16_f32 v155, v128, v129
	v_cvt_pk_bf16_f32 v156, v122, v123
	v_cvt_pk_bf16_f32 v157, v124, v125
	global_store_dwordx4 v[146:147], v[154:157], off sc1
	v_lshlrev_b32_e32 v153, 16, v154
	v_lshlrev_b32_e32 v158, 16, v155
	v_and_b32_e32 v154, 0xffff0000, v154
	v_and_b32_e32 v155, 0xffff0000, v155
	v_lshlrev_b32_e32 v159, 16, v156
	v_and_b32_e32 v156, 0xffff0000, v156
	v_lshlrev_b32_e32 v160, 16, v157
	v_and_b32_e32 v157, 0xffff0000, v157
	v_sub_f32_e32 v154, v127, v154
	v_sub_f32_e32 v155, v129, v155
	v_sub_f32_e32 v156, v123, v156
	v_sub_f32_e32 v157, v125, v157
	v_sub_f32_e32 v153, v126, v153
	v_sub_f32_e32 v158, v128, v158
	v_sub_f32_e32 v159, v122, v159
	v_sub_f32_e32 v160, v124, v160
	v_cvt_pk_bf16_f32 v154, v153, v154
	v_cvt_pk_bf16_f32 v155, v158, v155
	v_cvt_pk_bf16_f32 v156, v159, v156
	v_cvt_pk_bf16_f32 v157, v160, v157
	global_store_dwordx4 v[144:145], v[154:157], off sc1
.LBB0_1216:
	global_load_dwordx4 v[154:157], v[146:147], off offset:256
	s_nop 0
	global_load_dwordx4 v[158:161], v[144:145], off offset:256
	s_and_b64 vcc, exec, s[6:7]
	s_waitcnt vmcnt(1)
	v_lshlrev_b32_e32 v162, 16, v154
	v_and_b32_e32 v163, 0xffff0000, v154
	s_waitcnt vmcnt(0)
	v_lshlrev_b32_e32 v164, 16, v158
	v_and_b32_e32 v165, 0xffff0000, v158
	v_lshlrev_b32_e32 v154, 16, v155
	v_and_b32_e32 v155, 0xffff0000, v155
	v_lshlrev_b32_e32 v158, 16, v159
	v_and_b32_e32 v159, 0xffff0000, v159
	v_pk_add_f32 v[162:163], v[162:163], v[164:165]
	v_pk_add_f32 v[154:155], v[154:155], v[158:159]
	v_lshlrev_b32_e32 v158, 16, v156
	v_and_b32_e32 v159, 0xffff0000, v156
	v_lshlrev_b32_e32 v164, 16, v160
	v_and_b32_e32 v165, 0xffff0000, v160
	v_lshlrev_b32_e32 v156, 16, v157
	v_and_b32_e32 v157, 0xffff0000, v157
	v_lshlrev_b32_e32 v160, 16, v161
	v_and_b32_e32 v161, 0xffff0000, v161
	v_pk_add_f32 v[158:159], v[158:159], v[164:165]
	v_pk_add_f32 v[156:157], v[156:157], v[160:161]
	v_pk_fma_f32 v[120:121], v[120:121], 0.5, v[154:155] op_sel_hi:[1,0,1]
	v_pk_fma_f32 v[118:119], v[118:119], 0.5, v[162:163] op_sel_hi:[1,0,1]
	v_pk_fma_f32 v[116:117], v[116:117], 0.5, v[156:157] op_sel_hi:[1,0,1]
	v_pk_fma_f32 v[114:115], v[114:115], 0.5, v[158:159] op_sel_hi:[1,0,1]
	s_cbranch_vccnz .LBB0_1281
	global_store_dwordx4 v[148:149], v[118:121], off offset:512 sc1
	global_store_dwordx4 v[148:149], v[114:117], off offset:528 sc1
	s_cbranch_execnz .LBB0_1219
.LBB0_1218:
	v_cvt_pk_bf16_f32 v154, v118, v119
	v_cvt_pk_bf16_f32 v155, v120, v121
	v_cvt_pk_bf16_f32 v156, v114, v115
	v_cvt_pk_bf16_f32 v157, v116, v117
	global_store_dwordx4 v[146:147], v[154:157], off offset:256 sc1
	v_lshlrev_b32_e32 v146, 16, v154
	v_and_b32_e32 v147, 0xffff0000, v154
	v_lshlrev_b32_e32 v148, 16, v155
	v_and_b32_e32 v149, 0xffff0000, v155
	v_sub_f32_e32 v146, v118, v146
	v_sub_f32_e32 v147, v119, v147
	v_sub_f32_e32 v148, v120, v148
	v_sub_f32_e32 v149, v121, v149
	v_lshlrev_b32_e32 v153, 16, v156
	v_and_b32_e32 v154, 0xffff0000, v156
	v_lshlrev_b32_e32 v155, 16, v157
	v_and_b32_e32 v156, 0xffff0000, v157
	v_sub_f32_e32 v153, v114, v153
	v_sub_f32_e32 v154, v115, v154
	v_sub_f32_e32 v155, v116, v155
	v_sub_f32_e32 v156, v117, v156
	v_cvt_pk_bf16_f32 v146, v146, v147
	v_cvt_pk_bf16_f32 v147, v148, v149
	v_cvt_pk_bf16_f32 v148, v153, v154
	v_cvt_pk_bf16_f32 v149, v155, v156
	global_store_dwordx4 v[144:145], v[146:149], off offset:256 sc1

; __device__ __forceinline__ unsigned cvt_pk_bf16(float lo, float hi) { unsigned r; asm volatile("v_cvt_pk_bf16_f32 %0, %1, %2" : "=v"(r) : "v"(lo), "v"(hi)); return r; }
;     __device__ __forceinline__ void operator()(AccRef acc, const Unit& u, int wr, int wc, int, int) const {
;     ...
;                 const int row = row0 + ai * 128 + m * 16; float s = 0.f;
; #pragma unroll
;                 for (int bj = 0; bj < 2; ++bj) {
;                     const size_t p = (size_t)row * D + col0 + bj * 128;
;                     f32x4 x0, x1;
;                     if (xin32) { x0 = *(const f32x4*)(xin32 + p); x1 = *(const f32x4*)(xin32 + p + 4); }
;                     else { const v4u h = *(const v4u*)(xb + p), lo = *(const v4u*)(xl + p);
;                         x0 = (f32x4){bflo(h.x) + bflo(lo.x), bfhi(h.x) + bfhi(lo.x), bflo(h.y) + bflo(lo.y), bfhi(h.y) + bfhi(lo.y)};
;                         x1 = (f32x4){bflo(h.z) + bflo(lo.z), bfhi(h.z) + bfhi(lo.z), bflo(h.w) + bflo(lo.w), bfhi(h.w) + bfhi(lo.w)}; }
;                     x0 = x0 + alpha * acc[ai][bj][m][0]; x1 = x1 + alpha * acc[ai][bj][m][1];
;                     if (PROBE_ON) { x0 = x0 * pscale; x1 = x1 * pscale; if (p == 0) x0[0] += pspike; }
;                     if (xout32) { *(f32x4*)(xout32 + p) = x0; *(f32x4*)(xout32 + p + 4) = x1; }
;                     else {
;                         v4u w; w.x = cvt_pk_bf16(x0[0], x0[1]); w.y = cvt_pk_bf16(x0[2], x0[3]); w.z = cvt_pk_bf16(x1[0], x1[1]); w.w = cvt_pk_bf16(x1[2], x1[3]);
;                         *(v4u*)(xb + p) = w;
;                         const f32x4 r0 = {x0[0] - bflo(w.x), x0[1] - bfhi(w.x), x0[2] - bflo(w.y), x0[3] - bfhi(w.y)}, r1 = {x1[0] - bflo(w.z), x1[1] - bfhi(w.z), x1[2] - bflo(w.w), x1[3] - bfhi(w.w)};
;                         v4u q; q.x = cvt_pk_bf16(r0[0], r0[1]); q.y = cvt_pk_bf16(r0[2], r0[3]); q.z = cvt_pk_bf16(r1[0], r1[1]); q.w = cvt_pk_bf16(r1[2], r1[3]);
;                         *(v4u*)(xl + p) = q;
;                     }
;                     s += (x0[0] * x0[0] + x0[1] * x0[1]) + (x0[2] * x0[2] + x0[3] * x0[3]) + (x1[0] * x1[0] + x1[1] * x1[1]) + (x1[2] * x1[2] + x1[3] * x1[3]);
.LBB0_1221:
	s_or_b64 exec, exec, s[28:29]
	v_or_b32_e32 v114, 16, v142
	s_waitcnt lgkmcnt(0)
	v_ashrrev_i32_e32 v115, 31, v114
	v_lshlrev_b64 v[116:117], 11, v[114:115]
	v_lshl_add_u64 v[120:121], v[116:117], 0, v[140:141]
	v_lshlrev_b64 v[116:117], 1, v[120:121]
	v_lshl_add_u64 v[118:119], s[12:13], 0, v[116:117]
	v_lshl_add_u64 v[116:117], s[14:15], 0, v[116:117]
	global_load_dwordx4 v[124:127], v[118:119], off
	global_load_dwordx4 v[144:147], v[116:117], off
	s_and_b64 vcc, exec, s[6:7]
	v_lshl_add_u64 v[120:121], v[120:121], 2, s[0:1]
	s_waitcnt vmcnt(1)
	v_lshlrev_b32_e32 v128, 16, v124
	v_and_b32_e32 v129, 0xffff0000, v124
	s_waitcnt vmcnt(0)
	v_lshlrev_b32_e32 v148, 16, v144
	v_and_b32_e32 v149, 0xffff0000, v144
	v_lshlrev_b32_e32 v124, 16, v125
	v_and_b32_e32 v125, 0xffff0000, v125
	v_lshlrev_b32_e32 v144, 16, v145
	v_and_b32_e32 v145, 0xffff0000, v145
	v_pk_add_f32 v[128:129], v[128:129], v[148:149]
	v_pk_add_f32 v[124:125], v[124:125], v[144:145]
	v_lshlrev_b32_e32 v144, 16, v126
	v_and_b32_e32 v145, 0xffff0000, v126
	v_lshlrev_b32_e32 v148, 16, v146
	v_and_b32_e32 v149, 0xffff0000, v146
	v_lshlrev_b32_e32 v126, 16, v127
	v_and_b32_e32 v127, 0xffff0000, v127
	v_lshlrev_b32_e32 v146, 16, v147
	v_and_b32_e32 v147, 0xffff0000, v147
	v_pk_add_f32 v[144:145], v[144:145], v[148:149]
	v_pk_add_f32 v[126:127], v[126:127], v[146:147]
	v_pk_fma_f32 v[112:113], v[112:113], 0.5, v[124:125] op_sel_hi:[1,0,1]
	v_pk_fma_f32 v[110:111], v[110:111], 0.5, v[128:129] op_sel_hi:[1,0,1]
	v_pk_fma_f32 v[108:109], v[108:109], 0.5, v[126:127] op_sel_hi:[1,0,1]
	v_pk_fma_f32 v[106:107], v[106:107], 0.5, v[144:145] op_sel_hi:[1,0,1]
	s_cbranch_vccnz .LBB0_1282
	global_store_dwordx4 v[120:121], v[110:113], off sc1
	global_store_dwordx4 v[120:121], v[106:109], off offset:16 sc1
	s_cbranch_execnz .LBB0_1224
.LBB0_1223:
	v_cvt_pk_bf16_f32 v124, v110, v111
	v_cvt_pk_bf16_f32 v125, v112, v113
	v_cvt_pk_bf16_f32 v126, v106, v107
	v_cvt_pk_bf16_f32 v127, v108, v109
	global_store_dwordx4 v[118:119], v[124:127], off sc1
	v_lshlrev_b32_e32 v128, 16, v124
	v_lshlrev_b32_e32 v129, 16, v125
	v_and_b32_e32 v124, 0xffff0000, v124
	v_and_b32_e32 v125, 0xffff0000, v125
	v_lshlrev_b32_e32 v143, 16, v126
	v_and_b32_e32 v126, 0xffff0000, v126
	v_lshlrev_b32_e32 v144, 16, v127
	v_and_b32_e32 v127, 0xffff0000, v127
	v_sub_f32_e32 v124, v111, v124
	v_sub_f32_e32 v125, v113, v125
	v_sub_f32_e32 v126, v107, v126
	v_sub_f32_e32 v127, v109, v127
	v_sub_f32_e32 v128, v110, v128
	v_sub_f32_e32 v129, v112, v129
	v_sub_f32_e32 v143, v106, v143
	v_sub_f32_e32 v144, v108, v144
	v_cvt_pk_bf16_f32 v124, v128, v124
	v_cvt_pk_bf16_f32 v125, v129, v125
	v_cvt_pk_bf16_f32 v126, v143, v126
	v_cvt_pk_bf16_f32 v127, v144, v127
	global_store_dwordx4 v[116:117], v[124:127], off sc1
.LBB0_1224:
	global_load_dwordx4 v[124:127], v[118:119], off offset:256
	s_nop 0
	global_load_dwordx4 v[144:147], v[116:117], off offset:256
	s_and_b64 vcc, exec, s[6:7]
	s_waitcnt vmcnt(1)
	v_lshlrev_b32_e32 v128, 16, v124
	v_and_b32_e32 v129, 0xffff0000, v124
	s_waitcnt vmcnt(0)
	v_lshlrev_b32_e32 v148, 16, v144
	v_and_b32_e32 v149, 0xffff0000, v144
	v_lshlrev_b32_e32 v124, 16, v125
	v_and_b32_e32 v125, 0xffff0000, v125
	v_lshlrev_b32_e32 v144, 16, v145
	v_and_b32_e32 v145, 0xffff0000, v145
	v_pk_add_f32 v[128:129], v[128:129], v[148:149]
	v_pk_add_f32 v[124:125], v[124:125], v[144:145]
	v_lshlrev_b32_e32 v144, 16, v126
	v_and_b32_e32 v145, 0xffff0000, v126
	v_lshlrev_b32_e32 v148, 16, v146
	v_and_b32_e32 v149, 0xffff0000, v146
	v_lshlrev_b32_e32 v126, 16, v127
	v_and_b32_e32 v127, 0xffff0000, v127
	v_lshlrev_b32_e32 v146, 16, v147
	v_and_b32_e32 v147, 0xffff0000, v147
	v_pk_add_f32 v[144:145], v[144:145], v[148:149]
	v_pk_add_f32 v[126:127], v[126:127], v[146:147]
	v_pk_fma_f32 v[104:105], v[104:105], 0.5, v[124:125] op_sel_hi:[1,0,1]
	v_pk_fma_f32 v[102:103], v[102:103], 0.5, v[128:129] op_sel_hi:[1,0,1]
	v_pk_fma_f32 v[100:101], v[100:101], 0.5, v[126:127] op_sel_hi:[1,0,1]
	v_pk_fma_f32 v[98:99], v[98:99], 0.5, v[144:145] op_sel_hi:[1,0,1]
	s_cbranch_vccnz .LBB0_1283
	global_store_dwordx4 v[120:121], v[102:105], off offset:512 sc1
	global_store_dwordx4 v[120:121], v[98:101], off offset:528 sc1
	s_cbranch_execnz .LBB0_1227
.LBB0_1226:
	v_cvt_pk_bf16_f32 v124, v102, v103
	v_cvt_pk_bf16_f32 v125, v104, v105
	v_cvt_pk_bf16_f32 v126, v98, v99
	v_cvt_pk_bf16_f32 v127, v100, v101
	global_store_dwordx4 v[118:119], v[124:127], off offset:256 sc1
	v_lshlrev_b32_e32 v118, 16, v124
	v_and_b32_e32 v119, 0xffff0000, v124
	v_lshlrev_b32_e32 v120, 16, v125
	v_and_b32_e32 v121, 0xffff0000, v125
	v_sub_f32_e32 v118, v102, v118
	v_sub_f32_e32 v119, v103, v119
	v_sub_f32_e32 v120, v104, v120
	v_sub_f32_e32 v121, v105, v121
	v_lshlrev_b32_e32 v124, 16, v126
	v_and_b32_e32 v125, 0xffff0000, v126
	v_lshlrev_b32_e32 v126, 16, v127
	v_and_b32_e32 v127, 0xffff0000, v127
	v_sub_f32_e32 v124, v98, v124
	v_sub_f32_e32 v125, v99, v125
	v_sub_f32_e32 v126, v100, v126
	v_sub_f32_e32 v127, v101, v127
	v_cvt_pk_bf16_f32 v118, v118, v119
	v_cvt_pk_bf16_f32 v119, v120, v121
	v_cvt_pk_bf16_f32 v120, v124, v125
	v_cvt_pk_bf16_f32 v121, v126, v127
	global_store_dwordx4 v[116:117], v[118:121], off offset:256 sc1

; __device__ __forceinline__ unsigned cvt_pk_bf16(float lo, float hi) { unsigned r; asm volatile("v_cvt_pk_bf16_f32 %0, %1, %2" : "=v"(r) : "v"(lo), "v"(hi)); return r; }
;     __device__ __forceinline__ void operator()(AccRef acc, const Unit& u, int wr, int wc, int, int) const {
;     ...
;                 const int row = row0 + ai * 128 + m * 16; float s = 0.f;
; #pragma unroll
;                 for (int bj = 0; bj < 2; ++bj) {
;                     const size_t p = (size_t)row * D + col0 + bj * 128;
;                     f32x4 x0, x1;
;                     if (xin32) { x0 = *(const f32x4*)(xin32 + p); x1 = *(const f32x4*)(xin32 + p + 4); }
;                     else { const v4u h = *(const v4u*)(xb + p), lo = *(const v4u*)(xl + p);
;                         x0 = (f32x4){bflo(h.x) + bflo(lo.x), bfhi(h.x) + bfhi(lo.x), bflo(h.y) + bflo(lo.y), bfhi(h.y) + bfhi(lo.y)};
;                         x1 = (f32x4){bflo(h.z) + bflo(lo.z), bfhi(h.z) + bfhi(lo.z), bflo(h.w) + bflo(lo.w), bfhi(h.w) + bfhi(lo.w)}; }
;                     x0 = x0 + alpha * acc[ai][bj][m][0]; x1 = x1 + alpha * acc[ai][bj][m][1];
;                     if (PROBE_ON) { x0 = x0 * pscale; x1 = x1 * pscale; if (p == 0) x0[0] += pspike; }
;                     if (xout32) { *(f32x4*)(xout32 + p) = x0; *(f32x4*)(xout32 + p + 4) = x1; }
;                     else {
;                         v4u w; w.x = cvt_pk_bf16(x0[0], x0[1]); w.y = cvt_pk_bf16(x0[2], x0[3]); w.z = cvt_pk_bf16(x1[0], x1[1]); w.w = cvt_pk_bf16(x1[2], x1[3]);
;                         *(v4u*)(xb + p) = w;
;                         const f32x4 r0 = {x0[0] - bflo(w.x), x0[1] - bfhi(w.x), x0[2] - bflo(w.y), x0[3] - bfhi(w.y)}, r1 = {x1[0] - bflo(w.z), x1[1] - bfhi(w.z), x1[2] - bflo(w.w), x1[3] - bfhi(w.w)};
;                         v4u q; q.x = cvt_pk_bf16(r0[0], r0[1]); q.y = cvt_pk_bf16(r0[2], r0[3]); q.z = cvt_pk_bf16(r1[0], r1[1]); q.w = cvt_pk_bf16(r1[2], r1[3]);
;                         *(v4u*)(xl + p) = q;
;                     }
;                     s += (x0[0] * x0[0] + x0[1] * x0[1]) + (x0[2] * x0[2] + x0[3] * x0[3]) + (x1[0] * x1[0] + x1[1] * x1[1]) + (x1[2] * x1[2] + x1[3] * x1[3]);
.LBB0_1229:
	s_or_b64 exec, exec, s[28:29]
	v_or_b32_e32 v98, 32, v142
	s_waitcnt lgkmcnt(0)
	v_ashrrev_i32_e32 v99, 31, v98
	v_lshlrev_b64 v[100:101], 11, v[98:99]
	v_lshl_add_u64 v[112:113], v[100:101], 0, v[140:141]
	v_lshlrev_b64 v[100:101], 1, v[112:113]
	v_lshl_add_u64 v[102:103], s[12:13], 0, v[100:101]
	v_lshl_add_u64 v[100:101], s[14:15], 0, v[100:101]
	global_load_dwordx4 v[104:107], v[102:103], off
	global_load_dwordx4 v[108:111], v[100:101], off
	s_and_b64 vcc, exec, s[6:7]
	s_waitcnt vmcnt(1)
	v_lshlrev_b32_e32 v114, 16, v104
	v_and_b32_e32 v115, 0xffff0000, v104
	s_waitcnt vmcnt(0)
	v_lshlrev_b32_e32 v116, 16, v108
	v_and_b32_e32 v117, 0xffff0000, v108
	v_lshlrev_b32_e32 v104, 16, v105
	v_and_b32_e32 v105, 0xffff0000, v105
	v_lshlrev_b32_e32 v108, 16, v109
	v_and_b32_e32 v109, 0xffff0000, v109
	v_pk_add_f32 v[114:115], v[114:115], v[116:117]
	v_pk_add_f32 v[104:105], v[104:105], v[108:109]
	v_lshlrev_b32_e32 v108, 16, v106
	v_and_b32_e32 v109, 0xffff0000, v106
	v_lshlrev_b32_e32 v116, 16, v110
	v_and_b32_e32 v117, 0xffff0000, v110
	v_lshlrev_b32_e32 v106, 16, v107
	v_and_b32_e32 v107, 0xffff0000, v107
	v_lshlrev_b32_e32 v110, 16, v111
	v_and_b32_e32 v111, 0xffff0000, v111
	v_pk_add_f32 v[108:109], v[108:109], v[116:117]
	v_pk_add_f32 v[106:107], v[106:107], v[110:111]
	v_pk_fma_f32 v[96:97], v[96:97], 0.5, v[104:105] op_sel_hi:[1,0,1]
	v_pk_fma_f32 v[94:95], v[94:95], 0.5, v[114:115] op_sel_hi:[1,0,1]
	v_pk_fma_f32 v[92:93], v[92:93], 0.5, v[106:107] op_sel_hi:[1,0,1]
	v_pk_fma_f32 v[90:91], v[90:91], 0.5, v[108:109] op_sel_hi:[1,0,1]
	v_lshl_add_u64 v[104:105], v[112:113], 2, s[0:1]
	s_cbranch_vccnz .LBB0_1284
	global_store_dwordx4 v[104:105], v[94:97], off sc1
	global_store_dwordx4 v[104:105], v[90:93], off offset:16 sc1
	s_cbranch_execnz .LBB0_1232
.LBB0_1231:
	v_cvt_pk_bf16_f32 v106, v94, v95
	v_cvt_pk_bf16_f32 v107, v96, v97
	v_cvt_pk_bf16_f32 v108, v90, v91
	v_cvt_pk_bf16_f32 v109, v92, v93
	global_store_dwordx4 v[102:103], v[106:109], off sc1
	v_lshlrev_b32_e32 v110, 16, v106
	v_lshlrev_b32_e32 v111, 16, v107
	v_and_b32_e32 v106, 0xffff0000, v106
	v_and_b32_e32 v107, 0xffff0000, v107
	v_lshlrev_b32_e32 v112, 16, v108
	v_and_b32_e32 v108, 0xffff0000, v108
	v_lshlrev_b32_e32 v113, 16, v109
	v_and_b32_e32 v109, 0xffff0000, v109
	v_sub_f32_e32 v106, v95, v106
	v_sub_f32_e32 v107, v97, v107
	v_sub_f32_e32 v108, v91, v108
	v_sub_f32_e32 v109, v93, v109
	v_sub_f32_e32 v110, v94, v110
	v_sub_f32_e32 v111, v96, v111
	v_sub_f32_e32 v112, v90, v112
	v_sub_f32_e32 v113, v92, v113
	v_cvt_pk_bf16_f32 v106, v110, v106
	v_cvt_pk_bf16_f32 v107, v111, v107
	v_cvt_pk_bf16_f32 v108, v112, v108
	v_cvt_pk_bf16_f32 v109, v113, v109
	global_store_dwordx4 v[100:101], v[106:109], off sc1
.LBB0_1232:
	global_load_dwordx4 v[106:109], v[102:103], off offset:256
	s_nop 0
	global_load_dwordx4 v[110:113], v[100:101], off offset:256
	s_and_b64 vcc, exec, s[6:7]
	s_waitcnt vmcnt(1)
	v_lshlrev_b32_e32 v114, 16, v106
	v_and_b32_e32 v115, 0xffff0000, v106
	s_waitcnt vmcnt(0)
	v_lshlrev_b32_e32 v116, 16, v110
	v_and_b32_e32 v117, 0xffff0000, v110
	v_lshlrev_b32_e32 v106, 16, v107
	v_and_b32_e32 v107, 0xffff0000, v107
	v_lshlrev_b32_e32 v110, 16, v111
	v_and_b32_e32 v111, 0xffff0000, v111
	v_pk_add_f32 v[114:115], v[114:115], v[116:117]
	v_pk_add_f32 v[106:107], v[106:107], v[110:111]
	v_lshlrev_b32_e32 v110, 16, v108
	v_and_b32_e32 v111, 0xffff0000, v108
	v_lshlrev_b32_e32 v116, 16, v112
	v_and_b32_e32 v117, 0xffff0000, v112
	v_lshlrev_b32_e32 v108, 16, v109
	v_and_b32_e32 v109, 0xffff0000, v109
	v_lshlrev_b32_e32 v112, 16, v113
	v_and_b32_e32 v113, 0xffff0000, v113
	v_pk_add_f32 v[110:111], v[110:111], v[116:117]
	v_pk_add_f32 v[108:109], v[108:109], v[112:113]
	v_pk_fma_f32 v[88:89], v[88:89], 0.5, v[106:107] op_sel_hi:[1,0,1]
	v_pk_fma_f32 v[86:87], v[86:87], 0.5, v[114:115] op_sel_hi:[1,0,1]
	v_pk_fma_f32 v[84:85], v[84:85], 0.5, v[108:109] op_sel_hi:[1,0,1]
	v_pk_fma_f32 v[82:83], v[82:83], 0.5, v[110:111] op_sel_hi:[1,0,1]
	s_cbranch_vccnz .LBB0_1285
	global_store_dwordx4 v[104:105], v[86:89], off offset:512 sc1
	global_store_dwordx4 v[104:105], v[82:85], off offset:528 sc1
	s_cbranch_execnz .LBB0_1235
.LBB0_1234:
	v_cvt_pk_bf16_f32 v104, v86, v87
	v_cvt_pk_bf16_f32 v105, v88, v89
	v_cvt_pk_bf16_f32 v106, v82, v83
	v_cvt_pk_bf16_f32 v107, v84, v85
	global_store_dwordx4 v[102:103], v[104:107], off offset:256 sc1
	v_lshlrev_b32_e32 v102, 16, v104
	v_and_b32_e32 v103, 0xffff0000, v104
	v_lshlrev_b32_e32 v104, 16, v105
	v_and_b32_e32 v105, 0xffff0000, v105
	v_sub_f32_e32 v102, v86, v102
	v_sub_f32_e32 v103, v87, v103
	v_sub_f32_e32 v104, v88, v104
	v_sub_f32_e32 v105, v89, v105
	v_lshlrev_b32_e32 v108, 16, v106
	v_and_b32_e32 v106, 0xffff0000, v106
	v_lshlrev_b32_e32 v109, 16, v107
	v_and_b32_e32 v107, 0xffff0000, v107
	v_sub_f32_e32 v108, v82, v108
	v_sub_f32_e32 v106, v83, v106
	v_sub_f32_e32 v109, v84, v109
	v_sub_f32_e32 v107, v85, v107
	v_cvt_pk_bf16_f32 v102, v102, v103
	v_cvt_pk_bf16_f32 v103, v104, v105
	v_cvt_pk_bf16_f32 v104, v108, v106
	v_cvt_pk_bf16_f32 v105, v109, v107
	global_store_dwordx4 v[100:101], v[102:105], off offset:256 sc1

; __device__ __forceinline__ unsigned cvt_pk_bf16(float lo, float hi) { unsigned r; asm volatile("v_cvt_pk_bf16_f32 %0, %1, %2" : "=v"(r) : "v"(lo), "v"(hi)); return r; }
;     __device__ __forceinline__ void operator()(AccRef acc, const Unit& u, int wr, int wc, int, int) const {
;     ...
;                 const int row = row0 + ai * 128 + m * 16; float s = 0.f;
; #pragma unroll
;                 for (int bj = 0; bj < 2; ++bj) {
;                     const size_t p = (size_t)row * D + col0 + bj * 128;
;                     f32x4 x0, x1;
;                     if (xin32) { x0 = *(const f32x4*)(xin32 + p); x1 = *(const f32x4*)(xin32 + p + 4); }
;                     else { const v4u h = *(const v4u*)(xb + p), lo = *(const v4u*)(xl + p);
;                         x0 = (f32x4){bflo(h.x) + bflo(lo.x), bfhi(h.x) + bfhi(lo.x), bflo(h.y) + bflo(lo.y), bfhi(h.y) + bfhi(lo.y)};
;                         x1 = (f32x4){bflo(h.z) + bflo(lo.z), bfhi(h.z) + bfhi(lo.z), bflo(h.w) + bflo(lo.w), bfhi(h.w) + bfhi(lo.w)}; }
;                     x0 = x0 + alpha * acc[ai][bj][m][0]; x1 = x1 + alpha * acc[ai][bj][m][1];
;                     if (PROBE_ON) { x0 = x0 * pscale; x1 = x1 * pscale; if (p == 0) x0[0] += pspike; }
;                     if (xout32) { *(f32x4*)(xout32 + p) = x0; *(f32x4*)(xout32 + p + 4) = x1; }
;                     else {
;                         v4u w; w.x = cvt_pk_bf16(x0[0], x0[1]); w.y = cvt_pk_bf16(x0[2], x0[3]); w.z = cvt_pk_bf16(x1[0], x1[1]); w.w = cvt_pk_bf16(x1[2], x1[3]);
;                         *(v4u*)(xb + p) = w;
;                         const f32x4 r0 = {x0[0] - bflo(w.x), x0[1] - bfhi(w.x), x0[2] - bflo(w.y), x0[3] - bfhi(w.y)}, r1 = {x1[0] - bflo(w.z), x1[1] - bfhi(w.z), x1[2] - bflo(w.w), x1[3] - bfhi(w.w)};
;                         v4u q; q.x = cvt_pk_bf16(r0[0], r0[1]); q.y = cvt_pk_bf16(r0[2], r0[3]); q.z = cvt_pk_bf16(r1[0], r1[1]); q.w = cvt_pk_bf16(r1[2], r1[3]);
;                         *(v4u*)(xl + p) = q;
;                     }
;                     s += (x0[0] * x0[0] + x0[1] * x0[1]) + (x0[2] * x0[2] + x0[3] * x0[3]) + (x1[0] * x1[0] + x1[1] * x1[1]) + (x1[2] * x1[2] + x1[3] * x1[3]);
.LBB0_1237:
	s_or_b64 exec, exec, s[28:29]
	v_or_b32_e32 v82, 48, v142
	s_waitcnt lgkmcnt(0)
	v_ashrrev_i32_e32 v83, 31, v82
	v_lshlrev_b64 v[84:85], 11, v[82:83]
	v_lshl_add_u64 v[96:97], v[84:85], 0, v[140:141]
	v_lshlrev_b64 v[84:85], 1, v[96:97]
	v_lshl_add_u64 v[86:87], s[12:13], 0, v[84:85]
	v_lshl_add_u64 v[84:85], s[14:15], 0, v[84:85]
	global_load_dwordx4 v[88:91], v[86:87], off
	global_load_dwordx4 v[92:95], v[84:85], off
	s_and_b64 vcc, exec, s[6:7]
	s_waitcnt vmcnt(1)
	v_lshlrev_b32_e32 v98, 16, v88
	v_and_b32_e32 v99, 0xffff0000, v88
	s_waitcnt vmcnt(0)
	v_lshlrev_b32_e32 v100, 16, v92
	v_and_b32_e32 v101, 0xffff0000, v92
	v_lshlrev_b32_e32 v88, 16, v89
	v_and_b32_e32 v89, 0xffff0000, v89
	v_lshlrev_b32_e32 v92, 16, v93
	v_and_b32_e32 v93, 0xffff0000, v93
	v_pk_add_f32 v[98:99], v[98:99], v[100:101]
	v_pk_add_f32 v[88:89], v[88:89], v[92:93]
	v_lshlrev_b32_e32 v92, 16, v90
	v_and_b32_e32 v93, 0xffff0000, v90
	v_lshlrev_b32_e32 v100, 16, v94
	v_and_b32_e32 v101, 0xffff0000, v94
	v_lshlrev_b32_e32 v90, 16, v91
	v_and_b32_e32 v91, 0xffff0000, v91
	v_lshlrev_b32_e32 v94, 16, v95
	v_and_b32_e32 v95, 0xffff0000, v95
	v_pk_add_f32 v[92:93], v[92:93], v[100:101]
	v_pk_add_f32 v[90:91], v[90:91], v[94:95]
	v_pk_fma_f32 v[80:81], v[80:81], 0.5, v[88:89] op_sel_hi:[1,0,1]
	v_pk_fma_f32 v[78:79], v[78:79], 0.5, v[98:99] op_sel_hi:[1,0,1]
	v_pk_fma_f32 v[76:77], v[76:77], 0.5, v[90:91] op_sel_hi:[1,0,1]
	v_pk_fma_f32 v[74:75], v[74:75], 0.5, v[92:93] op_sel_hi:[1,0,1]
	v_lshl_add_u64 v[88:89], v[96:97], 2, s[0:1]
	s_cbranch_vccnz .LBB0_1286
	global_store_dwordx4 v[88:89], v[78:81], off sc1
	global_store_dwordx4 v[88:89], v[74:77], off offset:16 sc1
	s_cbranch_execnz .LBB0_1240
.LBB0_1239:
	v_cvt_pk_bf16_f32 v90, v78, v79
	v_cvt_pk_bf16_f32 v91, v80, v81
	v_cvt_pk_bf16_f32 v92, v74, v75
	v_cvt_pk_bf16_f32 v93, v76, v77
	global_store_dwordx4 v[86:87], v[90:93], off sc1
	v_lshlrev_b32_e32 v94, 16, v90
	v_lshlrev_b32_e32 v95, 16, v91
	v_and_b32_e32 v90, 0xffff0000, v90
	v_and_b32_e32 v91, 0xffff0000, v91
	v_lshlrev_b32_e32 v96, 16, v92
	v_and_b32_e32 v92, 0xffff0000, v92
	v_lshlrev_b32_e32 v97, 16, v93
	v_and_b32_e32 v93, 0xffff0000, v93
	v_sub_f32_e32 v90, v79, v90
	v_sub_f32_e32 v91, v81, v91
	v_sub_f32_e32 v92, v75, v92
	v_sub_f32_e32 v93, v77, v93
	v_sub_f32_e32 v94, v78, v94
	v_sub_f32_e32 v95, v80, v95
	v_sub_f32_e32 v96, v74, v96
	v_sub_f32_e32 v97, v76, v97
	v_cvt_pk_bf16_f32 v90, v94, v90
	v_cvt_pk_bf16_f32 v91, v95, v91
	v_cvt_pk_bf16_f32 v92, v96, v92
	v_cvt_pk_bf16_f32 v93, v97, v93
	global_store_dwordx4 v[84:85], v[90:93], off sc1
.LBB0_1240:
	global_load_dwordx4 v[90:93], v[86:87], off offset:256
	s_nop 0
	global_load_dwordx4 v[94:97], v[84:85], off offset:256
	s_and_b64 vcc, exec, s[6:7]
	s_waitcnt vmcnt(1)
	v_lshlrev_b32_e32 v98, 16, v90
	v_and_b32_e32 v99, 0xffff0000, v90
	s_waitcnt vmcnt(0)
	v_lshlrev_b32_e32 v100, 16, v94
	v_and_b32_e32 v101, 0xffff0000, v94
	v_lshlrev_b32_e32 v90, 16, v91
	v_and_b32_e32 v91, 0xffff0000, v91
	v_lshlrev_b32_e32 v94, 16, v95
	v_and_b32_e32 v95, 0xffff0000, v95
	v_pk_add_f32 v[98:99], v[98:99], v[100:101]
	v_pk_add_f32 v[90:91], v[90:91], v[94:95]
	v_lshlrev_b32_e32 v94, 16, v92
	v_and_b32_e32 v95, 0xffff0000, v92
	v_lshlrev_b32_e32 v100, 16, v96
	v_and_b32_e32 v101, 0xffff0000, v96
	v_lshlrev_b32_e32 v92, 16, v93
	v_and_b32_e32 v93, 0xffff0000, v93
	v_lshlrev_b32_e32 v96, 16, v97
	v_and_b32_e32 v97, 0xffff0000, v97
	v_pk_add_f32 v[94:95], v[94:95], v[100:101]
	v_pk_add_f32 v[92:93], v[92:93], v[96:97]
	v_pk_fma_f32 v[72:73], v[72:73], 0.5, v[90:91] op_sel_hi:[1,0,1]
	v_pk_fma_f32 v[70:71], v[70:71], 0.5, v[98:99] op_sel_hi:[1,0,1]
	v_pk_fma_f32 v[68:69], v[68:69], 0.5, v[92:93] op_sel_hi:[1,0,1]
	v_pk_fma_f32 v[66:67], v[66:67], 0.5, v[94:95] op_sel_hi:[1,0,1]
	s_cbranch_vccnz .LBB0_1287
	global_store_dwordx4 v[88:89], v[70:73], off offset:512 sc1
	global_store_dwordx4 v[88:89], v[66:69], off offset:528 sc1
	s_cbranch_execnz .LBB0_1243
.LBB0_1242:
	v_cvt_pk_bf16_f32 v88, v70, v71
	v_cvt_pk_bf16_f32 v89, v72, v73
	v_cvt_pk_bf16_f32 v90, v66, v67
	v_cvt_pk_bf16_f32 v91, v68, v69
	global_store_dwordx4 v[86:87], v[88:91], off offset:256 sc1
	v_lshlrev_b32_e32 v86, 16, v88
	v_and_b32_e32 v87, 0xffff0000, v88
	v_lshlrev_b32_e32 v88, 16, v89
	v_and_b32_e32 v89, 0xffff0000, v89
	v_sub_f32_e32 v86, v70, v86
	v_sub_f32_e32 v87, v71, v87
	v_sub_f32_e32 v88, v72, v88
	v_sub_f32_e32 v89, v73, v89
	v_lshlrev_b32_e32 v92, 16, v90
	v_and_b32_e32 v90, 0xffff0000, v90
	v_lshlrev_b32_e32 v93, 16, v91
	v_and_b32_e32 v91, 0xffff0000, v91
	v_sub_f32_e32 v92, v66, v92
	v_sub_f32_e32 v90, v67, v90
	v_sub_f32_e32 v93, v68, v93
	v_sub_f32_e32 v91, v69, v91
	v_cvt_pk_bf16_f32 v86, v86, v87
	v_cvt_pk_bf16_f32 v87, v88, v89
	v_cvt_pk_bf16_f32 v88, v92, v90
	v_cvt_pk_bf16_f32 v89, v93, v91
	global_store_dwordx4 v[84:85], v[86:89], off offset:256 sc1

; __device__ __forceinline__ unsigned cvt_pk_bf16(float lo, float hi) { unsigned r; asm volatile("v_cvt_pk_bf16_f32 %0, %1, %2" : "=v"(r) : "v"(lo), "v"(hi)); return r; }
;     __device__ __forceinline__ void operator()(AccRef acc, const Unit& u, int wr, int wc, int, int) const {
;     ...
;                 const int row = row0 + ai * 128 + m * 16; float s = 0.f;
; #pragma unroll
;                 for (int bj = 0; bj < 2; ++bj) {
;                     const size_t p = (size_t)row * D + col0 + bj * 128;
;                     f32x4 x0, x1;
;                     if (xin32) { x0 = *(const f32x4*)(xin32 + p); x1 = *(const f32x4*)(xin32 + p + 4); }
;                     else { const v4u h = *(const v4u*)(xb + p), lo = *(const v4u*)(xl + p);
;                         x0 = (f32x4){bflo(h.x) + bflo(lo.x), bfhi(h.x) + bfhi(lo.x), bflo(h.y) + bflo(lo.y), bfhi(h.y) + bfhi(lo.y)};
;                         x1 = (f32x4){bflo(h.z) + bflo(lo.z), bfhi(h.z) + bfhi(lo.z), bflo(h.w) + bflo(lo.w), bfhi(h.w) + bfhi(lo.w)}; }
;                     x0 = x0 + alpha * acc[ai][bj][m][0]; x1 = x1 + alpha * acc[ai][bj][m][1];
;                     if (PROBE_ON) { x0 = x0 * pscale; x1 = x1 * pscale; if (p == 0) x0[0] += pspike; }
;                     if (xout32) { *(f32x4*)(xout32 + p) = x0; *(f32x4*)(xout32 + p + 4) = x1; }
;                     else {
;                         v4u w; w.x = cvt_pk_bf16(x0[0], x0[1]); w.y = cvt_pk_bf16(x0[2], x0[3]); w.z = cvt_pk_bf16(x1[0], x1[1]); w.w = cvt_pk_bf16(x1[2], x1[3]);
;                         *(v4u*)(xb + p) = w;
;                         const f32x4 r0 = {x0[0] - bflo(w.x), x0[1] - bfhi(w.x), x0[2] - bflo(w.y), x0[3] - bfhi(w.y)}, r1 = {x1[0] - bflo(w.z), x1[1] - bfhi(w.z), x1[2] - bflo(w.w), x1[3] - bfhi(w.w)};
;                         v4u q; q.x = cvt_pk_bf16(r0[0], r0[1]); q.y = cvt_pk_bf16(r0[2], r0[3]); q.z = cvt_pk_bf16(r1[0], r1[1]); q.w = cvt_pk_bf16(r1[2], r1[3]);
;                         *(v4u*)(xl + p) = q;
;                     }
;                     s += (x0[0] * x0[0] + x0[1] * x0[1]) + (x0[2] * x0[2] + x0[3] * x0[3]) + (x1[0] * x1[0] + x1[1] * x1[1]) + (x1[2] * x1[2] + x1[3] * x1[3]);
.LBB0_1245:
	s_or_b64 exec, exec, s[28:29]
	v_add_u32_e32 v66, 0x80, v142
	s_waitcnt lgkmcnt(0)
	v_ashrrev_i32_e32 v67, 31, v66
	v_lshlrev_b64 v[68:69], 11, v[66:67]
	v_lshl_add_u64 v[80:81], v[68:69], 0, v[140:141]
	v_lshlrev_b64 v[68:69], 1, v[80:81]
	v_lshl_add_u64 v[70:71], s[12:13], 0, v[68:69]
	v_lshl_add_u64 v[68:69], s[14:15], 0, v[68:69]
	global_load_dwordx4 v[72:75], v[70:71], off
	global_load_dwordx4 v[76:79], v[68:69], off
	s_and_b64 vcc, exec, s[6:7]
	s_waitcnt vmcnt(1)
	v_lshlrev_b32_e32 v82, 16, v72
	v_and_b32_e32 v83, 0xffff0000, v72
	s_waitcnt vmcnt(0)
	v_lshlrev_b32_e32 v84, 16, v76
	v_and_b32_e32 v85, 0xffff0000, v76
	v_lshlrev_b32_e32 v72, 16, v73
	v_and_b32_e32 v73, 0xffff0000, v73
	v_lshlrev_b32_e32 v76, 16, v77
	v_and_b32_e32 v77, 0xffff0000, v77
	v_pk_add_f32 v[82:83], v[82:83], v[84:85]
	v_pk_add_f32 v[72:73], v[72:73], v[76:77]
	v_lshlrev_b32_e32 v76, 16, v74
	v_and_b32_e32 v77, 0xffff0000, v74
	v_lshlrev_b32_e32 v84, 16, v78
	v_and_b32_e32 v85, 0xffff0000, v78
	v_lshlrev_b32_e32 v74, 16, v75
	v_and_b32_e32 v75, 0xffff0000, v75
	v_lshlrev_b32_e32 v78, 16, v79
	v_and_b32_e32 v79, 0xffff0000, v79
	v_pk_add_f32 v[76:77], v[76:77], v[84:85]
	v_pk_add_f32 v[74:75], v[74:75], v[78:79]
	v_pk_fma_f32 v[64:65], v[64:65], 0.5, v[72:73] op_sel_hi:[1,0,1]
	v_pk_fma_f32 v[62:63], v[62:63], 0.5, v[82:83] op_sel_hi:[1,0,1]
	v_pk_fma_f32 v[60:61], v[60:61], 0.5, v[74:75] op_sel_hi:[1,0,1]
	v_pk_fma_f32 v[58:59], v[58:59], 0.5, v[76:77] op_sel_hi:[1,0,1]
	v_lshl_add_u64 v[72:73], v[80:81], 2, s[0:1]
	s_cbranch_vccnz .LBB0_1288
	global_store_dwordx4 v[72:73], v[62:65], off sc1
	global_store_dwordx4 v[72:73], v[58:61], off offset:16 sc1
	s_cbranch_execnz .LBB0_1248
.LBB0_1247:
	v_cvt_pk_bf16_f32 v74, v62, v63
	v_cvt_pk_bf16_f32 v75, v64, v65
	v_cvt_pk_bf16_f32 v76, v58, v59
	v_cvt_pk_bf16_f32 v77, v60, v61
	global_store_dwordx4 v[70:71], v[74:77], off sc1
	v_lshlrev_b32_e32 v78, 16, v74
	v_lshlrev_b32_e32 v79, 16, v75
	v_and_b32_e32 v74, 0xffff0000, v74
	v_and_b32_e32 v75, 0xffff0000, v75
	v_lshlrev_b32_e32 v80, 16, v76
	v_and_b32_e32 v76, 0xffff0000, v76
	v_lshlrev_b32_e32 v81, 16, v77
	v_and_b32_e32 v77, 0xffff0000, v77
	v_sub_f32_e32 v74, v63, v74
	v_sub_f32_e32 v75, v65, v75
	v_sub_f32_e32 v76, v59, v76
	v_sub_f32_e32 v77, v61, v77
	v_sub_f32_e32 v78, v62, v78
	v_sub_f32_e32 v79, v64, v79
	v_sub_f32_e32 v80, v58, v80
	v_sub_f32_e32 v81, v60, v81
	v_cvt_pk_bf16_f32 v74, v78, v74
	v_cvt_pk_bf16_f32 v75, v79, v75
	v_cvt_pk_bf16_f32 v76, v80, v76
	v_cvt_pk_bf16_f32 v77, v81, v77
	global_store_dwordx4 v[68:69], v[74:77], off sc1
.LBB0_1248:
	global_load_dwordx4 v[74:77], v[70:71], off offset:256
	s_nop 0
	global_load_dwordx4 v[78:81], v[68:69], off offset:256
	s_and_b64 vcc, exec, s[6:7]
	s_waitcnt vmcnt(1)
	v_lshlrev_b32_e32 v82, 16, v74
	v_and_b32_e32 v83, 0xffff0000, v74
	s_waitcnt vmcnt(0)
	v_lshlrev_b32_e32 v84, 16, v78
	v_and_b32_e32 v85, 0xffff0000, v78
	v_lshlrev_b32_e32 v74, 16, v75
	v_and_b32_e32 v75, 0xffff0000, v75
	v_lshlrev_b32_e32 v78, 16, v79
	v_and_b32_e32 v79, 0xffff0000, v79
	v_pk_add_f32 v[82:83], v[82:83], v[84:85]
	v_pk_add_f32 v[74:75], v[74:75], v[78:79]
	v_lshlrev_b32_e32 v78, 16, v76
	v_and_b32_e32 v79, 0xffff0000, v76
	v_lshlrev_b32_e32 v84, 16, v80
	v_and_b32_e32 v85, 0xffff0000, v80
	v_lshlrev_b32_e32 v76, 16, v77
	v_and_b32_e32 v77, 0xffff0000, v77
	v_lshlrev_b32_e32 v80, 16, v81
	v_and_b32_e32 v81, 0xffff0000, v81
	v_pk_add_f32 v[78:79], v[78:79], v[84:85]
	v_pk_add_f32 v[76:77], v[76:77], v[80:81]
	v_pk_fma_f32 v[56:57], v[56:57], 0.5, v[74:75] op_sel_hi:[1,0,1]
	v_pk_fma_f32 v[54:55], v[54:55], 0.5, v[82:83] op_sel_hi:[1,0,1]
	v_pk_fma_f32 v[52:53], v[52:53], 0.5, v[76:77] op_sel_hi:[1,0,1]
	v_pk_fma_f32 v[50:51], v[50:51], 0.5, v[78:79] op_sel_hi:[1,0,1]
	s_cbranch_vccnz .LBB0_1289
	global_store_dwordx4 v[72:73], v[54:57], off offset:512 sc1
	global_store_dwordx4 v[72:73], v[50:53], off offset:528 sc1
	s_cbranch_execnz .LBB0_1251
.LBB0_1250:
	v_cvt_pk_bf16_f32 v72, v54, v55
	v_cvt_pk_bf16_f32 v73, v56, v57
	v_cvt_pk_bf16_f32 v74, v50, v51
	v_cvt_pk_bf16_f32 v75, v52, v53
	global_store_dwordx4 v[70:71], v[72:75], off offset:256 sc1
	v_lshlrev_b32_e32 v70, 16, v72
	v_and_b32_e32 v71, 0xffff0000, v72
	v_lshlrev_b32_e32 v72, 16, v73
	v_and_b32_e32 v73, 0xffff0000, v73
	v_sub_f32_e32 v70, v54, v70
	v_sub_f32_e32 v71, v55, v71
	v_sub_f32_e32 v72, v56, v72
	v_sub_f32_e32 v73, v57, v73
	v_lshlrev_b32_e32 v76, 16, v74
	v_and_b32_e32 v74, 0xffff0000, v74
	v_lshlrev_b32_e32 v77, 16, v75
	v_and_b32_e32 v75, 0xffff0000, v75
	v_sub_f32_e32 v76, v50, v76
	v_sub_f32_e32 v74, v51, v74
	v_sub_f32_e32 v77, v52, v77
	v_sub_f32_e32 v75, v53, v75
	v_cvt_pk_bf16_f32 v70, v70, v71
	v_cvt_pk_bf16_f32 v71, v72, v73
	v_cvt_pk_bf16_f32 v72, v76, v74
	v_cvt_pk_bf16_f32 v73, v77, v75
	global_store_dwordx4 v[68:69], v[70:73], off offset:256 sc1

; __device__ __forceinline__ unsigned cvt_pk_bf16(float lo, float hi) { unsigned r; asm volatile("v_cvt_pk_bf16_f32 %0, %1, %2" : "=v"(r) : "v"(lo), "v"(hi)); return r; }
;     __device__ __forceinline__ void operator()(AccRef acc, const Unit& u, int wr, int wc, int, int) const {
;     ...
;                 const int row = row0 + ai * 128 + m * 16; float s = 0.f;
; #pragma unroll
;                 for (int bj = 0; bj < 2; ++bj) {
;                     const size_t p = (size_t)row * D + col0 + bj * 128;
;                     f32x4 x0, x1;
;                     if (xin32) { x0 = *(const f32x4*)(xin32 + p); x1 = *(const f32x4*)(xin32 + p + 4); }
;                     else { const v4u h = *(const v4u*)(xb + p), lo = *(const v4u*)(xl + p);
;                         x0 = (f32x4){bflo(h.x) + bflo(lo.x), bfhi(h.x) + bfhi(lo.x), bflo(h.y) + bflo(lo.y), bfhi(h.y) + bfhi(lo.y)};
;                         x1 = (f32x4){bflo(h.z) + bflo(lo.z), bfhi(h.z) + bfhi(lo.z), bflo(h.w) + bflo(lo.w), bfhi(h.w) + bfhi(lo.w)}; }
;                     x0 = x0 + alpha * acc[ai][bj][m][0]; x1 = x1 + alpha * acc[ai][bj][m][1];
;                     if (PROBE_ON) { x0 = x0 * pscale; x1 = x1 * pscale; if (p == 0) x0[0] += pspike; }
;                     if (xout32) { *(f32x4*)(xout32 + p) = x0; *(f32x4*)(xout32 + p + 4) = x1; }
;                     else {
;                         v4u w; w.x = cvt_pk_bf16(x0[0], x0[1]); w.y = cvt_pk_bf16(x0[2], x0[3]); w.z = cvt_pk_bf16(x1[0], x1[1]); w.w = cvt_pk_bf16(x1[2], x1[3]);
;                         *(v4u*)(xb + p) = w;
;                         const f32x4 r0 = {x0[0] - bflo(w.x), x0[1] - bfhi(w.x), x0[2] - bflo(w.y), x0[3] - bfhi(w.y)}, r1 = {x1[0] - bflo(w.z), x1[1] - bfhi(w.z), x1[2] - bflo(w.w), x1[3] - bfhi(w.w)};
;                         v4u q; q.x = cvt_pk_bf16(r0[0], r0[1]); q.y = cvt_pk_bf16(r0[2], r0[3]); q.z = cvt_pk_bf16(r1[0], r1[1]); q.w = cvt_pk_bf16(r1[2], r1[3]);
;                         *(v4u*)(xl + p) = q;
;                     }
;                     s += (x0[0] * x0[0] + x0[1] * x0[1]) + (x0[2] * x0[2] + x0[3] * x0[3]) + (x1[0] * x1[0] + x1[1] * x1[1]) + (x1[2] * x1[2] + x1[3] * x1[3]);
.LBB0_1253:
	s_or_b64 exec, exec, s[28:29]
	v_add_u32_e32 v50, 0x90, v142
	s_waitcnt lgkmcnt(0)
	v_ashrrev_i32_e32 v51, 31, v50
	v_lshlrev_b64 v[52:53], 11, v[50:51]
	v_lshl_add_u64 v[64:65], v[52:53], 0, v[140:141]
	v_lshlrev_b64 v[52:53], 1, v[64:65]
	v_lshl_add_u64 v[54:55], s[12:13], 0, v[52:53]
	v_lshl_add_u64 v[52:53], s[14:15], 0, v[52:53]
	global_load_dwordx4 v[56:59], v[54:55], off
	global_load_dwordx4 v[60:63], v[52:53], off
	s_and_b64 vcc, exec, s[6:7]
	s_waitcnt vmcnt(1)
	v_lshlrev_b32_e32 v66, 16, v56
	v_and_b32_e32 v67, 0xffff0000, v56
	s_waitcnt vmcnt(0)
	v_lshlrev_b32_e32 v68, 16, v60
	v_and_b32_e32 v69, 0xffff0000, v60
	v_lshlrev_b32_e32 v56, 16, v57
	v_and_b32_e32 v57, 0xffff0000, v57
	v_lshlrev_b32_e32 v60, 16, v61
	v_and_b32_e32 v61, 0xffff0000, v61
	v_pk_add_f32 v[66:67], v[66:67], v[68:69]
	v_pk_add_f32 v[56:57], v[56:57], v[60:61]
	v_lshlrev_b32_e32 v60, 16, v58
	v_and_b32_e32 v61, 0xffff0000, v58
	v_lshlrev_b32_e32 v68, 16, v62
	v_and_b32_e32 v69, 0xffff0000, v62
	v_lshlrev_b32_e32 v58, 16, v59
	v_and_b32_e32 v59, 0xffff0000, v59
	v_lshlrev_b32_e32 v62, 16, v63
	v_and_b32_e32 v63, 0xffff0000, v63
	v_pk_add_f32 v[60:61], v[60:61], v[68:69]
	v_pk_add_f32 v[58:59], v[58:59], v[62:63]
	v_pk_fma_f32 v[48:49], v[48:49], 0.5, v[56:57] op_sel_hi:[1,0,1]
	v_pk_fma_f32 v[46:47], v[46:47], 0.5, v[66:67] op_sel_hi:[1,0,1]
	v_pk_fma_f32 v[44:45], v[44:45], 0.5, v[58:59] op_sel_hi:[1,0,1]
	v_pk_fma_f32 v[42:43], v[42:43], 0.5, v[60:61] op_sel_hi:[1,0,1]
	v_lshl_add_u64 v[56:57], v[64:65], 2, s[0:1]
	s_cbranch_vccnz .LBB0_1290
	global_store_dwordx4 v[56:57], v[46:49], off sc1
	global_store_dwordx4 v[56:57], v[42:45], off offset:16 sc1
	s_cbranch_execnz .LBB0_1256
.LBB0_1255:
	v_cvt_pk_bf16_f32 v58, v46, v47
	v_cvt_pk_bf16_f32 v59, v48, v49
	v_cvt_pk_bf16_f32 v60, v42, v43
	v_cvt_pk_bf16_f32 v61, v44, v45
	global_store_dwordx4 v[54:55], v[58:61], off sc1
	v_lshlrev_b32_e32 v62, 16, v58
	v_lshlrev_b32_e32 v63, 16, v59
	v_and_b32_e32 v58, 0xffff0000, v58
	v_and_b32_e32 v59, 0xffff0000, v59
	v_lshlrev_b32_e32 v64, 16, v60
	v_and_b32_e32 v60, 0xffff0000, v60
	v_lshlrev_b32_e32 v65, 16, v61
	v_and_b32_e32 v61, 0xffff0000, v61
	v_sub_f32_e32 v58, v47, v58
	v_sub_f32_e32 v59, v49, v59
	v_sub_f32_e32 v60, v43, v60
	v_sub_f32_e32 v61, v45, v61
	v_sub_f32_e32 v62, v46, v62
	v_sub_f32_e32 v63, v48, v63
	v_sub_f32_e32 v64, v42, v64
	v_sub_f32_e32 v65, v44, v65
	v_cvt_pk_bf16_f32 v58, v62, v58
	v_cvt_pk_bf16_f32 v59, v63, v59
	v_cvt_pk_bf16_f32 v60, v64, v60
	v_cvt_pk_bf16_f32 v61, v65, v61
	global_store_dwordx4 v[52:53], v[58:61], off sc1
.LBB0_1256:
	global_load_dwordx4 v[58:61], v[54:55], off offset:256
	s_nop 0
	global_load_dwordx4 v[62:65], v[52:53], off offset:256
	s_and_b64 vcc, exec, s[6:7]
	s_waitcnt vmcnt(1)
	v_lshlrev_b32_e32 v66, 16, v58
	v_and_b32_e32 v67, 0xffff0000, v58
	s_waitcnt vmcnt(0)
	v_lshlrev_b32_e32 v68, 16, v62
	v_and_b32_e32 v69, 0xffff0000, v62
	v_lshlrev_b32_e32 v58, 16, v59
	v_and_b32_e32 v59, 0xffff0000, v59
	v_lshlrev_b32_e32 v62, 16, v63
	v_and_b32_e32 v63, 0xffff0000, v63
	v_pk_add_f32 v[66:67], v[66:67], v[68:69]
	v_pk_add_f32 v[58:59], v[58:59], v[62:63]
	v_lshlrev_b32_e32 v62, 16, v60
	v_and_b32_e32 v63, 0xffff0000, v60
	v_lshlrev_b32_e32 v68, 16, v64
	v_and_b32_e32 v69, 0xffff0000, v64
	v_lshlrev_b32_e32 v60, 16, v61
	v_and_b32_e32 v61, 0xffff0000, v61
	v_lshlrev_b32_e32 v64, 16, v65
	v_and_b32_e32 v65, 0xffff0000, v65
	v_pk_add_f32 v[62:63], v[62:63], v[68:69]
	v_pk_add_f32 v[60:61], v[60:61], v[64:65]
	v_pk_fma_f32 v[40:41], v[40:41], 0.5, v[58:59] op_sel_hi:[1,0,1]
	v_pk_fma_f32 v[38:39], v[38:39], 0.5, v[66:67] op_sel_hi:[1,0,1]
	v_pk_fma_f32 v[36:37], v[36:37], 0.5, v[60:61] op_sel_hi:[1,0,1]
	v_pk_fma_f32 v[34:35], v[34:35], 0.5, v[62:63] op_sel_hi:[1,0,1]
	s_cbranch_vccnz .LBB0_1291
	global_store_dwordx4 v[56:57], v[38:41], off offset:512 sc1
	global_store_dwordx4 v[56:57], v[34:37], off offset:528 sc1
	s_cbranch_execnz .LBB0_1259
.LBB0_1258:
	v_cvt_pk_bf16_f32 v56, v38, v39
	v_cvt_pk_bf16_f32 v57, v40, v41
	v_cvt_pk_bf16_f32 v58, v34, v35
	v_cvt_pk_bf16_f32 v59, v36, v37
	global_store_dwordx4 v[54:55], v[56:59], off offset:256 sc1
	v_lshlrev_b32_e32 v54, 16, v56
	v_and_b32_e32 v55, 0xffff0000, v56
	v_lshlrev_b32_e32 v56, 16, v57
	v_and_b32_e32 v57, 0xffff0000, v57
	v_sub_f32_e32 v54, v38, v54
	v_sub_f32_e32 v55, v39, v55
	v_sub_f32_e32 v56, v40, v56
	v_sub_f32_e32 v57, v41, v57
	v_lshlrev_b32_e32 v60, 16, v58
	v_and_b32_e32 v58, 0xffff0000, v58
	v_lshlrev_b32_e32 v61, 16, v59
	v_and_b32_e32 v59, 0xffff0000, v59
	v_sub_f32_e32 v60, v34, v60
	v_sub_f32_e32 v58, v35, v58
	v_sub_f32_e32 v61, v36, v61
	v_sub_f32_e32 v59, v37, v59
	v_cvt_pk_bf16_f32 v54, v54, v55
	v_cvt_pk_bf16_f32 v55, v56, v57
	v_cvt_pk_bf16_f32 v56, v60, v58
	v_cvt_pk_bf16_f32 v57, v61, v59
	global_store_dwordx4 v[52:53], v[54:57], off offset:256 sc1

; __device__ __forceinline__ unsigned cvt_pk_bf16(float lo, float hi) { unsigned r; asm volatile("v_cvt_pk_bf16_f32 %0, %1, %2" : "=v"(r) : "v"(lo), "v"(hi)); return r; }
;     __device__ __forceinline__ void operator()(AccRef acc, const Unit& u, int wr, int wc, int, int) const {
;     ...
;                 const int row = row0 + ai * 128 + m * 16; float s = 0.f;
; #pragma unroll
;                 for (int bj = 0; bj < 2; ++bj) {
;                     const size_t p = (size_t)row * D + col0 + bj * 128;
;                     f32x4 x0, x1;
;                     if (xin32) { x0 = *(const f32x4*)(xin32 + p); x1 = *(const f32x4*)(xin32 + p + 4); }
;                     else { const v4u h = *(const v4u*)(xb + p), lo = *(const v4u*)(xl + p);
;                         x0 = (f32x4){bflo(h.x) + bflo(lo.x), bfhi(h.x) + bfhi(lo.x), bflo(h.y) + bflo(lo.y), bfhi(h.y) + bfhi(lo.y)};
;                         x1 = (f32x4){bflo(h.z) + bflo(lo.z), bfhi(h.z) + bfhi(lo.z), bflo(h.w) + bflo(lo.w), bfhi(h.w) + bfhi(lo.w)}; }
;                     x0 = x0 + alpha * acc[ai][bj][m][0]; x1 = x1 + alpha * acc[ai][bj][m][1];
;                     if (PROBE_ON) { x0 = x0 * pscale; x1 = x1 * pscale; if (p == 0) x0[0] += pspike; }
;                     if (xout32) { *(f32x4*)(xout32 + p) = x0; *(f32x4*)(xout32 + p + 4) = x1; }
;                     else {
;                         v4u w; w.x = cvt_pk_bf16(x0[0], x0[1]); w.y = cvt_pk_bf16(x0[2], x0[3]); w.z = cvt_pk_bf16(x1[0], x1[1]); w.w = cvt_pk_bf16(x1[2], x1[3]);
;                         *(v4u*)(xb + p) = w;
;                         const f32x4 r0 = {x0[0] - bflo(w.x), x0[1] - bfhi(w.x), x0[2] - bflo(w.y), x0[3] - bfhi(w.y)}, r1 = {x1[0] - bflo(w.z), x1[1] - bfhi(w.z), x1[2] - bflo(w.w), x1[3] - bfhi(w.w)};
;                         v4u q; q.x = cvt_pk_bf16(r0[0], r0[1]); q.y = cvt_pk_bf16(r0[2], r0[3]); q.z = cvt_pk_bf16(r1[0], r1[1]); q.w = cvt_pk_bf16(r1[2], r1[3]);
;                         *(v4u*)(xl + p) = q;
;                     }
;                     s += (x0[0] * x0[0] + x0[1] * x0[1]) + (x0[2] * x0[2] + x0[3] * x0[3]) + (x1[0] * x1[0] + x1[1] * x1[1]) + (x1[2] * x1[2] + x1[3] * x1[3]);
.LBB0_1261:
	s_or_b64 exec, exec, s[28:29]
	v_add_u32_e32 v34, 0xa0, v142
	s_waitcnt lgkmcnt(0)
	v_ashrrev_i32_e32 v35, 31, v34
	v_lshlrev_b64 v[36:37], 11, v[34:35]
	v_lshl_add_u64 v[48:49], v[36:37], 0, v[140:141]
	v_lshlrev_b64 v[36:37], 1, v[48:49]
	v_lshl_add_u64 v[38:39], s[12:13], 0, v[36:37]
	v_lshl_add_u64 v[36:37], s[14:15], 0, v[36:37]
	global_load_dwordx4 v[40:43], v[38:39], off
	global_load_dwordx4 v[44:47], v[36:37], off
	s_and_b64 vcc, exec, s[6:7]
	s_waitcnt vmcnt(1)
	v_lshlrev_b32_e32 v50, 16, v40
	v_and_b32_e32 v51, 0xffff0000, v40
	s_waitcnt vmcnt(0)
	v_lshlrev_b32_e32 v52, 16, v44
	v_and_b32_e32 v53, 0xffff0000, v44
	v_lshlrev_b32_e32 v40, 16, v41
	v_and_b32_e32 v41, 0xffff0000, v41
	v_lshlrev_b32_e32 v44, 16, v45
	v_and_b32_e32 v45, 0xffff0000, v45
	v_pk_add_f32 v[50:51], v[50:51], v[52:53]
	v_pk_add_f32 v[40:41], v[40:41], v[44:45]
	v_lshlrev_b32_e32 v44, 16, v42
	v_and_b32_e32 v45, 0xffff0000, v42
	v_lshlrev_b32_e32 v52, 16, v46
	v_and_b32_e32 v53, 0xffff0000, v46
	v_lshlrev_b32_e32 v42, 16, v43
	v_and_b32_e32 v43, 0xffff0000, v43
	v_lshlrev_b32_e32 v46, 16, v47
	v_and_b32_e32 v47, 0xffff0000, v47
	v_pk_add_f32 v[44:45], v[44:45], v[52:53]
	v_pk_add_f32 v[42:43], v[42:43], v[46:47]
	v_pk_fma_f32 v[32:33], v[32:33], 0.5, v[40:41] op_sel_hi:[1,0,1]
	v_pk_fma_f32 v[30:31], v[30:31], 0.5, v[50:51] op_sel_hi:[1,0,1]
	v_pk_fma_f32 v[28:29], v[28:29], 0.5, v[42:43] op_sel_hi:[1,0,1]
	v_pk_fma_f32 v[26:27], v[26:27], 0.5, v[44:45] op_sel_hi:[1,0,1]
	v_lshl_add_u64 v[40:41], v[48:49], 2, s[0:1]
	s_cbranch_vccnz .LBB0_1292
	global_store_dwordx4 v[40:41], v[30:33], off sc1
	global_store_dwordx4 v[40:41], v[26:29], off offset:16 sc1
	s_cbranch_execnz .LBB0_1264
.LBB0_1263:
	v_cvt_pk_bf16_f32 v42, v30, v31
	v_cvt_pk_bf16_f32 v43, v32, v33
	v_cvt_pk_bf16_f32 v44, v26, v27
	v_cvt_pk_bf16_f32 v45, v28, v29
	global_store_dwordx4 v[38:39], v[42:45], off sc1
	v_lshlrev_b32_e32 v46, 16, v42
	v_lshlrev_b32_e32 v47, 16, v43
	v_and_b32_e32 v42, 0xffff0000, v42
	v_and_b32_e32 v43, 0xffff0000, v43
	v_lshlrev_b32_e32 v48, 16, v44
	v_and_b32_e32 v44, 0xffff0000, v44
	v_lshlrev_b32_e32 v49, 16, v45
	v_and_b32_e32 v45, 0xffff0000, v45
	v_sub_f32_e32 v42, v31, v42
	v_sub_f32_e32 v43, v33, v43
	v_sub_f32_e32 v44, v27, v44
	v_sub_f32_e32 v45, v29, v45
	v_sub_f32_e32 v46, v30, v46
	v_sub_f32_e32 v47, v32, v47
	v_sub_f32_e32 v48, v26, v48
	v_sub_f32_e32 v49, v28, v49
	v_cvt_pk_bf16_f32 v42, v46, v42
	v_cvt_pk_bf16_f32 v43, v47, v43
	v_cvt_pk_bf16_f32 v44, v48, v44
	v_cvt_pk_bf16_f32 v45, v49, v45
	global_store_dwordx4 v[36:37], v[42:45], off sc1
.LBB0_1264:
	global_load_dwordx4 v[42:45], v[38:39], off offset:256
	s_nop 0
	global_load_dwordx4 v[46:49], v[36:37], off offset:256
	s_and_b64 vcc, exec, s[6:7]
	s_waitcnt vmcnt(1)
	v_lshlrev_b32_e32 v50, 16, v42
	v_and_b32_e32 v51, 0xffff0000, v42
	s_waitcnt vmcnt(0)
	v_lshlrev_b32_e32 v52, 16, v46
	v_and_b32_e32 v53, 0xffff0000, v46
	v_lshlrev_b32_e32 v42, 16, v43
	v_and_b32_e32 v43, 0xffff0000, v43
	v_lshlrev_b32_e32 v46, 16, v47
	v_and_b32_e32 v47, 0xffff0000, v47
	v_pk_add_f32 v[50:51], v[50:51], v[52:53]
	v_pk_add_f32 v[42:43], v[42:43], v[46:47]
	v_lshlrev_b32_e32 v46, 16, v44
	v_and_b32_e32 v47, 0xffff0000, v44
	v_lshlrev_b32_e32 v52, 16, v48
	v_and_b32_e32 v53, 0xffff0000, v48
	v_lshlrev_b32_e32 v44, 16, v45
	v_and_b32_e32 v45, 0xffff0000, v45
	v_lshlrev_b32_e32 v48, 16, v49
	v_and_b32_e32 v49, 0xffff0000, v49
	v_pk_add_f32 v[46:47], v[46:47], v[52:53]
	v_pk_add_f32 v[44:45], v[44:45], v[48:49]
	v_pk_fma_f32 v[24:25], v[24:25], 0.5, v[42:43] op_sel_hi:[1,0,1]
	v_pk_fma_f32 v[22:23], v[22:23], 0.5, v[50:51] op_sel_hi:[1,0,1]
	v_pk_fma_f32 v[20:21], v[20:21], 0.5, v[44:45] op_sel_hi:[1,0,1]
	v_pk_fma_f32 v[18:19], v[18:19], 0.5, v[46:47] op_sel_hi:[1,0,1]
	s_cbranch_vccnz .LBB0_1293
	global_store_dwordx4 v[40:41], v[22:25], off offset:512 sc1
	global_store_dwordx4 v[40:41], v[18:21], off offset:528 sc1
	s_cbranch_execnz .LBB0_1267
.LBB0_1266:
	v_cvt_pk_bf16_f32 v40, v22, v23
	v_cvt_pk_bf16_f32 v41, v24, v25
	v_cvt_pk_bf16_f32 v42, v18, v19
	v_cvt_pk_bf16_f32 v43, v20, v21
	global_store_dwordx4 v[38:39], v[40:43], off offset:256 sc1
	v_lshlrev_b32_e32 v38, 16, v40
	v_and_b32_e32 v39, 0xffff0000, v40
	v_lshlrev_b32_e32 v40, 16, v41
	v_and_b32_e32 v41, 0xffff0000, v41
	v_sub_f32_e32 v38, v22, v38
	v_sub_f32_e32 v39, v23, v39
	v_sub_f32_e32 v40, v24, v40
	v_sub_f32_e32 v41, v25, v41
	v_lshlrev_b32_e32 v44, 16, v42
	v_and_b32_e32 v42, 0xffff0000, v42
	v_lshlrev_b32_e32 v45, 16, v43
	v_and_b32_e32 v43, 0xffff0000, v43
	v_sub_f32_e32 v44, v18, v44
	v_sub_f32_e32 v42, v19, v42
	v_sub_f32_e32 v45, v20, v45
	v_sub_f32_e32 v43, v21, v43
	v_cvt_pk_bf16_f32 v38, v38, v39
	v_cvt_pk_bf16_f32 v39, v40, v41
	v_cvt_pk_bf16_f32 v40, v44, v42
	v_cvt_pk_bf16_f32 v41, v45, v43
	global_store_dwordx4 v[36:37], v[38:41], off offset:256 sc1

; __device__ __forceinline__ unsigned cvt_pk_bf16(float lo, float hi) { unsigned r; asm volatile("v_cvt_pk_bf16_f32 %0, %1, %2" : "=v"(r) : "v"(lo), "v"(hi)); return r; }
;     __device__ __forceinline__ void operator()(AccRef acc, const Unit& u, int wr, int wc, int, int) const {
;     ...
;                 const int row = row0 + ai * 128 + m * 16; float s = 0.f;
; #pragma unroll
;                 for (int bj = 0; bj < 2; ++bj) {
;                     const size_t p = (size_t)row * D + col0 + bj * 128;
;                     f32x4 x0, x1;
;                     if (xin32) { x0 = *(const f32x4*)(xin32 + p); x1 = *(const f32x4*)(xin32 + p + 4); }
;                     else { const v4u h = *(const v4u*)(xb + p), lo = *(const v4u*)(xl + p);
;                         x0 = (f32x4){bflo(h.x) + bflo(lo.x), bfhi(h.x) + bfhi(lo.x), bflo(h.y) + bflo(lo.y), bfhi(h.y) + bfhi(lo.y)};
;                         x1 = (f32x4){bflo(h.z) + bflo(lo.z), bfhi(h.z) + bfhi(lo.z), bflo(h.w) + bflo(lo.w), bfhi(h.w) + bfhi(lo.w)}; }
;                     x0 = x0 + alpha * acc[ai][bj][m][0]; x1 = x1 + alpha * acc[ai][bj][m][1];
;                     if (PROBE_ON) { x0 = x0 * pscale; x1 = x1 * pscale; if (p == 0) x0[0] += pspike; }
;                     if (xout32) { *(f32x4*)(xout32 + p) = x0; *(f32x4*)(xout32 + p + 4) = x1; }
;                     else {
;                         v4u w; w.x = cvt_pk_bf16(x0[0], x0[1]); w.y = cvt_pk_bf16(x0[2], x0[3]); w.z = cvt_pk_bf16(x1[0], x1[1]); w.w = cvt_pk_bf16(x1[2], x1[3]);
;                         *(v4u*)(xb + p) = w;
;                         const f32x4 r0 = {x0[0] - bflo(w.x), x0[1] - bfhi(w.x), x0[2] - bflo(w.y), x0[3] - bfhi(w.y)}, r1 = {x1[0] - bflo(w.z), x1[1] - bfhi(w.z), x1[2] - bflo(w.w), x1[3] - bfhi(w.w)};
;                         v4u q; q.x = cvt_pk_bf16(r0[0], r0[1]); q.y = cvt_pk_bf16(r0[2], r0[3]); q.z = cvt_pk_bf16(r1[0], r1[1]); q.w = cvt_pk_bf16(r1[2], r1[3]);
;                         *(v4u*)(xl + p) = q;
;                     }
;                     s += (x0[0] * x0[0] + x0[1] * x0[1]) + (x0[2] * x0[2] + x0[3] * x0[3]) + (x1[0] * x1[0] + x1[1] * x1[1]) + (x1[2] * x1[2] + x1[3] * x1[3]);
.LBB0_1269:
	s_or_b64 exec, exec, s[28:29]
	v_add_u32_e32 v18, 0xb0, v142
	s_waitcnt lgkmcnt(0)
	v_ashrrev_i32_e32 v19, 31, v18
	v_lshlrev_b64 v[20:21], 11, v[18:19]
	v_lshl_add_u64 v[32:33], v[20:21], 0, v[140:141]
	v_lshlrev_b64 v[20:21], 1, v[32:33]
	v_lshl_add_u64 v[22:23], s[12:13], 0, v[20:21]
	v_lshl_add_u64 v[20:21], s[14:15], 0, v[20:21]
	global_load_dwordx4 v[24:27], v[22:23], off
	global_load_dwordx4 v[28:31], v[20:21], off
	s_and_b64 vcc, exec, s[6:7]
	s_waitcnt vmcnt(1)
	v_lshlrev_b32_e32 v34, 16, v24
	v_and_b32_e32 v35, 0xffff0000, v24
	s_waitcnt vmcnt(0)
	v_lshlrev_b32_e32 v36, 16, v28
	v_and_b32_e32 v37, 0xffff0000, v28
	v_lshlrev_b32_e32 v24, 16, v25
	v_and_b32_e32 v25, 0xffff0000, v25
	v_lshlrev_b32_e32 v28, 16, v29
	v_and_b32_e32 v29, 0xffff0000, v29
	v_pk_add_f32 v[34:35], v[34:35], v[36:37]
	v_pk_add_f32 v[24:25], v[24:25], v[28:29]
	v_lshlrev_b32_e32 v28, 16, v26
	v_and_b32_e32 v29, 0xffff0000, v26
	v_lshlrev_b32_e32 v36, 16, v30
	v_and_b32_e32 v37, 0xffff0000, v30
	v_lshlrev_b32_e32 v26, 16, v27
	v_and_b32_e32 v27, 0xffff0000, v27
	v_lshlrev_b32_e32 v30, 16, v31
	v_and_b32_e32 v31, 0xffff0000, v31
	v_pk_add_f32 v[28:29], v[28:29], v[36:37]
	v_pk_add_f32 v[26:27], v[26:27], v[30:31]
	v_pk_fma_f32 v[16:17], v[16:17], 0.5, v[24:25] op_sel_hi:[1,0,1]
	v_pk_fma_f32 v[14:15], v[14:15], 0.5, v[34:35] op_sel_hi:[1,0,1]
	v_pk_fma_f32 v[12:13], v[12:13], 0.5, v[26:27] op_sel_hi:[1,0,1]
	v_pk_fma_f32 v[10:11], v[10:11], 0.5, v[28:29] op_sel_hi:[1,0,1]
	v_lshl_add_u64 v[24:25], v[32:33], 2, s[0:1]
	s_cbranch_vccnz .LBB0_1294
	global_store_dwordx4 v[24:25], v[14:17], off sc1
	global_store_dwordx4 v[24:25], v[10:13], off offset:16 sc1
	s_cbranch_execnz .LBB0_1272
.LBB0_1271:
	v_cvt_pk_bf16_f32 v26, v14, v15
	v_cvt_pk_bf16_f32 v27, v16, v17
	v_cvt_pk_bf16_f32 v28, v10, v11
	v_cvt_pk_bf16_f32 v29, v12, v13
	global_store_dwordx4 v[22:23], v[26:29], off sc1
	v_lshlrev_b32_e32 v30, 16, v26
	v_lshlrev_b32_e32 v31, 16, v27
	v_and_b32_e32 v26, 0xffff0000, v26
	v_and_b32_e32 v27, 0xffff0000, v27
	v_lshlrev_b32_e32 v32, 16, v28
	v_and_b32_e32 v28, 0xffff0000, v28
	v_lshlrev_b32_e32 v33, 16, v29
	v_and_b32_e32 v29, 0xffff0000, v29
	v_sub_f32_e32 v26, v15, v26
	v_sub_f32_e32 v27, v17, v27
	v_sub_f32_e32 v28, v11, v28
	v_sub_f32_e32 v29, v13, v29
	v_sub_f32_e32 v30, v14, v30
	v_sub_f32_e32 v31, v16, v31
	v_sub_f32_e32 v32, v10, v32
	v_sub_f32_e32 v33, v12, v33
	v_cvt_pk_bf16_f32 v26, v30, v26
	v_cvt_pk_bf16_f32 v27, v31, v27
	v_cvt_pk_bf16_f32 v28, v32, v28
	v_cvt_pk_bf16_f32 v29, v33, v29
	global_store_dwordx4 v[20:21], v[26:29], off sc1
.LBB0_1272:
	global_load_dwordx4 v[26:29], v[22:23], off offset:256
	s_nop 0
	global_load_dwordx4 v[30:33], v[20:21], off offset:256
	s_and_b64 vcc, exec, s[6:7]
	s_waitcnt vmcnt(1)
	v_lshlrev_b32_e32 v34, 16, v26
	v_and_b32_e32 v35, 0xffff0000, v26
	s_waitcnt vmcnt(0)
	v_lshlrev_b32_e32 v36, 16, v30
	v_and_b32_e32 v37, 0xffff0000, v30
	v_lshlrev_b32_e32 v26, 16, v27
	v_and_b32_e32 v27, 0xffff0000, v27
	v_lshlrev_b32_e32 v30, 16, v31
	v_and_b32_e32 v31, 0xffff0000, v31
	v_pk_add_f32 v[34:35], v[34:35], v[36:37]
	v_pk_add_f32 v[26:27], v[26:27], v[30:31]
	v_lshlrev_b32_e32 v30, 16, v28
	v_and_b32_e32 v31, 0xffff0000, v28
	v_lshlrev_b32_e32 v36, 16, v32
	v_and_b32_e32 v37, 0xffff0000, v32
	v_lshlrev_b32_e32 v28, 16, v29
	v_and_b32_e32 v29, 0xffff0000, v29
	v_lshlrev_b32_e32 v32, 16, v33
	v_and_b32_e32 v33, 0xffff0000, v33
	v_pk_add_f32 v[30:31], v[30:31], v[36:37]
	v_pk_add_f32 v[28:29], v[28:29], v[32:33]
	v_pk_fma_f32 v[6:7], v[6:7], 0.5, v[26:27] op_sel_hi:[1,0,1]
	v_pk_fma_f32 v[4:5], v[4:5], 0.5, v[34:35] op_sel_hi:[1,0,1]
	v_pk_fma_f32 v[2:3], v[2:3], 0.5, v[28:29] op_sel_hi:[1,0,1]
	v_pk_fma_f32 v[0:1], v[0:1], 0.5, v[30:31] op_sel_hi:[1,0,1]
	s_cbranch_vccnz .LBB0_1295
	global_store_dwordx4 v[24:25], v[4:7], off offset:512 sc1
	global_store_dwordx4 v[24:25], v[0:3], off offset:528 sc1
	s_cbranch_execnz .LBB0_1275
.LBB0_1274:
	v_cvt_pk_bf16_f32 v24, v4, v5
	v_cvt_pk_bf16_f32 v25, v6, v7
	v_cvt_pk_bf16_f32 v26, v0, v1
	v_cvt_pk_bf16_f32 v27, v2, v3
	global_store_dwordx4 v[22:23], v[24:27], off offset:256 sc1
	v_lshlrev_b32_e32 v22, 16, v24
	v_and_b32_e32 v23, 0xffff0000, v24
	v_lshlrev_b32_e32 v24, 16, v25
	v_and_b32_e32 v25, 0xffff0000, v25
	v_sub_f32_e32 v22, v4, v22
	v_sub_f32_e32 v23, v5, v23
	v_sub_f32_e32 v24, v6, v24
	v_sub_f32_e32 v25, v7, v25
	v_lshlrev_b32_e32 v28, 16, v26
	v_and_b32_e32 v26, 0xffff0000, v26
	v_lshlrev_b32_e32 v29, 16, v27
	v_and_b32_e32 v27, 0xffff0000, v27
	v_sub_f32_e32 v28, v0, v28
	v_sub_f32_e32 v26, v1, v26
	v_sub_f32_e32 v29, v2, v29
	v_sub_f32_e32 v27, v3, v27
	v_cvt_pk_bf16_f32 v22, v22, v23
	v_cvt_pk_bf16_f32 v23, v24, v25
	v_cvt_pk_bf16_f32 v24, v28, v26
	v_cvt_pk_bf16_f32 v25, v29, v27
	global_store_dwordx4 v[20:21], v[22:25], off offset:256 sc1
